# back-edge rotation (strategy 7.11): the K-loop pointer/counter updates and exit compare moved in front of the loop's last s_barrier in the P1/P5/P7/P8 loops and their peeled first iterations
# baseline (speedup 1.0000x reference)
.LBB0_188:
	s_ashr_i32 s21, s20, 31
	s_lshl_b64 s[22:23], s[20:21], 20
	s_add_u32 s22, s31, s22
	s_addc_u32 s23, s34, s23
	s_and_b64 s[24:25], s[2:3], exec
	s_cselect_b32 s5, s23, s29
	s_cselect_b32 s7, s22, s28
	s_ashr_i32 s19, s18, 31
	s_lshl_b64 s[24:25], s[18:19], 20
	s_add_u32 s24, s35, s24
	s_addc_u32 s25, s36, s25
	s_and_b64 s[26:27], s[2:3], exec
	s_cselect_b32 s19, s25, s9
	s_cselect_b32 s21, s24, s8
	s_add_u32 s59, s8, 0x100
	s_addc_u32 s60, s9, 0
	s_add_u32 s8, s28, 0x80080
	v_mov_b32_e32 v0, 0
	s_addc_u32 s9, s29, 0
	s_mov_b32 s61, -2
	s_cmp_eq_u32 s56, 1
	s_cbranch_scc1 .Lpeel_zero_P1
	v_add_u32_e32 v140, s37, v193
	v_add_u32_e32 v160, s40, v193
	ds_read_b128 v[128:131], v140
	ds_read_b128 v[132:135], v140 offset:1024
	ds_read_b128 v[136:139], v140 offset:2048
	ds_read_b128 v[140:143], v140 offset:3072
	ds_read_b128 v[144:147], v160
	ds_read_b128 v[148:151], v160 offset:1024
	ds_read_b128 v[176:179], v160 offset:2048
	ds_read_b128 v[180:183], v160 offset:3072
	s_add_u32 s26, s8, 0xfff80080
	s_addc_u32 s27, s9, -1
	s_cmp_eq_u32 s61, 28
	s_cselect_b32 s29, s5, s27
	s_cselect_b32 s28, s7, s26
	s_cselect_b32 s27, s19, s60
	s_cselect_b32 s26, s21, s59
	v_lshl_add_u64 v[162:163], s[8:9], 0, v[174:175]
	s_add_i32 m0, s43, 0xc000
	ds_read_b128 v[184:187], v199
	ds_read_b128 v[188:191], v199 offset:1024
	ds_read_b128 v[200:203], v199 offset:2048
	ds_read_b128 v[204:207], v199 offset:3072
	ds_read_b128 v[208:211], v199 offset:4096
	ds_read_b128 v[212:215], v199 offset:5120
	ds_read_b128 v[216:219], v199 offset:6144
	ds_read_b128 v[230:233], v199 offset:7168
	global_load_lds_dwordx4 v[162:163], off
	v_lshl_add_u64 v[162:163], s[8:9], 0, v[172:173]
	s_add_i32 m0, s43, 0xe000
	s_nop 0
	global_load_lds_dwordx4 v[162:163], off
	s_waitcnt vmcnt(16)
	s_waitcnt lgkmcnt(0)
	s_barrier
	s_setprio 1
	s_waitcnt lgkmcnt(0)
	v_mfma_f32_16x16x32_bf16 v[124:127], v[128:131], v[184:187], 0
	v_mfma_f32_16x16x32_bf16 v[120:123], v[136:139], v[184:187], 0
	v_mfma_f32_16x16x32_bf16 v[108:111], v[128:131], v[200:203], 0
	v_mfma_f32_16x16x32_bf16 v[104:107], v[136:139], v[200:203], 0
	v_mfma_f32_16x16x32_bf16 v[92:95], v[128:131], v[208:211], 0
	v_mfma_f32_16x16x32_bf16 v[88:91], v[136:139], v[208:211], 0
	v_mfma_f32_16x16x32_bf16 v[76:79], v[128:131], v[216:219], 0
	v_mfma_f32_16x16x32_bf16 v[72:75], v[136:139], v[216:219], 0
	v_mfma_f32_16x16x32_bf16 v[124:127], v[132:135], v[188:191], v[124:127]
	v_mfma_f32_16x16x32_bf16 v[120:123], v[140:143], v[188:191], v[120:123]
	v_mfma_f32_16x16x32_bf16 v[108:111], v[132:135], v[204:207], v[108:111]
	v_mfma_f32_16x16x32_bf16 v[104:107], v[140:143], v[204:207], v[104:107]
	v_mfma_f32_16x16x32_bf16 v[92:95], v[132:135], v[212:215], v[92:95]
	v_mfma_f32_16x16x32_bf16 v[88:91], v[140:143], v[212:215], v[88:91]
	v_mfma_f32_16x16x32_bf16 v[76:79], v[132:135], v[230:233], v[76:79]
	v_mfma_f32_16x16x32_bf16 v[72:75], v[140:143], v[230:233], v[72:75]
	s_setprio 0
	s_setprio 1
	v_mfma_f32_16x16x32_bf16 v[116:119], v[144:147], v[184:187], 0
	v_mfma_f32_16x16x32_bf16 v[112:115], v[176:179], v[184:187], 0
	v_mfma_f32_16x16x32_bf16 v[100:103], v[144:147], v[200:203], 0
	v_mfma_f32_16x16x32_bf16 v[96:99], v[176:179], v[200:203], 0
	v_mfma_f32_16x16x32_bf16 v[84:87], v[144:147], v[208:211], 0
	v_mfma_f32_16x16x32_bf16 v[80:83], v[176:179], v[208:211], 0
	v_mfma_f32_16x16x32_bf16 v[68:71], v[144:147], v[216:219], 0
	v_mfma_f32_16x16x32_bf16 v[64:67], v[176:179], v[216:219], 0
	v_mfma_f32_16x16x32_bf16 v[116:119], v[148:151], v[188:191], v[116:119]
	v_mfma_f32_16x16x32_bf16 v[112:115], v[180:183], v[188:191], v[112:115]
	v_mfma_f32_16x16x32_bf16 v[100:103], v[148:151], v[204:207], v[100:103]
	v_mfma_f32_16x16x32_bf16 v[96:99], v[180:183], v[204:207], v[96:99]
	v_mfma_f32_16x16x32_bf16 v[84:87], v[148:151], v[212:215], v[84:87]
	v_mfma_f32_16x16x32_bf16 v[80:83], v[180:183], v[212:215], v[80:83]
	v_mfma_f32_16x16x32_bf16 v[68:71], v[148:151], v[230:233], v[68:71]
	v_mfma_f32_16x16x32_bf16 v[64:67], v[180:183], v[230:233], v[64:67]
	s_setprio 0
	s_barrier
	s_mov_b32 m0, s38
	v_lshl_add_u64 v[162:163], s[26:27], 0, v[154:155]
	s_add_u32 s62, s26, 0x80000
	ds_read_b128 v[184:187], v199 offset:16384
	ds_read_b128 v[188:191], v199 offset:17408
	ds_read_b128 v[200:203], v199 offset:18432
	ds_read_b128 v[204:207], v199 offset:19456
	ds_read_b128 v[208:211], v199 offset:20480
	ds_read_b128 v[212:215], v199 offset:21504
	ds_read_b128 v[216:219], v199 offset:22528
	ds_read_b128 v[230:233], v199 offset:23552
	global_load_lds_dwordx4 v[162:163], off
	v_lshl_add_u64 v[166:167], s[26:27], 0, v[158:159]
	s_mov_b32 m0, s39
	s_addc_u32 s63, s27, 0
	global_load_lds_dwordx4 v[166:167], off
	v_lshl_add_u64 v[194:195], s[62:63], 0, v[154:155]
	s_mov_b32 m0, s41
	v_lshl_add_u64 v[196:197], s[28:29], 0, v[156:157]
	global_load_lds_dwordx4 v[194:195], off
	v_lshl_add_u64 v[194:195], s[62:63], 0, v[158:159]
	s_mov_b32 m0, s42
	s_nop 0
	global_load_lds_dwordx4 v[194:195], off
	v_lshl_add_u64 v[194:195], s[28:29], 0, v[152:153]
	s_mov_b32 m0, s43
	s_nop 0
	global_load_lds_dwordx4 v[194:195], off
	s_mov_b32 m0, s44
	s_nop 0
	global_load_lds_dwordx4 v[196:197], off
	s_waitcnt vmcnt(16)
	s_waitcnt lgkmcnt(0)
	s_barrier
	s_setprio 1
	s_waitcnt lgkmcnt(0)
	v_mfma_f32_16x16x32_bf16 v[60:63], v[128:131], v[184:187], 0
	v_mfma_f32_16x16x32_bf16 v[56:59], v[136:139], v[184:187], 0
	v_mfma_f32_16x16x32_bf16 v[44:47], v[128:131], v[200:203], 0
	v_mfma_f32_16x16x32_bf16 v[40:43], v[136:139], v[200:203], 0
	v_mfma_f32_16x16x32_bf16 v[28:31], v[128:131], v[208:211], 0
	v_mfma_f32_16x16x32_bf16 v[24:27], v[136:139], v[208:211], 0
	v_mfma_f32_16x16x32_bf16 v[12:15], v[128:131], v[216:219], 0
	v_mfma_f32_16x16x32_bf16 v[8:11], v[136:139], v[216:219], 0
	v_mfma_f32_16x16x32_bf16 v[60:63], v[132:135], v[188:191], v[60:63]
	v_mfma_f32_16x16x32_bf16 v[56:59], v[140:143], v[188:191], v[56:59]
	v_mfma_f32_16x16x32_bf16 v[44:47], v[132:135], v[204:207], v[44:47]
	v_mfma_f32_16x16x32_bf16 v[40:43], v[140:143], v[204:207], v[40:43]
	v_mfma_f32_16x16x32_bf16 v[28:31], v[132:135], v[212:215], v[28:31]
	v_mfma_f32_16x16x32_bf16 v[24:27], v[140:143], v[212:215], v[24:27]
	v_mfma_f32_16x16x32_bf16 v[12:15], v[132:135], v[230:233], v[12:15]
	v_mfma_f32_16x16x32_bf16 v[8:11], v[140:143], v[230:233], v[8:11]
	s_setprio 0
	s_setprio 1
	v_mfma_f32_16x16x32_bf16 v[52:55], v[144:147], v[184:187], 0
	v_mfma_f32_16x16x32_bf16 v[48:51], v[176:179], v[184:187], 0
	v_mfma_f32_16x16x32_bf16 v[36:39], v[144:147], v[200:203], 0
	v_mfma_f32_16x16x32_bf16 v[32:35], v[176:179], v[200:203], 0
	v_mfma_f32_16x16x32_bf16 v[20:23], v[144:147], v[208:211], 0
	v_mfma_f32_16x16x32_bf16 v[16:19], v[176:179], v[208:211], 0
	v_mfma_f32_16x16x32_bf16 v[4:7], v[144:147], v[216:219], 0
	v_mfma_f32_16x16x32_bf16 v[0:3], v[176:179], v[216:219], 0
	v_mfma_f32_16x16x32_bf16 v[52:55], v[148:151], v[188:191], v[52:55]
	v_mfma_f32_16x16x32_bf16 v[48:51], v[180:183], v[188:191], v[48:51]
	v_mfma_f32_16x16x32_bf16 v[36:39], v[148:151], v[204:207], v[36:39]
	v_mfma_f32_16x16x32_bf16 v[32:35], v[180:183], v[204:207], v[32:35]
	v_mfma_f32_16x16x32_bf16 v[20:23], v[148:151], v[212:215], v[20:23]
	v_mfma_f32_16x16x32_bf16 v[16:19], v[180:183], v[212:215], v[16:19]
	v_mfma_f32_16x16x32_bf16 v[4:7], v[148:151], v[230:233], v[4:7]
	v_mfma_f32_16x16x32_bf16 v[0:3], v[180:183], v[230:233], v[0:3]
	s_setprio 0
	s_barrier
	v_add_u32_e32 v140, s48, v193
	v_add_u32_e32 v160, s53, v193
	ds_read_b128 v[128:131], v140
	ds_read_b128 v[132:135], v140 offset:1024
	ds_read_b128 v[136:139], v140 offset:2048
	ds_read_b128 v[140:143], v140 offset:3072
	ds_read_b128 v[144:147], v160
	ds_read_b128 v[148:151], v160 offset:1024
	ds_read_b128 v[176:179], v160 offset:2048
	ds_read_b128 v[180:183], v160 offset:3072
	s_add_u32 s28, s28, 0x80000
	s_addc_u32 s29, s29, 0
	s_mov_b32 m0, s45
	v_lshl_add_u64 v[220:221], s[28:29], 0, v[152:153]
	ds_read_b128 v[184:187], v199 offset:32768
	ds_read_b128 v[188:191], v199 offset:33792
	ds_read_b128 v[200:203], v199 offset:34816
	ds_read_b128 v[204:207], v199 offset:35840
	ds_read_b128 v[208:211], v199 offset:36864
	ds_read_b128 v[212:215], v199 offset:37888
	ds_read_b128 v[216:219], v199 offset:38912
	ds_read_b128 v[230:233], v199 offset:39936
	global_load_lds_dwordx4 v[220:221], off
	v_lshl_add_u64 v[220:221], s[28:29], 0, v[156:157]
	s_mov_b32 m0, s47
	s_nop 0
	global_load_lds_dwordx4 v[220:221], off
	s_waitcnt vmcnt(8)
	s_waitcnt lgkmcnt(0)
	s_barrier
	s_setprio 1
	s_waitcnt lgkmcnt(0)
	v_mfma_f32_16x16x32_bf16 v[124:127], v[128:131], v[184:187], v[124:127]
	v_mfma_f32_16x16x32_bf16 v[120:123], v[136:139], v[184:187], v[120:123]
	v_mfma_f32_16x16x32_bf16 v[108:111], v[128:131], v[200:203], v[108:111]
	v_mfma_f32_16x16x32_bf16 v[104:107], v[136:139], v[200:203], v[104:107]
	v_mfma_f32_16x16x32_bf16 v[92:95], v[128:131], v[208:211], v[92:95]
	v_mfma_f32_16x16x32_bf16 v[88:91], v[136:139], v[208:211], v[88:91]
	v_mfma_f32_16x16x32_bf16 v[76:79], v[128:131], v[216:219], v[76:79]
	v_mfma_f32_16x16x32_bf16 v[72:75], v[136:139], v[216:219], v[72:75]
	v_mfma_f32_16x16x32_bf16 v[124:127], v[132:135], v[188:191], v[124:127]
	v_mfma_f32_16x16x32_bf16 v[120:123], v[140:143], v[188:191], v[120:123]
	v_mfma_f32_16x16x32_bf16 v[108:111], v[132:135], v[204:207], v[108:111]
	v_mfma_f32_16x16x32_bf16 v[104:107], v[140:143], v[204:207], v[104:107]
	v_mfma_f32_16x16x32_bf16 v[92:95], v[132:135], v[212:215], v[92:95]
	v_mfma_f32_16x16x32_bf16 v[88:91], v[140:143], v[212:215], v[88:91]
	v_mfma_f32_16x16x32_bf16 v[76:79], v[132:135], v[230:233], v[76:79]
	v_mfma_f32_16x16x32_bf16 v[72:75], v[140:143], v[230:233], v[72:75]
	s_setprio 0
	s_setprio 1
	v_mfma_f32_16x16x32_bf16 v[116:119], v[144:147], v[184:187], v[116:119]
	v_mfma_f32_16x16x32_bf16 v[112:115], v[176:179], v[184:187], v[112:115]
	v_mfma_f32_16x16x32_bf16 v[100:103], v[144:147], v[200:203], v[100:103]
	v_mfma_f32_16x16x32_bf16 v[96:99], v[176:179], v[200:203], v[96:99]
	v_mfma_f32_16x16x32_bf16 v[84:87], v[144:147], v[208:211], v[84:87]
	v_mfma_f32_16x16x32_bf16 v[80:83], v[176:179], v[208:211], v[80:83]
	v_mfma_f32_16x16x32_bf16 v[68:71], v[144:147], v[216:219], v[68:71]
	v_mfma_f32_16x16x32_bf16 v[64:67], v[176:179], v[216:219], v[64:67]
	v_mfma_f32_16x16x32_bf16 v[116:119], v[148:151], v[188:191], v[116:119]
	v_mfma_f32_16x16x32_bf16 v[112:115], v[180:183], v[188:191], v[112:115]
	v_mfma_f32_16x16x32_bf16 v[100:103], v[148:151], v[204:207], v[100:103]
	v_mfma_f32_16x16x32_bf16 v[96:99], v[180:183], v[204:207], v[96:99]
	v_mfma_f32_16x16x32_bf16 v[84:87], v[148:151], v[212:215], v[84:87]
	v_mfma_f32_16x16x32_bf16 v[80:83], v[180:183], v[212:215], v[80:83]
	v_mfma_f32_16x16x32_bf16 v[68:71], v[148:151], v[230:233], v[68:71]
	v_mfma_f32_16x16x32_bf16 v[64:67], v[180:183], v[230:233], v[64:67]
	s_setprio 0
	s_barrier
	s_mov_b32 m0, s49
	v_lshl_add_u64 v[162:163], v[162:163], 0, s[86:87]
	s_add_u32 s26, s26, 0x80080
	ds_read_b128 v[184:187], v199 offset:49152
	ds_read_b128 v[188:191], v199 offset:50176
	ds_read_b128 v[200:203], v199 offset:51200
	ds_read_b128 v[204:207], v199 offset:52224
	ds_read_b128 v[208:211], v199 offset:53248
	ds_read_b128 v[212:215], v199 offset:54272
	ds_read_b128 v[216:219], v199 offset:55296
	ds_read_b128 v[230:233], v199 offset:56320
	global_load_lds_dwordx4 v[162:163], off
	v_lshl_add_u64 v[162:163], v[166:167], 0, s[86:87]
	s_mov_b32 m0, s50
	s_addc_u32 s27, s27, 0
	global_load_lds_dwordx4 v[162:163], off
	v_lshl_add_u64 v[162:163], s[26:27], 0, v[154:155]
	s_mov_b32 m0, s54
	s_nop 0
	global_load_lds_dwordx4 v[162:163], off
	v_lshl_add_u64 v[162:163], s[26:27], 0, v[158:159]
	s_mov_b32 m0, s55
	s_nop 0
	global_load_lds_dwordx4 v[162:163], off
	v_lshl_add_u64 v[162:163], v[194:195], 0, s[86:87]
	s_mov_b32 m0, s51
	s_nop 0
	global_load_lds_dwordx4 v[162:163], off
	v_lshl_add_u64 v[162:163], v[196:197], 0, s[86:87]
	s_mov_b32 m0, s52
	s_nop 0
	global_load_lds_dwordx4 v[162:163], off
	s_waitcnt vmcnt(8)
	s_waitcnt lgkmcnt(0)
	s_barrier
	s_setprio 1
	s_waitcnt lgkmcnt(0)
	v_mfma_f32_16x16x32_bf16 v[60:63], v[128:131], v[184:187], v[60:63]
	v_mfma_f32_16x16x32_bf16 v[56:59], v[136:139], v[184:187], v[56:59]
	v_mfma_f32_16x16x32_bf16 v[44:47], v[128:131], v[200:203], v[44:47]
	v_mfma_f32_16x16x32_bf16 v[40:43], v[136:139], v[200:203], v[40:43]
	v_mfma_f32_16x16x32_bf16 v[28:31], v[128:131], v[208:211], v[28:31]
	v_mfma_f32_16x16x32_bf16 v[24:27], v[136:139], v[208:211], v[24:27]
	v_mfma_f32_16x16x32_bf16 v[12:15], v[128:131], v[216:219], v[12:15]
	v_mfma_f32_16x16x32_bf16 v[8:11], v[136:139], v[216:219], v[8:11]
	v_mfma_f32_16x16x32_bf16 v[60:63], v[132:135], v[188:191], v[60:63]
	v_mfma_f32_16x16x32_bf16 v[56:59], v[140:143], v[188:191], v[56:59]
	v_mfma_f32_16x16x32_bf16 v[44:47], v[132:135], v[204:207], v[44:47]
	v_mfma_f32_16x16x32_bf16 v[40:43], v[140:143], v[204:207], v[40:43]
	v_mfma_f32_16x16x32_bf16 v[28:31], v[132:135], v[212:215], v[28:31]
	v_mfma_f32_16x16x32_bf16 v[24:27], v[140:143], v[212:215], v[24:27]
	v_mfma_f32_16x16x32_bf16 v[12:15], v[132:135], v[230:233], v[12:15]
	v_mfma_f32_16x16x32_bf16 v[8:11], v[140:143], v[230:233], v[8:11]
	s_setprio 0
	s_setprio 1
	v_mfma_f32_16x16x32_bf16 v[52:55], v[144:147], v[184:187], v[52:55]
	v_mfma_f32_16x16x32_bf16 v[48:51], v[176:179], v[184:187], v[48:51]
	v_mfma_f32_16x16x32_bf16 v[36:39], v[144:147], v[200:203], v[36:39]
	v_mfma_f32_16x16x32_bf16 v[32:35], v[176:179], v[200:203], v[32:35]
	v_mfma_f32_16x16x32_bf16 v[20:23], v[144:147], v[208:211], v[20:23]
	v_mfma_f32_16x16x32_bf16 v[16:19], v[176:179], v[208:211], v[16:19]
	v_mfma_f32_16x16x32_bf16 v[4:7], v[144:147], v[216:219], v[4:7]
	v_mfma_f32_16x16x32_bf16 v[0:3], v[176:179], v[216:219], v[0:3]
	v_mfma_f32_16x16x32_bf16 v[52:55], v[148:151], v[188:191], v[52:55]
	v_mfma_f32_16x16x32_bf16 v[48:51], v[180:183], v[188:191], v[48:51]
	v_mfma_f32_16x16x32_bf16 v[36:39], v[148:151], v[204:207], v[36:39]
	v_mfma_f32_16x16x32_bf16 v[32:35], v[180:183], v[204:207], v[32:35]
	v_mfma_f32_16x16x32_bf16 v[20:23], v[148:151], v[212:215], v[20:23]
	v_mfma_f32_16x16x32_bf16 v[16:19], v[180:183], v[212:215], v[16:19]
	v_mfma_f32_16x16x32_bf16 v[4:7], v[148:151], v[230:233], v[4:7]
	v_mfma_f32_16x16x32_bf16 v[0:3], v[180:183], v[230:233], v[0:3]
	s_setprio 0
	s_add_i32 s61, s61, 2
	s_add_u32 s59, s59, 0x100
	s_addc_u32 s60, s60, 0
	s_add_u32 s8, s8, 0x100
	s_addc_u32 s9, s9, 0
	s_barrier
	s_branch .LBB0_189

.LBB0_189:
	v_add_u32_e32 v140, s37, v193
	v_add_u32_e32 v160, s40, v193
	ds_read_b128 v[128:131], v140
	ds_read_b128 v[132:135], v140 offset:1024
	ds_read_b128 v[136:139], v140 offset:2048
	ds_read_b128 v[140:143], v140 offset:3072
	ds_read_b128 v[144:147], v160
	ds_read_b128 v[148:151], v160 offset:1024
	ds_read_b128 v[176:179], v160 offset:2048
	ds_read_b128 v[180:183], v160 offset:3072
	s_add_u32 s26, s8, 0xfff80080
	s_addc_u32 s27, s9, -1
	s_cmp_eq_u32 s61, 28
	s_cselect_b32 s29, s5, s27
	s_cselect_b32 s28, s7, s26
	s_cselect_b32 s27, s19, s60
	s_cselect_b32 s26, s21, s59
	v_lshl_add_u64 v[162:163], s[8:9], 0, v[174:175]
	s_add_i32 m0, s43, 0xc000
	ds_read_b128 v[184:187], v199
	ds_read_b128 v[188:191], v199 offset:1024
	ds_read_b128 v[200:203], v199 offset:2048
	ds_read_b128 v[204:207], v199 offset:3072
	ds_read_b128 v[208:211], v199 offset:4096
	ds_read_b128 v[212:215], v199 offset:5120
	ds_read_b128 v[216:219], v199 offset:6144
	ds_read_b128 v[230:233], v199 offset:7168
	global_load_lds_dwordx4 v[162:163], off
	v_lshl_add_u64 v[162:163], s[8:9], 0, v[172:173]
	s_add_i32 m0, s43, 0xe000
	s_nop 0
	global_load_lds_dwordx4 v[162:163], off
	s_waitcnt vmcnt(8)
	s_waitcnt lgkmcnt(0)
	s_barrier
	s_setprio 1
	s_waitcnt lgkmcnt(0)
	v_mfma_f32_16x16x32_bf16 v[124:127], v[128:131], v[184:187], v[124:127]
	v_mfma_f32_16x16x32_bf16 v[120:123], v[136:139], v[184:187], v[120:123]
	v_mfma_f32_16x16x32_bf16 v[108:111], v[128:131], v[200:203], v[108:111]
	v_mfma_f32_16x16x32_bf16 v[104:107], v[136:139], v[200:203], v[104:107]
	v_mfma_f32_16x16x32_bf16 v[92:95], v[128:131], v[208:211], v[92:95]
	v_mfma_f32_16x16x32_bf16 v[88:91], v[136:139], v[208:211], v[88:91]
	v_mfma_f32_16x16x32_bf16 v[76:79], v[128:131], v[216:219], v[76:79]
	v_mfma_f32_16x16x32_bf16 v[72:75], v[136:139], v[216:219], v[72:75]
	v_mfma_f32_16x16x32_bf16 v[124:127], v[132:135], v[188:191], v[124:127]
	v_mfma_f32_16x16x32_bf16 v[120:123], v[140:143], v[188:191], v[120:123]
	v_mfma_f32_16x16x32_bf16 v[108:111], v[132:135], v[204:207], v[108:111]
	v_mfma_f32_16x16x32_bf16 v[104:107], v[140:143], v[204:207], v[104:107]
	v_mfma_f32_16x16x32_bf16 v[92:95], v[132:135], v[212:215], v[92:95]
	v_mfma_f32_16x16x32_bf16 v[88:91], v[140:143], v[212:215], v[88:91]
	v_mfma_f32_16x16x32_bf16 v[76:79], v[132:135], v[230:233], v[76:79]
	v_mfma_f32_16x16x32_bf16 v[72:75], v[140:143], v[230:233], v[72:75]
	s_setprio 0
	s_setprio 1
	v_mfma_f32_16x16x32_bf16 v[116:119], v[144:147], v[184:187], v[116:119]
	v_mfma_f32_16x16x32_bf16 v[112:115], v[176:179], v[184:187], v[112:115]
	v_mfma_f32_16x16x32_bf16 v[100:103], v[144:147], v[200:203], v[100:103]
	v_mfma_f32_16x16x32_bf16 v[96:99], v[176:179], v[200:203], v[96:99]
	v_mfma_f32_16x16x32_bf16 v[84:87], v[144:147], v[208:211], v[84:87]
	v_mfma_f32_16x16x32_bf16 v[80:83], v[176:179], v[208:211], v[80:83]
	v_mfma_f32_16x16x32_bf16 v[68:71], v[144:147], v[216:219], v[68:71]
	v_mfma_f32_16x16x32_bf16 v[64:67], v[176:179], v[216:219], v[64:67]
	v_mfma_f32_16x16x32_bf16 v[116:119], v[148:151], v[188:191], v[116:119]
	v_mfma_f32_16x16x32_bf16 v[112:115], v[180:183], v[188:191], v[112:115]
	v_mfma_f32_16x16x32_bf16 v[100:103], v[148:151], v[204:207], v[100:103]
	v_mfma_f32_16x16x32_bf16 v[96:99], v[180:183], v[204:207], v[96:99]
	v_mfma_f32_16x16x32_bf16 v[84:87], v[148:151], v[212:215], v[84:87]
	v_mfma_f32_16x16x32_bf16 v[80:83], v[180:183], v[212:215], v[80:83]
	v_mfma_f32_16x16x32_bf16 v[68:71], v[148:151], v[230:233], v[68:71]
	v_mfma_f32_16x16x32_bf16 v[64:67], v[180:183], v[230:233], v[64:67]
	s_setprio 0
	s_barrier
	s_mov_b32 m0, s38
	v_lshl_add_u64 v[162:163], s[26:27], 0, v[154:155]
	s_add_u32 s62, s26, 0x80000
	ds_read_b128 v[184:187], v199 offset:16384
	ds_read_b128 v[188:191], v199 offset:17408
	ds_read_b128 v[200:203], v199 offset:18432
	ds_read_b128 v[204:207], v199 offset:19456
	ds_read_b128 v[208:211], v199 offset:20480
	ds_read_b128 v[212:215], v199 offset:21504
	ds_read_b128 v[216:219], v199 offset:22528
	ds_read_b128 v[230:233], v199 offset:23552
	global_load_lds_dwordx4 v[162:163], off
	v_lshl_add_u64 v[166:167], s[26:27], 0, v[158:159]
	s_mov_b32 m0, s39
	s_addc_u32 s63, s27, 0
	global_load_lds_dwordx4 v[166:167], off
	v_lshl_add_u64 v[194:195], s[62:63], 0, v[154:155]
	s_mov_b32 m0, s41
	v_lshl_add_u64 v[196:197], s[28:29], 0, v[156:157]
	global_load_lds_dwordx4 v[194:195], off
	v_lshl_add_u64 v[194:195], s[62:63], 0, v[158:159]
	s_mov_b32 m0, s42
	s_nop 0
	global_load_lds_dwordx4 v[194:195], off
	v_lshl_add_u64 v[194:195], s[28:29], 0, v[152:153]
	s_mov_b32 m0, s43
	s_nop 0
	global_load_lds_dwordx4 v[194:195], off
	s_mov_b32 m0, s44
	s_nop 0
	global_load_lds_dwordx4 v[196:197], off
	s_waitcnt vmcnt(8)
	s_waitcnt lgkmcnt(0)
	s_barrier
	s_setprio 1
	s_waitcnt lgkmcnt(0)
	v_mfma_f32_16x16x32_bf16 v[60:63], v[128:131], v[184:187], v[60:63]
	v_mfma_f32_16x16x32_bf16 v[56:59], v[136:139], v[184:187], v[56:59]
	v_mfma_f32_16x16x32_bf16 v[44:47], v[128:131], v[200:203], v[44:47]
	v_mfma_f32_16x16x32_bf16 v[40:43], v[136:139], v[200:203], v[40:43]
	v_mfma_f32_16x16x32_bf16 v[28:31], v[128:131], v[208:211], v[28:31]
	v_mfma_f32_16x16x32_bf16 v[24:27], v[136:139], v[208:211], v[24:27]
	v_mfma_f32_16x16x32_bf16 v[12:15], v[128:131], v[216:219], v[12:15]
	v_mfma_f32_16x16x32_bf16 v[8:11], v[136:139], v[216:219], v[8:11]
	v_mfma_f32_16x16x32_bf16 v[60:63], v[132:135], v[188:191], v[60:63]
	v_mfma_f32_16x16x32_bf16 v[56:59], v[140:143], v[188:191], v[56:59]
	v_mfma_f32_16x16x32_bf16 v[44:47], v[132:135], v[204:207], v[44:47]
	v_mfma_f32_16x16x32_bf16 v[40:43], v[140:143], v[204:207], v[40:43]
	v_mfma_f32_16x16x32_bf16 v[28:31], v[132:135], v[212:215], v[28:31]
	v_mfma_f32_16x16x32_bf16 v[24:27], v[140:143], v[212:215], v[24:27]
	v_mfma_f32_16x16x32_bf16 v[12:15], v[132:135], v[230:233], v[12:15]
	v_mfma_f32_16x16x32_bf16 v[8:11], v[140:143], v[230:233], v[8:11]
	s_setprio 0
	s_setprio 1
	v_mfma_f32_16x16x32_bf16 v[52:55], v[144:147], v[184:187], v[52:55]
	v_mfma_f32_16x16x32_bf16 v[48:51], v[176:179], v[184:187], v[48:51]
	v_mfma_f32_16x16x32_bf16 v[36:39], v[144:147], v[200:203], v[36:39]
	v_mfma_f32_16x16x32_bf16 v[32:35], v[176:179], v[200:203], v[32:35]
	v_mfma_f32_16x16x32_bf16 v[20:23], v[144:147], v[208:211], v[20:23]
	v_mfma_f32_16x16x32_bf16 v[16:19], v[176:179], v[208:211], v[16:19]
	v_mfma_f32_16x16x32_bf16 v[4:7], v[144:147], v[216:219], v[4:7]
	v_mfma_f32_16x16x32_bf16 v[0:3], v[176:179], v[216:219], v[0:3]
	v_mfma_f32_16x16x32_bf16 v[52:55], v[148:151], v[188:191], v[52:55]
	v_mfma_f32_16x16x32_bf16 v[48:51], v[180:183], v[188:191], v[48:51]
	v_mfma_f32_16x16x32_bf16 v[36:39], v[148:151], v[204:207], v[36:39]
	v_mfma_f32_16x16x32_bf16 v[32:35], v[180:183], v[204:207], v[32:35]
	v_mfma_f32_16x16x32_bf16 v[20:23], v[148:151], v[212:215], v[20:23]
	v_mfma_f32_16x16x32_bf16 v[16:19], v[180:183], v[212:215], v[16:19]
	v_mfma_f32_16x16x32_bf16 v[4:7], v[148:151], v[230:233], v[4:7]
	v_mfma_f32_16x16x32_bf16 v[0:3], v[180:183], v[230:233], v[0:3]
	s_setprio 0
	s_barrier
	v_add_u32_e32 v140, s48, v193
	v_add_u32_e32 v160, s53, v193
	ds_read_b128 v[128:131], v140
	ds_read_b128 v[132:135], v140 offset:1024
	ds_read_b128 v[136:139], v140 offset:2048
	ds_read_b128 v[140:143], v140 offset:3072
	ds_read_b128 v[144:147], v160
	ds_read_b128 v[148:151], v160 offset:1024
	ds_read_b128 v[176:179], v160 offset:2048
	ds_read_b128 v[180:183], v160 offset:3072
	s_add_u32 s28, s28, 0x80000
	s_addc_u32 s29, s29, 0
	s_mov_b32 m0, s45
	v_lshl_add_u64 v[220:221], s[28:29], 0, v[152:153]
	ds_read_b128 v[184:187], v199 offset:32768
	ds_read_b128 v[188:191], v199 offset:33792
	ds_read_b128 v[200:203], v199 offset:34816
	ds_read_b128 v[204:207], v199 offset:35840
	ds_read_b128 v[208:211], v199 offset:36864
	ds_read_b128 v[212:215], v199 offset:37888
	ds_read_b128 v[216:219], v199 offset:38912
	ds_read_b128 v[230:233], v199 offset:39936
	global_load_lds_dwordx4 v[220:221], off
	v_lshl_add_u64 v[220:221], s[28:29], 0, v[156:157]
	s_mov_b32 m0, s47
	s_nop 0
	global_load_lds_dwordx4 v[220:221], off
	s_waitcnt vmcnt(8)
	s_waitcnt lgkmcnt(0)
	s_barrier
	s_setprio 1
	s_waitcnt lgkmcnt(0)
	v_mfma_f32_16x16x32_bf16 v[124:127], v[128:131], v[184:187], v[124:127]
	v_mfma_f32_16x16x32_bf16 v[120:123], v[136:139], v[184:187], v[120:123]
	v_mfma_f32_16x16x32_bf16 v[108:111], v[128:131], v[200:203], v[108:111]
	v_mfma_f32_16x16x32_bf16 v[104:107], v[136:139], v[200:203], v[104:107]
	v_mfma_f32_16x16x32_bf16 v[92:95], v[128:131], v[208:211], v[92:95]
	v_mfma_f32_16x16x32_bf16 v[88:91], v[136:139], v[208:211], v[88:91]
	v_mfma_f32_16x16x32_bf16 v[76:79], v[128:131], v[216:219], v[76:79]
	v_mfma_f32_16x16x32_bf16 v[72:75], v[136:139], v[216:219], v[72:75]
	v_mfma_f32_16x16x32_bf16 v[124:127], v[132:135], v[188:191], v[124:127]
	v_mfma_f32_16x16x32_bf16 v[120:123], v[140:143], v[188:191], v[120:123]
	v_mfma_f32_16x16x32_bf16 v[108:111], v[132:135], v[204:207], v[108:111]
	v_mfma_f32_16x16x32_bf16 v[104:107], v[140:143], v[204:207], v[104:107]
	v_mfma_f32_16x16x32_bf16 v[92:95], v[132:135], v[212:215], v[92:95]
	v_mfma_f32_16x16x32_bf16 v[88:91], v[140:143], v[212:215], v[88:91]
	v_mfma_f32_16x16x32_bf16 v[76:79], v[132:135], v[230:233], v[76:79]
	v_mfma_f32_16x16x32_bf16 v[72:75], v[140:143], v[230:233], v[72:75]
	s_setprio 0
	s_setprio 1
	v_mfma_f32_16x16x32_bf16 v[116:119], v[144:147], v[184:187], v[116:119]
	v_mfma_f32_16x16x32_bf16 v[112:115], v[176:179], v[184:187], v[112:115]
	v_mfma_f32_16x16x32_bf16 v[100:103], v[144:147], v[200:203], v[100:103]
	v_mfma_f32_16x16x32_bf16 v[96:99], v[176:179], v[200:203], v[96:99]
	v_mfma_f32_16x16x32_bf16 v[84:87], v[144:147], v[208:211], v[84:87]
	v_mfma_f32_16x16x32_bf16 v[80:83], v[176:179], v[208:211], v[80:83]
	v_mfma_f32_16x16x32_bf16 v[68:71], v[144:147], v[216:219], v[68:71]
	v_mfma_f32_16x16x32_bf16 v[64:67], v[176:179], v[216:219], v[64:67]
	v_mfma_f32_16x16x32_bf16 v[116:119], v[148:151], v[188:191], v[116:119]
	v_mfma_f32_16x16x32_bf16 v[112:115], v[180:183], v[188:191], v[112:115]
	v_mfma_f32_16x16x32_bf16 v[100:103], v[148:151], v[204:207], v[100:103]
	v_mfma_f32_16x16x32_bf16 v[96:99], v[180:183], v[204:207], v[96:99]
	v_mfma_f32_16x16x32_bf16 v[84:87], v[148:151], v[212:215], v[84:87]
	v_mfma_f32_16x16x32_bf16 v[80:83], v[180:183], v[212:215], v[80:83]
	v_mfma_f32_16x16x32_bf16 v[68:71], v[148:151], v[230:233], v[68:71]
	v_mfma_f32_16x16x32_bf16 v[64:67], v[180:183], v[230:233], v[64:67]
	s_setprio 0
	s_barrier
	s_mov_b32 m0, s49
	v_lshl_add_u64 v[162:163], v[162:163], 0, s[86:87]
	s_add_u32 s26, s26, 0x80080
	ds_read_b128 v[184:187], v199 offset:49152
	ds_read_b128 v[188:191], v199 offset:50176
	ds_read_b128 v[200:203], v199 offset:51200
	ds_read_b128 v[204:207], v199 offset:52224
	ds_read_b128 v[208:211], v199 offset:53248
	ds_read_b128 v[212:215], v199 offset:54272
	ds_read_b128 v[216:219], v199 offset:55296
	ds_read_b128 v[230:233], v199 offset:56320
	global_load_lds_dwordx4 v[162:163], off
	v_lshl_add_u64 v[162:163], v[166:167], 0, s[86:87]
	s_mov_b32 m0, s50
	s_addc_u32 s27, s27, 0
	global_load_lds_dwordx4 v[162:163], off
	v_lshl_add_u64 v[162:163], s[26:27], 0, v[154:155]
	s_mov_b32 m0, s54
	s_nop 0
	global_load_lds_dwordx4 v[162:163], off
	v_lshl_add_u64 v[162:163], s[26:27], 0, v[158:159]
	s_mov_b32 m0, s55
	s_nop 0
	global_load_lds_dwordx4 v[162:163], off
	v_lshl_add_u64 v[162:163], v[194:195], 0, s[86:87]
	s_mov_b32 m0, s51
	s_nop 0
	global_load_lds_dwordx4 v[162:163], off
	v_lshl_add_u64 v[162:163], v[196:197], 0, s[86:87]
	s_mov_b32 m0, s52
	s_nop 0
	global_load_lds_dwordx4 v[162:163], off
	s_waitcnt vmcnt(8)
	s_waitcnt lgkmcnt(0)
	s_barrier
	s_setprio 1
	s_waitcnt lgkmcnt(0)
	v_mfma_f32_16x16x32_bf16 v[60:63], v[128:131], v[184:187], v[60:63]
	v_mfma_f32_16x16x32_bf16 v[56:59], v[136:139], v[184:187], v[56:59]
	v_mfma_f32_16x16x32_bf16 v[44:47], v[128:131], v[200:203], v[44:47]
	v_mfma_f32_16x16x32_bf16 v[40:43], v[136:139], v[200:203], v[40:43]
	v_mfma_f32_16x16x32_bf16 v[28:31], v[128:131], v[208:211], v[28:31]
	v_mfma_f32_16x16x32_bf16 v[24:27], v[136:139], v[208:211], v[24:27]
	v_mfma_f32_16x16x32_bf16 v[12:15], v[128:131], v[216:219], v[12:15]
	v_mfma_f32_16x16x32_bf16 v[8:11], v[136:139], v[216:219], v[8:11]
	v_mfma_f32_16x16x32_bf16 v[60:63], v[132:135], v[188:191], v[60:63]
	v_mfma_f32_16x16x32_bf16 v[56:59], v[140:143], v[188:191], v[56:59]
	v_mfma_f32_16x16x32_bf16 v[44:47], v[132:135], v[204:207], v[44:47]
	v_mfma_f32_16x16x32_bf16 v[40:43], v[140:143], v[204:207], v[40:43]
	v_mfma_f32_16x16x32_bf16 v[28:31], v[132:135], v[212:215], v[28:31]
	v_mfma_f32_16x16x32_bf16 v[24:27], v[140:143], v[212:215], v[24:27]
	v_mfma_f32_16x16x32_bf16 v[12:15], v[132:135], v[230:233], v[12:15]
	v_mfma_f32_16x16x32_bf16 v[8:11], v[140:143], v[230:233], v[8:11]
	s_setprio 0
	s_setprio 1
	v_mfma_f32_16x16x32_bf16 v[52:55], v[144:147], v[184:187], v[52:55]
	v_mfma_f32_16x16x32_bf16 v[48:51], v[176:179], v[184:187], v[48:51]
	v_mfma_f32_16x16x32_bf16 v[36:39], v[144:147], v[200:203], v[36:39]
	v_mfma_f32_16x16x32_bf16 v[32:35], v[176:179], v[200:203], v[32:35]
	v_mfma_f32_16x16x32_bf16 v[20:23], v[144:147], v[208:211], v[20:23]
	v_mfma_f32_16x16x32_bf16 v[16:19], v[176:179], v[208:211], v[16:19]
	v_mfma_f32_16x16x32_bf16 v[4:7], v[144:147], v[216:219], v[4:7]
	v_mfma_f32_16x16x32_bf16 v[0:3], v[176:179], v[216:219], v[0:3]
	v_mfma_f32_16x16x32_bf16 v[52:55], v[148:151], v[188:191], v[52:55]
	v_mfma_f32_16x16x32_bf16 v[48:51], v[180:183], v[188:191], v[48:51]
	v_mfma_f32_16x16x32_bf16 v[36:39], v[148:151], v[204:207], v[36:39]
	v_mfma_f32_16x16x32_bf16 v[32:35], v[180:183], v[204:207], v[32:35]
	v_mfma_f32_16x16x32_bf16 v[20:23], v[148:151], v[212:215], v[20:23]
	v_mfma_f32_16x16x32_bf16 v[16:19], v[180:183], v[212:215], v[16:19]
	v_mfma_f32_16x16x32_bf16 v[4:7], v[148:151], v[230:233], v[4:7]
	v_mfma_f32_16x16x32_bf16 v[0:3], v[180:183], v[230:233], v[0:3]
	s_setprio 0
	s_add_i32 s61, s61, 2
	s_add_u32 s59, s59, 0x100
	s_addc_u32 s60, s60, 0
	s_add_u32 s8, s8, 0x100
	s_addc_u32 s9, s9, 0
	s_cmp_gt_u32 s61, 29
	s_barrier
	s_cbranch_scc0 .LBB0_189
	s_and_b64 vcc, exec, s[12:13]
	s_cbranch_vccz .LBB0_192
	s_barrier

.LBB0_750:
	v_mov_b64_e32 v[0:1], 0x400
	s_ashr_i32 s7, s6, 31
	v_cmp_lt_i64_e32 vcc, s[8:9], v[0:1]
	s_lshl_b64 s[8:9], s[6:7], 20
	s_add_u32 s8, s23, s8
	s_addc_u32 s9, s24, s9
	s_and_b64 s[10:11], vcc, exec
	s_cselect_b32 s7, s9, s17
	s_cselect_b32 s50, s8, s16
	s_ashr_i32 s5, s4, 31
	s_lshl_b64 s[10:11], s[4:5], 20
	s_add_u32 s10, s25, s10
	s_addc_u32 s11, s26, s11
	s_and_b64 s[18:19], vcc, exec
	s_cselect_b32 s5, s11, s15
	s_cselect_b32 s51, s10, s14
	s_add_u32 s52, s14, 0x100
	s_addc_u32 s53, s15, 0
	s_add_u32 s14, s16, 0x80080
	v_mov_b32_e32 v0, 0
	s_addc_u32 s15, s17, 0
	s_mov_b32 s54, -2
	s_cmp_eq_u32 s48, 1
	s_cbranch_scc1 .Lpeel_zero_P5
	v_add_u32_e32 v120, s13, v230
	v_add_u32_e32 v148, s29, v230
	ds_read_b128 v[88:91], v120
	ds_read_b128 v[100:103], v120 offset:1024
	ds_read_b128 v[112:115], v120 offset:2048
	ds_read_b128 v[120:123], v120 offset:3072
	ds_read_b128 v[124:127], v148
	ds_read_b128 v[140:143], v148 offset:1024
	ds_read_b128 v[144:147], v148 offset:2048
	ds_read_b128 v[148:151], v148 offset:3072
	s_add_u32 s16, s14, 0xfff80080
	s_addc_u32 s17, s15, -1
	s_cmp_eq_u32 s54, 28
	s_cselect_b32 s19, s7, s17
	s_cselect_b32 s18, s50, s16
	s_cselect_b32 s17, s5, s53
	s_cselect_b32 s16, s51, s52
	v_lshl_add_u64 v[206:207], s[14:15], 0, v[204:205]
	s_add_i32 m0, s34, 0xc000
	ds_read_b128 v[152:155], v232
	ds_read_b128 v[170:173], v232 offset:1024
	ds_read_b128 v[174:177], v232 offset:2048
	ds_read_b128 v[178:181], v232 offset:3072
	ds_read_b128 v[182:185], v232 offset:4096
	ds_read_b128 v[186:189], v232 offset:5120
	ds_read_b128 v[190:193], v232 offset:6144
	ds_read_b128 v[194:197], v232 offset:7168
	global_load_lds_dwordx4 v[206:207], off
	v_lshl_add_u64 v[206:207], s[14:15], 0, v[202:203]
	s_add_i32 m0, s34, 0xe000
	s_nop 0
	global_load_lds_dwordx4 v[206:207], off
	s_waitcnt vmcnt(40)
	s_waitcnt lgkmcnt(0)
	s_barrier
	s_setprio 1
	s_waitcnt lgkmcnt(0)
	v_mfma_f32_16x16x32_bf16 v[166:169], v[88:91], v[152:155], 0
	v_mfma_f32_16x16x32_bf16 v[156:159], v[112:115], v[152:155], 0
	v_mfma_f32_16x16x32_bf16 v[128:131], v[88:91], v[174:177], 0
	v_mfma_f32_16x16x32_bf16 v[116:119], v[112:115], v[174:177], 0
	v_mfma_f32_16x16x32_bf16 v[96:99], v[88:91], v[182:185], 0
	v_mfma_f32_16x16x32_bf16 v[92:95], v[112:115], v[182:185], 0
	v_mfma_f32_16x16x32_bf16 v[76:79], v[88:91], v[190:193], 0
	v_mfma_f32_16x16x32_bf16 v[72:75], v[112:115], v[190:193], 0
	v_mfma_f32_16x16x32_bf16 v[166:169], v[100:103], v[170:173], v[166:169]
	v_mfma_f32_16x16x32_bf16 v[156:159], v[120:123], v[170:173], v[156:159]
	v_mfma_f32_16x16x32_bf16 v[128:131], v[100:103], v[178:181], v[128:131]
	v_mfma_f32_16x16x32_bf16 v[116:119], v[120:123], v[178:181], v[116:119]
	v_mfma_f32_16x16x32_bf16 v[96:99], v[100:103], v[186:189], v[96:99]
	v_mfma_f32_16x16x32_bf16 v[92:95], v[120:123], v[186:189], v[92:95]
	v_mfma_f32_16x16x32_bf16 v[76:79], v[100:103], v[194:197], v[76:79]
	v_mfma_f32_16x16x32_bf16 v[72:75], v[120:123], v[194:197], v[72:75]
	s_setprio 0
	s_setprio 1
	v_mfma_f32_16x16x32_bf16 v[136:139], v[124:127], v[152:155], 0
	v_mfma_f32_16x16x32_bf16 v[132:135], v[144:147], v[152:155], 0
	v_mfma_f32_16x16x32_bf16 v[108:111], v[124:127], v[174:177], 0
	v_mfma_f32_16x16x32_bf16 v[104:107], v[144:147], v[174:177], 0
	v_mfma_f32_16x16x32_bf16 v[84:87], v[124:127], v[182:185], 0
	v_mfma_f32_16x16x32_bf16 v[80:83], v[144:147], v[182:185], 0
	v_mfma_f32_16x16x32_bf16 v[68:71], v[124:127], v[190:193], 0
	v_mfma_f32_16x16x32_bf16 v[64:67], v[144:147], v[190:193], 0
	v_mfma_f32_16x16x32_bf16 v[136:139], v[140:143], v[170:173], v[136:139]
	v_mfma_f32_16x16x32_bf16 v[132:135], v[148:151], v[170:173], v[132:135]
	v_mfma_f32_16x16x32_bf16 v[108:111], v[140:143], v[178:181], v[108:111]
	v_mfma_f32_16x16x32_bf16 v[104:107], v[148:151], v[178:181], v[104:107]
	v_mfma_f32_16x16x32_bf16 v[84:87], v[140:143], v[186:189], v[84:87]
	v_mfma_f32_16x16x32_bf16 v[80:83], v[148:151], v[186:189], v[80:83]
	v_mfma_f32_16x16x32_bf16 v[68:71], v[140:143], v[194:197], v[68:71]
	v_mfma_f32_16x16x32_bf16 v[64:67], v[148:151], v[194:197], v[64:67]
	s_setprio 0
	s_barrier
	s_mov_b32 m0, s27
	v_lshl_add_u64 v[206:207], s[16:17], 0, v[160:161]
	s_add_u32 s56, s16, 0x80000
	ds_read_b128 v[152:155], v232 offset:16384
	ds_read_b128 v[170:173], v232 offset:17408
	ds_read_b128 v[174:177], v232 offset:18432
	ds_read_b128 v[178:181], v232 offset:19456
	ds_read_b128 v[182:185], v232 offset:20480
	ds_read_b128 v[186:189], v232 offset:21504
	ds_read_b128 v[190:193], v232 offset:22528
	ds_read_b128 v[194:197], v232 offset:23552
	global_load_lds_dwordx4 v[206:207], off
	v_lshl_add_u64 v[208:209], s[16:17], 0, v[200:201]
	s_mov_b32 m0, s28
	s_addc_u32 s57, s17, 0
	global_load_lds_dwordx4 v[208:209], off
	v_lshl_add_u64 v[210:211], s[56:57], 0, v[160:161]
	s_mov_b32 m0, s30
	v_lshl_add_u64 v[212:213], s[18:19], 0, v[198:199]
	global_load_lds_dwordx4 v[210:211], off
	v_lshl_add_u64 v[210:211], s[56:57], 0, v[200:201]
	s_mov_b32 m0, s31
	s_nop 0
	global_load_lds_dwordx4 v[210:211], off
	v_lshl_add_u64 v[210:211], s[18:19], 0, v[162:163]
	s_mov_b32 m0, s34
	s_nop 0
	global_load_lds_dwordx4 v[210:211], off
	s_mov_b32 m0, s35
	s_nop 0
	global_load_lds_dwordx4 v[212:213], off
	s_waitcnt vmcnt(40)
	s_waitcnt lgkmcnt(0)
	s_barrier
	s_setprio 1
	s_waitcnt lgkmcnt(0)
	v_mfma_f32_16x16x32_bf16 v[60:63], v[88:91], v[152:155], 0
	v_mfma_f32_16x16x32_bf16 v[56:59], v[112:115], v[152:155], 0
	v_mfma_f32_16x16x32_bf16 v[44:47], v[88:91], v[174:177], 0
	v_mfma_f32_16x16x32_bf16 v[40:43], v[112:115], v[174:177], 0
	v_mfma_f32_16x16x32_bf16 v[28:31], v[88:91], v[182:185], 0
	v_mfma_f32_16x16x32_bf16 v[24:27], v[112:115], v[182:185], 0
	v_mfma_f32_16x16x32_bf16 v[12:15], v[88:91], v[190:193], 0
	v_mfma_f32_16x16x32_bf16 v[8:11], v[112:115], v[190:193], 0
	v_mfma_f32_16x16x32_bf16 v[60:63], v[100:103], v[170:173], v[60:63]
	v_mfma_f32_16x16x32_bf16 v[56:59], v[120:123], v[170:173], v[56:59]
	v_mfma_f32_16x16x32_bf16 v[44:47], v[100:103], v[178:181], v[44:47]
	v_mfma_f32_16x16x32_bf16 v[40:43], v[120:123], v[178:181], v[40:43]
	v_mfma_f32_16x16x32_bf16 v[28:31], v[100:103], v[186:189], v[28:31]
	v_mfma_f32_16x16x32_bf16 v[24:27], v[120:123], v[186:189], v[24:27]
	v_mfma_f32_16x16x32_bf16 v[12:15], v[100:103], v[194:197], v[12:15]
	v_mfma_f32_16x16x32_bf16 v[8:11], v[120:123], v[194:197], v[8:11]
	s_setprio 0
	s_setprio 1
	v_mfma_f32_16x16x32_bf16 v[52:55], v[124:127], v[152:155], 0
	v_mfma_f32_16x16x32_bf16 v[48:51], v[144:147], v[152:155], 0
	v_mfma_f32_16x16x32_bf16 v[36:39], v[124:127], v[174:177], 0
	v_mfma_f32_16x16x32_bf16 v[32:35], v[144:147], v[174:177], 0
	v_mfma_f32_16x16x32_bf16 v[20:23], v[124:127], v[182:185], 0
	v_mfma_f32_16x16x32_bf16 v[16:19], v[144:147], v[182:185], 0
	v_mfma_f32_16x16x32_bf16 v[4:7], v[124:127], v[190:193], 0
	v_mfma_f32_16x16x32_bf16 v[0:3], v[144:147], v[190:193], 0
	v_mfma_f32_16x16x32_bf16 v[52:55], v[140:143], v[170:173], v[52:55]
	v_mfma_f32_16x16x32_bf16 v[48:51], v[148:151], v[170:173], v[48:51]
	v_mfma_f32_16x16x32_bf16 v[36:39], v[140:143], v[178:181], v[36:39]
	v_mfma_f32_16x16x32_bf16 v[32:35], v[148:151], v[178:181], v[32:35]
	v_mfma_f32_16x16x32_bf16 v[20:23], v[140:143], v[186:189], v[20:23]
	v_mfma_f32_16x16x32_bf16 v[16:19], v[148:151], v[186:189], v[16:19]
	v_mfma_f32_16x16x32_bf16 v[4:7], v[140:143], v[194:197], v[4:7]
	v_mfma_f32_16x16x32_bf16 v[0:3], v[148:151], v[194:197], v[0:3]
	s_setprio 0
	s_barrier
	v_add_u32_e32 v120, s39, v230
	v_add_u32_e32 v148, s44, v230
	ds_read_b128 v[88:91], v120
	ds_read_b128 v[100:103], v120 offset:1024
	ds_read_b128 v[112:115], v120 offset:2048
	ds_read_b128 v[120:123], v120 offset:3072
	ds_read_b128 v[124:127], v148
	ds_read_b128 v[140:143], v148 offset:1024
	ds_read_b128 v[144:147], v148 offset:2048
	ds_read_b128 v[148:151], v148 offset:3072
	s_add_u32 s18, s18, 0x80000
	s_addc_u32 s19, s19, 0
	s_mov_b32 m0, s36
	v_lshl_add_u64 v[214:215], s[18:19], 0, v[162:163]
	ds_read_b128 v[152:155], v232 offset:32768
	ds_read_b128 v[170:173], v232 offset:33792
	ds_read_b128 v[174:177], v232 offset:34816
	ds_read_b128 v[178:181], v232 offset:35840
	ds_read_b128 v[182:185], v232 offset:36864
	ds_read_b128 v[186:189], v232 offset:37888
	ds_read_b128 v[190:193], v232 offset:38912
	ds_read_b128 v[194:197], v232 offset:39936
	global_load_lds_dwordx4 v[214:215], off
	v_lshl_add_u64 v[214:215], s[18:19], 0, v[198:199]
	s_mov_b32 m0, s37
	s_nop 0
	global_load_lds_dwordx4 v[214:215], off
	s_waitcnt vmcnt(8)
	s_waitcnt lgkmcnt(0)
	s_barrier
	s_setprio 1
	s_waitcnt lgkmcnt(0)
	v_mfma_f32_16x16x32_bf16 v[166:169], v[88:91], v[152:155], v[166:169]
	v_mfma_f32_16x16x32_bf16 v[156:159], v[112:115], v[152:155], v[156:159]
	v_mfma_f32_16x16x32_bf16 v[128:131], v[88:91], v[174:177], v[128:131]
	v_mfma_f32_16x16x32_bf16 v[116:119], v[112:115], v[174:177], v[116:119]
	v_mfma_f32_16x16x32_bf16 v[96:99], v[88:91], v[182:185], v[96:99]
	v_mfma_f32_16x16x32_bf16 v[92:95], v[112:115], v[182:185], v[92:95]
	v_mfma_f32_16x16x32_bf16 v[76:79], v[88:91], v[190:193], v[76:79]
	v_mfma_f32_16x16x32_bf16 v[72:75], v[112:115], v[190:193], v[72:75]
	v_mfma_f32_16x16x32_bf16 v[166:169], v[100:103], v[170:173], v[166:169]
	v_mfma_f32_16x16x32_bf16 v[156:159], v[120:123], v[170:173], v[156:159]
	v_mfma_f32_16x16x32_bf16 v[128:131], v[100:103], v[178:181], v[128:131]
	v_mfma_f32_16x16x32_bf16 v[116:119], v[120:123], v[178:181], v[116:119]
	v_mfma_f32_16x16x32_bf16 v[96:99], v[100:103], v[186:189], v[96:99]
	v_mfma_f32_16x16x32_bf16 v[92:95], v[120:123], v[186:189], v[92:95]
	v_mfma_f32_16x16x32_bf16 v[76:79], v[100:103], v[194:197], v[76:79]
	v_mfma_f32_16x16x32_bf16 v[72:75], v[120:123], v[194:197], v[72:75]
	s_setprio 0
	s_setprio 1
	v_mfma_f32_16x16x32_bf16 v[136:139], v[124:127], v[152:155], v[136:139]
	v_mfma_f32_16x16x32_bf16 v[132:135], v[144:147], v[152:155], v[132:135]
	v_mfma_f32_16x16x32_bf16 v[108:111], v[124:127], v[174:177], v[108:111]
	v_mfma_f32_16x16x32_bf16 v[104:107], v[144:147], v[174:177], v[104:107]
	v_mfma_f32_16x16x32_bf16 v[84:87], v[124:127], v[182:185], v[84:87]
	v_mfma_f32_16x16x32_bf16 v[80:83], v[144:147], v[182:185], v[80:83]
	v_mfma_f32_16x16x32_bf16 v[68:71], v[124:127], v[190:193], v[68:71]
	v_mfma_f32_16x16x32_bf16 v[64:67], v[144:147], v[190:193], v[64:67]
	v_mfma_f32_16x16x32_bf16 v[136:139], v[140:143], v[170:173], v[136:139]
	v_mfma_f32_16x16x32_bf16 v[132:135], v[148:151], v[170:173], v[132:135]
	v_mfma_f32_16x16x32_bf16 v[108:111], v[140:143], v[178:181], v[108:111]
	v_mfma_f32_16x16x32_bf16 v[104:107], v[148:151], v[178:181], v[104:107]
	v_mfma_f32_16x16x32_bf16 v[84:87], v[140:143], v[186:189], v[84:87]
	v_mfma_f32_16x16x32_bf16 v[80:83], v[148:151], v[186:189], v[80:83]
	v_mfma_f32_16x16x32_bf16 v[68:71], v[140:143], v[194:197], v[68:71]
	v_mfma_f32_16x16x32_bf16 v[64:67], v[148:151], v[194:197], v[64:67]
	s_setprio 0
	s_barrier
	s_mov_b32 m0, s40
	v_lshl_add_u64 v[206:207], v[206:207], 0, s[86:87]
	s_add_u32 s16, s16, 0x80080
	ds_read_b128 v[152:155], v232 offset:49152
	ds_read_b128 v[170:173], v232 offset:50176
	ds_read_b128 v[174:177], v232 offset:51200
	ds_read_b128 v[178:181], v232 offset:52224
	ds_read_b128 v[182:185], v232 offset:53248
	ds_read_b128 v[186:189], v232 offset:54272
	ds_read_b128 v[190:193], v232 offset:55296
	ds_read_b128 v[194:197], v232 offset:56320
	global_load_lds_dwordx4 v[206:207], off
	v_lshl_add_u64 v[206:207], v[208:209], 0, s[86:87]
	s_mov_b32 m0, s41
	s_addc_u32 s17, s17, 0
	global_load_lds_dwordx4 v[206:207], off
	v_lshl_add_u64 v[206:207], s[16:17], 0, v[160:161]
	s_mov_b32 m0, s45
	s_nop 0
	global_load_lds_dwordx4 v[206:207], off
	v_lshl_add_u64 v[206:207], s[16:17], 0, v[200:201]
	s_mov_b32 m0, s46
	s_nop 0
	global_load_lds_dwordx4 v[206:207], off
	v_lshl_add_u64 v[206:207], v[210:211], 0, s[86:87]
	s_mov_b32 m0, s42
	s_nop 0
	global_load_lds_dwordx4 v[206:207], off
	v_lshl_add_u64 v[206:207], v[212:213], 0, s[86:87]
	s_mov_b32 m0, s43
	s_nop 0
	global_load_lds_dwordx4 v[206:207], off
	s_waitcnt vmcnt(8)
	s_waitcnt lgkmcnt(0)
	s_barrier
	s_setprio 1
	s_waitcnt lgkmcnt(0)
	v_mfma_f32_16x16x32_bf16 v[60:63], v[88:91], v[152:155], v[60:63]
	v_mfma_f32_16x16x32_bf16 v[56:59], v[112:115], v[152:155], v[56:59]
	v_mfma_f32_16x16x32_bf16 v[44:47], v[88:91], v[174:177], v[44:47]
	v_mfma_f32_16x16x32_bf16 v[40:43], v[112:115], v[174:177], v[40:43]
	v_mfma_f32_16x16x32_bf16 v[28:31], v[88:91], v[182:185], v[28:31]
	v_mfma_f32_16x16x32_bf16 v[24:27], v[112:115], v[182:185], v[24:27]
	v_mfma_f32_16x16x32_bf16 v[12:15], v[88:91], v[190:193], v[12:15]
	v_mfma_f32_16x16x32_bf16 v[8:11], v[112:115], v[190:193], v[8:11]
	v_mfma_f32_16x16x32_bf16 v[60:63], v[100:103], v[170:173], v[60:63]
	v_mfma_f32_16x16x32_bf16 v[56:59], v[120:123], v[170:173], v[56:59]
	v_mfma_f32_16x16x32_bf16 v[44:47], v[100:103], v[178:181], v[44:47]
	v_mfma_f32_16x16x32_bf16 v[40:43], v[120:123], v[178:181], v[40:43]
	v_mfma_f32_16x16x32_bf16 v[28:31], v[100:103], v[186:189], v[28:31]
	v_mfma_f32_16x16x32_bf16 v[24:27], v[120:123], v[186:189], v[24:27]
	v_mfma_f32_16x16x32_bf16 v[12:15], v[100:103], v[194:197], v[12:15]
	v_mfma_f32_16x16x32_bf16 v[8:11], v[120:123], v[194:197], v[8:11]
	s_setprio 0
	s_setprio 1
	v_mfma_f32_16x16x32_bf16 v[52:55], v[124:127], v[152:155], v[52:55]
	v_mfma_f32_16x16x32_bf16 v[48:51], v[144:147], v[152:155], v[48:51]
	v_mfma_f32_16x16x32_bf16 v[36:39], v[124:127], v[174:177], v[36:39]
	v_mfma_f32_16x16x32_bf16 v[32:35], v[144:147], v[174:177], v[32:35]
	v_mfma_f32_16x16x32_bf16 v[20:23], v[124:127], v[182:185], v[20:23]
	v_mfma_f32_16x16x32_bf16 v[16:19], v[144:147], v[182:185], v[16:19]
	v_mfma_f32_16x16x32_bf16 v[4:7], v[124:127], v[190:193], v[4:7]
	v_mfma_f32_16x16x32_bf16 v[0:3], v[144:147], v[190:193], v[0:3]
	v_mfma_f32_16x16x32_bf16 v[52:55], v[140:143], v[170:173], v[52:55]
	v_mfma_f32_16x16x32_bf16 v[48:51], v[148:151], v[170:173], v[48:51]
	v_mfma_f32_16x16x32_bf16 v[36:39], v[140:143], v[178:181], v[36:39]
	v_mfma_f32_16x16x32_bf16 v[32:35], v[148:151], v[178:181], v[32:35]
	v_mfma_f32_16x16x32_bf16 v[20:23], v[140:143], v[186:189], v[20:23]
	v_mfma_f32_16x16x32_bf16 v[16:19], v[148:151], v[186:189], v[16:19]
	v_mfma_f32_16x16x32_bf16 v[4:7], v[140:143], v[194:197], v[4:7]
	v_mfma_f32_16x16x32_bf16 v[0:3], v[148:151], v[194:197], v[0:3]
	s_setprio 0
	s_add_i32 s54, s54, 2
	s_add_u32 s52, s52, 0x100
	s_addc_u32 s53, s53, 0
	s_add_u32 s14, s14, 0x100
	s_addc_u32 s15, s15, 0
	s_barrier
	s_branch .LBB0_751

.LBB0_751:
	v_add_u32_e32 v120, s13, v230
	v_add_u32_e32 v148, s29, v230
	ds_read_b128 v[88:91], v120
	ds_read_b128 v[100:103], v120 offset:1024
	ds_read_b128 v[112:115], v120 offset:2048
	ds_read_b128 v[120:123], v120 offset:3072
	ds_read_b128 v[124:127], v148
	ds_read_b128 v[140:143], v148 offset:1024
	ds_read_b128 v[144:147], v148 offset:2048
	ds_read_b128 v[148:151], v148 offset:3072
	s_add_u32 s16, s14, 0xfff80080
	s_addc_u32 s17, s15, -1
	s_cmp_eq_u32 s54, 28
	s_cselect_b32 s19, s7, s17
	s_cselect_b32 s18, s50, s16
	s_cselect_b32 s17, s5, s53
	s_cselect_b32 s16, s51, s52
	v_lshl_add_u64 v[206:207], s[14:15], 0, v[204:205]
	s_add_i32 m0, s34, 0xc000
	ds_read_b128 v[152:155], v232
	ds_read_b128 v[170:173], v232 offset:1024
	ds_read_b128 v[174:177], v232 offset:2048
	ds_read_b128 v[178:181], v232 offset:3072
	ds_read_b128 v[182:185], v232 offset:4096
	ds_read_b128 v[186:189], v232 offset:5120
	ds_read_b128 v[190:193], v232 offset:6144
	ds_read_b128 v[194:197], v232 offset:7168
	global_load_lds_dwordx4 v[206:207], off
	v_lshl_add_u64 v[206:207], s[14:15], 0, v[202:203]
	s_add_i32 m0, s34, 0xe000
	s_nop 0
	global_load_lds_dwordx4 v[206:207], off
	s_waitcnt vmcnt(8)
	s_waitcnt lgkmcnt(0)
	s_barrier
	s_setprio 1
	s_waitcnt lgkmcnt(0)
	v_mfma_f32_16x16x32_bf16 v[166:169], v[88:91], v[152:155], v[166:169]
	v_mfma_f32_16x16x32_bf16 v[156:159], v[112:115], v[152:155], v[156:159]
	v_mfma_f32_16x16x32_bf16 v[128:131], v[88:91], v[174:177], v[128:131]
	v_mfma_f32_16x16x32_bf16 v[116:119], v[112:115], v[174:177], v[116:119]
	v_mfma_f32_16x16x32_bf16 v[96:99], v[88:91], v[182:185], v[96:99]
	v_mfma_f32_16x16x32_bf16 v[92:95], v[112:115], v[182:185], v[92:95]
	v_mfma_f32_16x16x32_bf16 v[76:79], v[88:91], v[190:193], v[76:79]
	v_mfma_f32_16x16x32_bf16 v[72:75], v[112:115], v[190:193], v[72:75]
	v_mfma_f32_16x16x32_bf16 v[166:169], v[100:103], v[170:173], v[166:169]
	v_mfma_f32_16x16x32_bf16 v[156:159], v[120:123], v[170:173], v[156:159]
	v_mfma_f32_16x16x32_bf16 v[128:131], v[100:103], v[178:181], v[128:131]
	v_mfma_f32_16x16x32_bf16 v[116:119], v[120:123], v[178:181], v[116:119]
	v_mfma_f32_16x16x32_bf16 v[96:99], v[100:103], v[186:189], v[96:99]
	v_mfma_f32_16x16x32_bf16 v[92:95], v[120:123], v[186:189], v[92:95]
	v_mfma_f32_16x16x32_bf16 v[76:79], v[100:103], v[194:197], v[76:79]
	v_mfma_f32_16x16x32_bf16 v[72:75], v[120:123], v[194:197], v[72:75]
	s_setprio 0
	s_setprio 1
	v_mfma_f32_16x16x32_bf16 v[136:139], v[124:127], v[152:155], v[136:139]
	v_mfma_f32_16x16x32_bf16 v[132:135], v[144:147], v[152:155], v[132:135]
	v_mfma_f32_16x16x32_bf16 v[108:111], v[124:127], v[174:177], v[108:111]
	v_mfma_f32_16x16x32_bf16 v[104:107], v[144:147], v[174:177], v[104:107]
	v_mfma_f32_16x16x32_bf16 v[84:87], v[124:127], v[182:185], v[84:87]
	v_mfma_f32_16x16x32_bf16 v[80:83], v[144:147], v[182:185], v[80:83]
	v_mfma_f32_16x16x32_bf16 v[68:71], v[124:127], v[190:193], v[68:71]
	v_mfma_f32_16x16x32_bf16 v[64:67], v[144:147], v[190:193], v[64:67]
	v_mfma_f32_16x16x32_bf16 v[136:139], v[140:143], v[170:173], v[136:139]
	v_mfma_f32_16x16x32_bf16 v[132:135], v[148:151], v[170:173], v[132:135]
	v_mfma_f32_16x16x32_bf16 v[108:111], v[140:143], v[178:181], v[108:111]
	v_mfma_f32_16x16x32_bf16 v[104:107], v[148:151], v[178:181], v[104:107]
	v_mfma_f32_16x16x32_bf16 v[84:87], v[140:143], v[186:189], v[84:87]
	v_mfma_f32_16x16x32_bf16 v[80:83], v[148:151], v[186:189], v[80:83]
	v_mfma_f32_16x16x32_bf16 v[68:71], v[140:143], v[194:197], v[68:71]
	v_mfma_f32_16x16x32_bf16 v[64:67], v[148:151], v[194:197], v[64:67]
	s_setprio 0
	s_barrier
	s_mov_b32 m0, s27
	v_lshl_add_u64 v[206:207], s[16:17], 0, v[160:161]
	s_add_u32 s56, s16, 0x80000
	ds_read_b128 v[152:155], v232 offset:16384
	ds_read_b128 v[170:173], v232 offset:17408
	ds_read_b128 v[174:177], v232 offset:18432
	ds_read_b128 v[178:181], v232 offset:19456
	ds_read_b128 v[182:185], v232 offset:20480
	ds_read_b128 v[186:189], v232 offset:21504
	ds_read_b128 v[190:193], v232 offset:22528
	ds_read_b128 v[194:197], v232 offset:23552
	global_load_lds_dwordx4 v[206:207], off
	v_lshl_add_u64 v[208:209], s[16:17], 0, v[200:201]
	s_mov_b32 m0, s28
	s_addc_u32 s57, s17, 0
	global_load_lds_dwordx4 v[208:209], off
	v_lshl_add_u64 v[210:211], s[56:57], 0, v[160:161]
	s_mov_b32 m0, s30
	v_lshl_add_u64 v[212:213], s[18:19], 0, v[198:199]
	global_load_lds_dwordx4 v[210:211], off
	v_lshl_add_u64 v[210:211], s[56:57], 0, v[200:201]
	s_mov_b32 m0, s31
	s_nop 0
	global_load_lds_dwordx4 v[210:211], off
	v_lshl_add_u64 v[210:211], s[18:19], 0, v[162:163]
	s_mov_b32 m0, s34
	s_nop 0
	global_load_lds_dwordx4 v[210:211], off
	s_mov_b32 m0, s35
	s_nop 0
	global_load_lds_dwordx4 v[212:213], off
	s_waitcnt vmcnt(8)
	s_waitcnt lgkmcnt(0)
	s_barrier
	s_setprio 1
	s_waitcnt lgkmcnt(0)
	v_mfma_f32_16x16x32_bf16 v[60:63], v[88:91], v[152:155], v[60:63]
	v_mfma_f32_16x16x32_bf16 v[56:59], v[112:115], v[152:155], v[56:59]
	v_mfma_f32_16x16x32_bf16 v[44:47], v[88:91], v[174:177], v[44:47]
	v_mfma_f32_16x16x32_bf16 v[40:43], v[112:115], v[174:177], v[40:43]
	v_mfma_f32_16x16x32_bf16 v[28:31], v[88:91], v[182:185], v[28:31]
	v_mfma_f32_16x16x32_bf16 v[24:27], v[112:115], v[182:185], v[24:27]
	v_mfma_f32_16x16x32_bf16 v[12:15], v[88:91], v[190:193], v[12:15]
	v_mfma_f32_16x16x32_bf16 v[8:11], v[112:115], v[190:193], v[8:11]
	v_mfma_f32_16x16x32_bf16 v[60:63], v[100:103], v[170:173], v[60:63]
	v_mfma_f32_16x16x32_bf16 v[56:59], v[120:123], v[170:173], v[56:59]
	v_mfma_f32_16x16x32_bf16 v[44:47], v[100:103], v[178:181], v[44:47]
	v_mfma_f32_16x16x32_bf16 v[40:43], v[120:123], v[178:181], v[40:43]
	v_mfma_f32_16x16x32_bf16 v[28:31], v[100:103], v[186:189], v[28:31]
	v_mfma_f32_16x16x32_bf16 v[24:27], v[120:123], v[186:189], v[24:27]
	v_mfma_f32_16x16x32_bf16 v[12:15], v[100:103], v[194:197], v[12:15]
	v_mfma_f32_16x16x32_bf16 v[8:11], v[120:123], v[194:197], v[8:11]
	s_setprio 0
	s_setprio 1
	v_mfma_f32_16x16x32_bf16 v[52:55], v[124:127], v[152:155], v[52:55]
	v_mfma_f32_16x16x32_bf16 v[48:51], v[144:147], v[152:155], v[48:51]
	v_mfma_f32_16x16x32_bf16 v[36:39], v[124:127], v[174:177], v[36:39]
	v_mfma_f32_16x16x32_bf16 v[32:35], v[144:147], v[174:177], v[32:35]
	v_mfma_f32_16x16x32_bf16 v[20:23], v[124:127], v[182:185], v[20:23]
	v_mfma_f32_16x16x32_bf16 v[16:19], v[144:147], v[182:185], v[16:19]
	v_mfma_f32_16x16x32_bf16 v[4:7], v[124:127], v[190:193], v[4:7]
	v_mfma_f32_16x16x32_bf16 v[0:3], v[144:147], v[190:193], v[0:3]
	v_mfma_f32_16x16x32_bf16 v[52:55], v[140:143], v[170:173], v[52:55]
	v_mfma_f32_16x16x32_bf16 v[48:51], v[148:151], v[170:173], v[48:51]
	v_mfma_f32_16x16x32_bf16 v[36:39], v[140:143], v[178:181], v[36:39]
	v_mfma_f32_16x16x32_bf16 v[32:35], v[148:151], v[178:181], v[32:35]
	v_mfma_f32_16x16x32_bf16 v[20:23], v[140:143], v[186:189], v[20:23]
	v_mfma_f32_16x16x32_bf16 v[16:19], v[148:151], v[186:189], v[16:19]
	v_mfma_f32_16x16x32_bf16 v[4:7], v[140:143], v[194:197], v[4:7]
	v_mfma_f32_16x16x32_bf16 v[0:3], v[148:151], v[194:197], v[0:3]
	s_setprio 0
	s_barrier
	v_add_u32_e32 v120, s39, v230
	v_add_u32_e32 v148, s44, v230
	ds_read_b128 v[88:91], v120
	ds_read_b128 v[100:103], v120 offset:1024
	ds_read_b128 v[112:115], v120 offset:2048
	ds_read_b128 v[120:123], v120 offset:3072
	ds_read_b128 v[124:127], v148
	ds_read_b128 v[140:143], v148 offset:1024
	ds_read_b128 v[144:147], v148 offset:2048
	ds_read_b128 v[148:151], v148 offset:3072
	s_add_u32 s18, s18, 0x80000
	s_addc_u32 s19, s19, 0
	s_mov_b32 m0, s36
	v_lshl_add_u64 v[214:215], s[18:19], 0, v[162:163]
	ds_read_b128 v[152:155], v232 offset:32768
	ds_read_b128 v[170:173], v232 offset:33792
	ds_read_b128 v[174:177], v232 offset:34816
	ds_read_b128 v[178:181], v232 offset:35840
	ds_read_b128 v[182:185], v232 offset:36864
	ds_read_b128 v[186:189], v232 offset:37888
	ds_read_b128 v[190:193], v232 offset:38912
	ds_read_b128 v[194:197], v232 offset:39936
	global_load_lds_dwordx4 v[214:215], off
	v_lshl_add_u64 v[214:215], s[18:19], 0, v[198:199]
	s_mov_b32 m0, s37
	s_nop 0
	global_load_lds_dwordx4 v[214:215], off
	s_waitcnt vmcnt(8)
	s_waitcnt lgkmcnt(0)
	s_barrier
	s_setprio 1
	s_waitcnt lgkmcnt(0)
	v_mfma_f32_16x16x32_bf16 v[166:169], v[88:91], v[152:155], v[166:169]
	v_mfma_f32_16x16x32_bf16 v[156:159], v[112:115], v[152:155], v[156:159]
	v_mfma_f32_16x16x32_bf16 v[128:131], v[88:91], v[174:177], v[128:131]
	v_mfma_f32_16x16x32_bf16 v[116:119], v[112:115], v[174:177], v[116:119]
	v_mfma_f32_16x16x32_bf16 v[96:99], v[88:91], v[182:185], v[96:99]
	v_mfma_f32_16x16x32_bf16 v[92:95], v[112:115], v[182:185], v[92:95]
	v_mfma_f32_16x16x32_bf16 v[76:79], v[88:91], v[190:193], v[76:79]
	v_mfma_f32_16x16x32_bf16 v[72:75], v[112:115], v[190:193], v[72:75]
	v_mfma_f32_16x16x32_bf16 v[166:169], v[100:103], v[170:173], v[166:169]
	v_mfma_f32_16x16x32_bf16 v[156:159], v[120:123], v[170:173], v[156:159]
	v_mfma_f32_16x16x32_bf16 v[128:131], v[100:103], v[178:181], v[128:131]
	v_mfma_f32_16x16x32_bf16 v[116:119], v[120:123], v[178:181], v[116:119]
	v_mfma_f32_16x16x32_bf16 v[96:99], v[100:103], v[186:189], v[96:99]
	v_mfma_f32_16x16x32_bf16 v[92:95], v[120:123], v[186:189], v[92:95]
	v_mfma_f32_16x16x32_bf16 v[76:79], v[100:103], v[194:197], v[76:79]
	v_mfma_f32_16x16x32_bf16 v[72:75], v[120:123], v[194:197], v[72:75]
	s_setprio 0
	s_setprio 1
	v_mfma_f32_16x16x32_bf16 v[136:139], v[124:127], v[152:155], v[136:139]
	v_mfma_f32_16x16x32_bf16 v[132:135], v[144:147], v[152:155], v[132:135]
	v_mfma_f32_16x16x32_bf16 v[108:111], v[124:127], v[174:177], v[108:111]
	v_mfma_f32_16x16x32_bf16 v[104:107], v[144:147], v[174:177], v[104:107]
	v_mfma_f32_16x16x32_bf16 v[84:87], v[124:127], v[182:185], v[84:87]
	v_mfma_f32_16x16x32_bf16 v[80:83], v[144:147], v[182:185], v[80:83]
	v_mfma_f32_16x16x32_bf16 v[68:71], v[124:127], v[190:193], v[68:71]
	v_mfma_f32_16x16x32_bf16 v[64:67], v[144:147], v[190:193], v[64:67]
	v_mfma_f32_16x16x32_bf16 v[136:139], v[140:143], v[170:173], v[136:139]
	v_mfma_f32_16x16x32_bf16 v[132:135], v[148:151], v[170:173], v[132:135]
	v_mfma_f32_16x16x32_bf16 v[108:111], v[140:143], v[178:181], v[108:111]
	v_mfma_f32_16x16x32_bf16 v[104:107], v[148:151], v[178:181], v[104:107]
	v_mfma_f32_16x16x32_bf16 v[84:87], v[140:143], v[186:189], v[84:87]
	v_mfma_f32_16x16x32_bf16 v[80:83], v[148:151], v[186:189], v[80:83]
	v_mfma_f32_16x16x32_bf16 v[68:71], v[140:143], v[194:197], v[68:71]
	v_mfma_f32_16x16x32_bf16 v[64:67], v[148:151], v[194:197], v[64:67]
	s_setprio 0
	s_barrier
	s_mov_b32 m0, s40
	v_lshl_add_u64 v[206:207], v[206:207], 0, s[86:87]
	s_add_u32 s16, s16, 0x80080
	ds_read_b128 v[152:155], v232 offset:49152
	ds_read_b128 v[170:173], v232 offset:50176
	ds_read_b128 v[174:177], v232 offset:51200
	ds_read_b128 v[178:181], v232 offset:52224
	ds_read_b128 v[182:185], v232 offset:53248
	ds_read_b128 v[186:189], v232 offset:54272
	ds_read_b128 v[190:193], v232 offset:55296
	ds_read_b128 v[194:197], v232 offset:56320
	global_load_lds_dwordx4 v[206:207], off
	v_lshl_add_u64 v[206:207], v[208:209], 0, s[86:87]
	s_mov_b32 m0, s41
	s_addc_u32 s17, s17, 0
	global_load_lds_dwordx4 v[206:207], off
	v_lshl_add_u64 v[206:207], s[16:17], 0, v[160:161]
	s_mov_b32 m0, s45
	s_nop 0
	global_load_lds_dwordx4 v[206:207], off
	v_lshl_add_u64 v[206:207], s[16:17], 0, v[200:201]
	s_mov_b32 m0, s46
	s_nop 0
	global_load_lds_dwordx4 v[206:207], off
	v_lshl_add_u64 v[206:207], v[210:211], 0, s[86:87]
	s_mov_b32 m0, s42
	s_nop 0
	global_load_lds_dwordx4 v[206:207], off
	v_lshl_add_u64 v[206:207], v[212:213], 0, s[86:87]
	s_mov_b32 m0, s43
	s_nop 0
	global_load_lds_dwordx4 v[206:207], off
	s_waitcnt vmcnt(8)
	s_waitcnt lgkmcnt(0)
	s_barrier
	s_setprio 1
	s_waitcnt lgkmcnt(0)
	v_mfma_f32_16x16x32_bf16 v[60:63], v[88:91], v[152:155], v[60:63]
	v_mfma_f32_16x16x32_bf16 v[56:59], v[112:115], v[152:155], v[56:59]
	v_mfma_f32_16x16x32_bf16 v[44:47], v[88:91], v[174:177], v[44:47]
	v_mfma_f32_16x16x32_bf16 v[40:43], v[112:115], v[174:177], v[40:43]
	v_mfma_f32_16x16x32_bf16 v[28:31], v[88:91], v[182:185], v[28:31]
	v_mfma_f32_16x16x32_bf16 v[24:27], v[112:115], v[182:185], v[24:27]
	v_mfma_f32_16x16x32_bf16 v[12:15], v[88:91], v[190:193], v[12:15]
	v_mfma_f32_16x16x32_bf16 v[8:11], v[112:115], v[190:193], v[8:11]
	v_mfma_f32_16x16x32_bf16 v[60:63], v[100:103], v[170:173], v[60:63]
	v_mfma_f32_16x16x32_bf16 v[56:59], v[120:123], v[170:173], v[56:59]
	v_mfma_f32_16x16x32_bf16 v[44:47], v[100:103], v[178:181], v[44:47]
	v_mfma_f32_16x16x32_bf16 v[40:43], v[120:123], v[178:181], v[40:43]
	v_mfma_f32_16x16x32_bf16 v[28:31], v[100:103], v[186:189], v[28:31]
	v_mfma_f32_16x16x32_bf16 v[24:27], v[120:123], v[186:189], v[24:27]
	v_mfma_f32_16x16x32_bf16 v[12:15], v[100:103], v[194:197], v[12:15]
	v_mfma_f32_16x16x32_bf16 v[8:11], v[120:123], v[194:197], v[8:11]
	s_setprio 0
	s_setprio 1
	v_mfma_f32_16x16x32_bf16 v[52:55], v[124:127], v[152:155], v[52:55]
	v_mfma_f32_16x16x32_bf16 v[48:51], v[144:147], v[152:155], v[48:51]
	v_mfma_f32_16x16x32_bf16 v[36:39], v[124:127], v[174:177], v[36:39]
	v_mfma_f32_16x16x32_bf16 v[32:35], v[144:147], v[174:177], v[32:35]
	v_mfma_f32_16x16x32_bf16 v[20:23], v[124:127], v[182:185], v[20:23]
	v_mfma_f32_16x16x32_bf16 v[16:19], v[144:147], v[182:185], v[16:19]
	v_mfma_f32_16x16x32_bf16 v[4:7], v[124:127], v[190:193], v[4:7]
	v_mfma_f32_16x16x32_bf16 v[0:3], v[144:147], v[190:193], v[0:3]
	v_mfma_f32_16x16x32_bf16 v[52:55], v[140:143], v[170:173], v[52:55]
	v_mfma_f32_16x16x32_bf16 v[48:51], v[148:151], v[170:173], v[48:51]
	v_mfma_f32_16x16x32_bf16 v[36:39], v[140:143], v[178:181], v[36:39]
	v_mfma_f32_16x16x32_bf16 v[32:35], v[148:151], v[178:181], v[32:35]
	v_mfma_f32_16x16x32_bf16 v[20:23], v[140:143], v[186:189], v[20:23]
	v_mfma_f32_16x16x32_bf16 v[16:19], v[148:151], v[186:189], v[16:19]
	v_mfma_f32_16x16x32_bf16 v[4:7], v[140:143], v[194:197], v[4:7]
	v_mfma_f32_16x16x32_bf16 v[0:3], v[148:151], v[194:197], v[0:3]
	s_setprio 0
	s_add_i32 s54, s54, 2
	s_add_u32 s52, s52, 0x100
	s_addc_u32 s53, s53, 0
	s_add_u32 s14, s14, 0x100
	s_addc_u32 s15, s15, 0
	s_cmp_gt_u32 s54, 29
	s_barrier
	s_cbranch_scc0 .LBB0_751
	v_lshl_or_b32 v90, s49, 8, v231
	v_lshl_add_u32 v88, s12, 8, v165
	v_ashrrev_i32_e32 v91, 31, v90
	v_lshlrev_b64 v[206:207], 1, v[90:91]
	v_ashrrev_i32_e32 v89, 31, v88
	v_lshl_add_u64 v[90:91], s[0:1], 0, v[206:207]
	v_lshlrev_b64 v[222:223], 12, v[88:89]
	v_lshl_add_u64 v[100:101], v[90:91], 0, v[222:223]
	global_load_dwordx4 v[194:197], v[100:101], off nt
	global_load_dwordx4 v[190:193], v[100:101], off offset:256 nt
	v_or_b32_e32 v100, 16, v88
	v_ashrrev_i32_e32 v101, 31, v100
	v_lshlrev_b64 v[220:221], 12, v[100:101]
	v_lshl_add_u64 v[100:101], v[90:91], 0, v[220:221]
	global_load_dwordx4 v[186:189], v[100:101], off nt
	global_load_dwordx4 v[182:185], v[100:101], off offset:256 nt
	v_or_b32_e32 v100, 32, v88
	v_ashrrev_i32_e32 v101, 31, v100
	v_lshlrev_b64 v[218:219], 12, v[100:101]
	v_lshl_add_u64 v[100:101], v[90:91], 0, v[218:219]
	global_load_dwordx4 v[178:181], v[100:101], off nt
	global_load_dwordx4 v[174:177], v[100:101], off offset:256 nt
	v_or_b32_e32 v88, 48, v88
	v_ashrrev_i32_e32 v89, 31, v88
	v_lshlrev_b64 v[216:217], 12, v[88:89]
	v_lshl_add_u64 v[88:89], v[90:91], 0, v[216:217]
	global_load_dwordx4 v[170:173], v[88:89], off nt
	global_load_dwordx4 v[152:155], v[88:89], off offset:256 nt
	v_lshl_add_u64 v[214:215], v[222:223], 0, s[58:59]
	v_lshl_add_u64 v[88:89], v[90:91], 0, v[214:215]
	global_load_dwordx4 v[148:151], v[88:89], off nt
	global_load_dwordx4 v[144:147], v[88:89], off offset:256 nt
	s_mov_b64 s[14:15], 0x90000
	v_lshl_add_u64 v[212:213], v[222:223], 0, s[14:15]
	v_lshl_add_u64 v[88:89], v[90:91], 0, v[212:213]
	global_load_dwordx4 v[140:143], v[88:89], off nt
	global_load_dwordx4 v[124:127], v[88:89], off offset:256 nt
	s_mov_b64 s[14:15], 0xa0000
	v_lshl_add_u64 v[210:211], v[222:223], 0, s[14:15]
	v_lshl_add_u64 v[88:89], v[90:91], 0, v[210:211]
	global_load_dwordx4 v[120:123], v[88:89], off nt
	global_load_dwordx4 v[112:115], v[88:89], off offset:256 nt
	s_mov_b64 s[14:15], 0xb0000
	v_lshl_add_u64 v[208:209], v[222:223], 0, s[14:15]
	v_lshl_add_u64 v[88:89], v[90:91], 0, v[208:209]
	global_load_dwordx4 v[100:103], v[88:89], off nt
	s_nop 0
	global_load_dwordx4 v[88:91], v[88:89], off offset:256 nt
	s_and_b64 vcc, exec, s[2:3]
	s_mov_b32 s49, s4
	s_mov_b32 s12, s6
	s_mov_b64 s[14:15], s[10:11]
	s_mov_b64 s[16:17], s[8:9]
	s_waitcnt vmcnt(0)
	v_cvt_f32_f16_e32 v224, v194
	v_cvt_f32_f16_sdwa v225, v194 dst_sel:DWORD dst_unused:UNUSED_PAD src0_sel:WORD_1
	v_pk_add_f32 v[166:167], v[166:167], v[224:225]
	s_nop 0
	v_cvt_pk_f16_f32 v194, v166, v167
	v_cvt_f32_f16_e32 v166, v196
	v_cvt_f32_f16_sdwa v167, v196 dst_sel:DWORD dst_unused:UNUSED_PAD src0_sel:WORD_1
	v_pk_add_f32 v[156:157], v[156:157], v[166:167]
	s_nop 0
	v_cvt_pk_f16_f32 v196, v156, v157
	v_cvt_f32_f16_e32 v156, v195
	v_cvt_f32_f16_sdwa v157, v195 dst_sel:DWORD dst_unused:UNUSED_PAD src0_sel:WORD_1
	v_pk_add_f32 v[156:157], v[168:169], v[156:157]
	s_nop 0
	v_cvt_pk_f16_f32 v195, v156, v157
	v_cvt_f32_f16_e32 v156, v197
	v_cvt_f32_f16_sdwa v157, v197 dst_sel:DWORD dst_unused:UNUSED_PAD src0_sel:WORD_1
	v_pk_add_f32 v[156:157], v[158:159], v[156:157]
	s_nop 0
	v_cvt_pk_f16_f32 v197, v156, v157
	v_lshl_add_u64 v[156:157], s[0:1], 0, v[222:223]
	v_lshl_add_u64 v[166:167], v[156:157], 0, v[206:207]
	v_cvt_f32_f16_e32 v156, v190
	v_cvt_f32_f16_sdwa v157, v190 dst_sel:DWORD dst_unused:UNUSED_PAD src0_sel:WORD_1
	global_store_dwordx4 v[166:167], v[194:197], off
	v_pk_add_f32 v[136:137], v[136:137], v[156:157]
	s_nop 0
	v_cvt_pk_f16_f32 v156, v136, v137
	v_cvt_f32_f16_e32 v136, v192
	v_cvt_f32_f16_sdwa v137, v192 dst_sel:DWORD dst_unused:UNUSED_PAD src0_sel:WORD_1
	v_pk_add_f32 v[132:133], v[132:133], v[136:137]
	s_nop 0
	v_cvt_pk_f16_f32 v158, v132, v133
	v_cvt_f32_f16_e32 v132, v191
	v_cvt_f32_f16_sdwa v133, v191 dst_sel:DWORD dst_unused:UNUSED_PAD src0_sel:WORD_1
	v_pk_add_f32 v[132:133], v[138:139], v[132:133]
	s_nop 0
	v_cvt_pk_f16_f32 v157, v132, v133
	v_cvt_f32_f16_e32 v132, v193
	v_cvt_f32_f16_sdwa v133, v193 dst_sel:DWORD dst_unused:UNUSED_PAD src0_sel:WORD_1
	v_pk_add_f32 v[132:133], v[134:135], v[132:133]
	s_nop 0
	v_cvt_pk_f16_f32 v159, v132, v133
	v_cvt_f32_f16_e32 v132, v186
	v_cvt_f32_f16_sdwa v133, v186 dst_sel:DWORD dst_unused:UNUSED_PAD src0_sel:WORD_1
	global_store_dwordx4 v[166:167], v[156:159], off offset:256
	v_pk_add_f32 v[128:129], v[128:129], v[132:133]
	s_nop 0
	v_cvt_pk_f16_f32 v132, v128, v129
	v_cvt_f32_f16_e32 v128, v188
	v_cvt_f32_f16_sdwa v129, v188 dst_sel:DWORD dst_unused:UNUSED_PAD src0_sel:WORD_1
	v_pk_add_f32 v[116:117], v[116:117], v[128:129]
	s_nop 0
	v_cvt_pk_f16_f32 v134, v116, v117
	v_cvt_f32_f16_e32 v116, v187
	v_cvt_f32_f16_sdwa v117, v187 dst_sel:DWORD dst_unused:UNUSED_PAD src0_sel:WORD_1
	v_pk_add_f32 v[116:117], v[130:131], v[116:117]
	s_nop 0
	v_cvt_pk_f16_f32 v133, v116, v117
	v_cvt_f32_f16_e32 v116, v189
	v_cvt_f32_f16_sdwa v117, v189 dst_sel:DWORD dst_unused:UNUSED_PAD src0_sel:WORD_1
	v_pk_add_f32 v[116:117], v[118:119], v[116:117]
	s_nop 0
	v_cvt_pk_f16_f32 v135, v116, v117
	v_lshl_add_u64 v[116:117], s[0:1], 0, v[220:221]
	v_lshl_add_u64 v[128:129], v[116:117], 0, v[206:207]
	v_cvt_f32_f16_e32 v116, v182
	v_cvt_f32_f16_sdwa v117, v182 dst_sel:DWORD dst_unused:UNUSED_PAD src0_sel:WORD_1
	global_store_dwordx4 v[128:129], v[132:135], off
	v_pk_add_f32 v[108:109], v[108:109], v[116:117]
	s_nop 0
	v_cvt_pk_f16_f32 v116, v108, v109
	v_cvt_f32_f16_e32 v108, v184
	v_cvt_f32_f16_sdwa v109, v184 dst_sel:DWORD dst_unused:UNUSED_PAD src0_sel:WORD_1
	v_pk_add_f32 v[104:105], v[104:105], v[108:109]
	s_nop 0
	v_cvt_pk_f16_f32 v118, v104, v105
	v_cvt_f32_f16_e32 v104, v183
	v_cvt_f32_f16_sdwa v105, v183 dst_sel:DWORD dst_unused:UNUSED_PAD src0_sel:WORD_1
	v_pk_add_f32 v[104:105], v[110:111], v[104:105]
	s_nop 0
	v_cvt_pk_f16_f32 v117, v104, v105
	v_cvt_f32_f16_e32 v104, v185
	v_cvt_f32_f16_sdwa v105, v185 dst_sel:DWORD dst_unused:UNUSED_PAD src0_sel:WORD_1
	v_pk_add_f32 v[104:105], v[106:107], v[104:105]
	s_nop 0
	v_cvt_pk_f16_f32 v119, v104, v105
	v_cvt_f32_f16_e32 v104, v178
	v_cvt_f32_f16_sdwa v105, v178 dst_sel:DWORD dst_unused:UNUSED_PAD src0_sel:WORD_1
	global_store_dwordx4 v[128:129], v[116:119], off offset:256
	v_pk_add_f32 v[96:97], v[96:97], v[104:105]
	s_nop 0
	v_cvt_pk_f16_f32 v104, v96, v97
	v_cvt_f32_f16_e32 v96, v180
	v_cvt_f32_f16_sdwa v97, v180 dst_sel:DWORD dst_unused:UNUSED_PAD src0_sel:WORD_1
	v_pk_add_f32 v[92:93], v[92:93], v[96:97]
	s_nop 0
	v_cvt_pk_f16_f32 v106, v92, v93
	v_cvt_f32_f16_e32 v92, v179
	v_cvt_f32_f16_sdwa v93, v179 dst_sel:DWORD dst_unused:UNUSED_PAD src0_sel:WORD_1
	v_pk_add_f32 v[92:93], v[98:99], v[92:93]
	s_nop 0
	v_cvt_pk_f16_f32 v105, v92, v93
	v_cvt_f32_f16_e32 v92, v181
	v_cvt_f32_f16_sdwa v93, v181 dst_sel:DWORD dst_unused:UNUSED_PAD src0_sel:WORD_1
	v_pk_add_f32 v[92:93], v[94:95], v[92:93]
	s_nop 0
	v_cvt_pk_f16_f32 v107, v92, v93
	v_lshl_add_u64 v[92:93], s[0:1], 0, v[218:219]
	v_lshl_add_u64 v[96:97], v[92:93], 0, v[206:207]
	v_cvt_f32_f16_e32 v92, v174
	v_cvt_f32_f16_sdwa v93, v174 dst_sel:DWORD dst_unused:UNUSED_PAD src0_sel:WORD_1
	global_store_dwordx4 v[96:97], v[104:107], off
	v_pk_add_f32 v[84:85], v[84:85], v[92:93]
	s_nop 0
	v_cvt_pk_f16_f32 v92, v84, v85
	v_cvt_f32_f16_e32 v84, v176
	v_cvt_f32_f16_sdwa v85, v176 dst_sel:DWORD dst_unused:UNUSED_PAD src0_sel:WORD_1
	v_pk_add_f32 v[80:81], v[80:81], v[84:85]
	s_nop 0
	v_cvt_pk_f16_f32 v94, v80, v81
	v_cvt_f32_f16_e32 v80, v175
	v_cvt_f32_f16_sdwa v81, v175 dst_sel:DWORD dst_unused:UNUSED_PAD src0_sel:WORD_1
	v_pk_add_f32 v[80:81], v[86:87], v[80:81]
	s_nop 0
	v_cvt_pk_f16_f32 v93, v80, v81
	v_cvt_f32_f16_e32 v80, v177
	v_cvt_f32_f16_sdwa v81, v177 dst_sel:DWORD dst_unused:UNUSED_PAD src0_sel:WORD_1
	v_pk_add_f32 v[80:81], v[82:83], v[80:81]
	s_nop 0
	v_cvt_pk_f16_f32 v95, v80, v81
	v_cvt_f32_f16_e32 v80, v170
	v_cvt_f32_f16_sdwa v81, v170 dst_sel:DWORD dst_unused:UNUSED_PAD src0_sel:WORD_1
	global_store_dwordx4 v[96:97], v[92:95], off offset:256
	v_pk_add_f32 v[76:77], v[76:77], v[80:81]
	s_nop 0
	v_cvt_pk_f16_f32 v80, v76, v77
	v_cvt_f32_f16_e32 v76, v172
	v_cvt_f32_f16_sdwa v77, v172 dst_sel:DWORD dst_unused:UNUSED_PAD src0_sel:WORD_1
	v_pk_add_f32 v[72:73], v[72:73], v[76:77]
	s_nop 0
	v_cvt_pk_f16_f32 v82, v72, v73
	v_cvt_f32_f16_e32 v72, v171
	v_cvt_f32_f16_sdwa v73, v171 dst_sel:DWORD dst_unused:UNUSED_PAD src0_sel:WORD_1
	v_pk_add_f32 v[72:73], v[78:79], v[72:73]
	s_nop 0
	v_cvt_pk_f16_f32 v81, v72, v73
	v_cvt_f32_f16_e32 v72, v173
	v_cvt_f32_f16_sdwa v73, v173 dst_sel:DWORD dst_unused:UNUSED_PAD src0_sel:WORD_1
	v_pk_add_f32 v[72:73], v[74:75], v[72:73]
	s_nop 0
	v_cvt_pk_f16_f32 v83, v72, v73
	v_lshl_add_u64 v[72:73], s[0:1], 0, v[216:217]
	v_lshl_add_u64 v[76:77], v[72:73], 0, v[206:207]
	v_cvt_f32_f16_e32 v72, v152
	v_cvt_f32_f16_sdwa v73, v152 dst_sel:DWORD dst_unused:UNUSED_PAD src0_sel:WORD_1
	global_store_dwordx4 v[76:77], v[80:83], off
	v_pk_add_f32 v[68:69], v[68:69], v[72:73]
	s_nop 0
	v_cvt_pk_f16_f32 v72, v68, v69
	v_cvt_f32_f16_e32 v68, v154
	v_cvt_f32_f16_sdwa v69, v154 dst_sel:DWORD dst_unused:UNUSED_PAD src0_sel:WORD_1
	v_pk_add_f32 v[64:65], v[64:65], v[68:69]
	s_nop 0
	v_cvt_pk_f16_f32 v74, v64, v65
	v_cvt_f32_f16_e32 v64, v153
	v_cvt_f32_f16_sdwa v65, v153 dst_sel:DWORD dst_unused:UNUSED_PAD src0_sel:WORD_1
	v_pk_add_f32 v[64:65], v[70:71], v[64:65]
	s_nop 0
	v_cvt_pk_f16_f32 v73, v64, v65
	v_cvt_f32_f16_e32 v64, v155
	v_cvt_f32_f16_sdwa v65, v155 dst_sel:DWORD dst_unused:UNUSED_PAD src0_sel:WORD_1
	v_pk_add_f32 v[64:65], v[66:67], v[64:65]
	s_nop 0
	v_cvt_pk_f16_f32 v75, v64, v65
	v_cvt_f32_f16_e32 v64, v148
	v_cvt_f32_f16_sdwa v65, v148 dst_sel:DWORD dst_unused:UNUSED_PAD src0_sel:WORD_1
	global_store_dwordx4 v[76:77], v[72:75], off offset:256
	v_pk_add_f32 v[60:61], v[60:61], v[64:65]
	s_nop 0
	v_cvt_pk_f16_f32 v64, v60, v61
	v_cvt_f32_f16_e32 v60, v150
	v_cvt_f32_f16_sdwa v61, v150 dst_sel:DWORD dst_unused:UNUSED_PAD src0_sel:WORD_1
	v_pk_add_f32 v[56:57], v[56:57], v[60:61]
	s_nop 0
	v_cvt_pk_f16_f32 v66, v56, v57
	v_cvt_f32_f16_e32 v56, v149
	v_cvt_f32_f16_sdwa v57, v149 dst_sel:DWORD dst_unused:UNUSED_PAD src0_sel:WORD_1
	v_pk_add_f32 v[56:57], v[62:63], v[56:57]
	s_nop 0
	v_cvt_pk_f16_f32 v65, v56, v57
	v_cvt_f32_f16_e32 v56, v151
	v_cvt_f32_f16_sdwa v57, v151 dst_sel:DWORD dst_unused:UNUSED_PAD src0_sel:WORD_1
	v_pk_add_f32 v[56:57], v[58:59], v[56:57]
	s_nop 0
	v_cvt_pk_f16_f32 v67, v56, v57
	v_lshl_add_u64 v[56:57], s[0:1], 0, v[214:215]
	v_lshl_add_u64 v[60:61], v[56:57], 0, v[206:207]
	v_cvt_f32_f16_e32 v56, v144
	v_cvt_f32_f16_sdwa v57, v144 dst_sel:DWORD dst_unused:UNUSED_PAD src0_sel:WORD_1
	global_store_dwordx4 v[60:61], v[64:67], off
	v_pk_add_f32 v[52:53], v[52:53], v[56:57]
	s_nop 0
	v_cvt_pk_f16_f32 v56, v52, v53
	v_cvt_f32_f16_e32 v52, v146
	v_cvt_f32_f16_sdwa v53, v146 dst_sel:DWORD dst_unused:UNUSED_PAD src0_sel:WORD_1
	v_pk_add_f32 v[48:49], v[48:49], v[52:53]
	s_nop 0
	v_cvt_pk_f16_f32 v58, v48, v49
	v_cvt_f32_f16_e32 v48, v145
	v_cvt_f32_f16_sdwa v49, v145 dst_sel:DWORD dst_unused:UNUSED_PAD src0_sel:WORD_1
	v_pk_add_f32 v[48:49], v[54:55], v[48:49]
	s_nop 0
	v_cvt_pk_f16_f32 v57, v48, v49
	v_cvt_f32_f16_e32 v48, v147
	v_cvt_f32_f16_sdwa v49, v147 dst_sel:DWORD dst_unused:UNUSED_PAD src0_sel:WORD_1
	v_pk_add_f32 v[48:49], v[50:51], v[48:49]
	s_nop 0
	v_cvt_pk_f16_f32 v59, v48, v49
	v_cvt_f32_f16_e32 v48, v140
	v_cvt_f32_f16_sdwa v49, v140 dst_sel:DWORD dst_unused:UNUSED_PAD src0_sel:WORD_1
	global_store_dwordx4 v[60:61], v[56:59], off offset:256
	v_pk_add_f32 v[44:45], v[44:45], v[48:49]
	s_nop 0
	v_cvt_pk_f16_f32 v48, v44, v45
	v_cvt_f32_f16_e32 v44, v142
	v_cvt_f32_f16_sdwa v45, v142 dst_sel:DWORD dst_unused:UNUSED_PAD src0_sel:WORD_1
	v_pk_add_f32 v[40:41], v[40:41], v[44:45]
	s_nop 0
	v_cvt_pk_f16_f32 v50, v40, v41
	v_cvt_f32_f16_e32 v40, v141
	v_cvt_f32_f16_sdwa v41, v141 dst_sel:DWORD dst_unused:UNUSED_PAD src0_sel:WORD_1
	v_pk_add_f32 v[40:41], v[46:47], v[40:41]
	s_nop 0
	v_cvt_pk_f16_f32 v49, v40, v41
	v_cvt_f32_f16_e32 v40, v143
	v_cvt_f32_f16_sdwa v41, v143 dst_sel:DWORD dst_unused:UNUSED_PAD src0_sel:WORD_1
	v_pk_add_f32 v[40:41], v[42:43], v[40:41]
	s_nop 0
	v_cvt_pk_f16_f32 v51, v40, v41
	v_lshl_add_u64 v[40:41], s[0:1], 0, v[212:213]
	v_lshl_add_u64 v[44:45], v[40:41], 0, v[206:207]
	v_cvt_f32_f16_e32 v40, v124
	v_cvt_f32_f16_sdwa v41, v124 dst_sel:DWORD dst_unused:UNUSED_PAD src0_sel:WORD_1
	global_store_dwordx4 v[44:45], v[48:51], off
	v_pk_add_f32 v[36:37], v[36:37], v[40:41]
	s_nop 0
	v_cvt_pk_f16_f32 v40, v36, v37
	v_cvt_f32_f16_e32 v36, v126
	v_cvt_f32_f16_sdwa v37, v126 dst_sel:DWORD dst_unused:UNUSED_PAD src0_sel:WORD_1
	v_pk_add_f32 v[32:33], v[32:33], v[36:37]
	s_nop 0
	v_cvt_pk_f16_f32 v42, v32, v33
	v_cvt_f32_f16_e32 v32, v125
	v_cvt_f32_f16_sdwa v33, v125 dst_sel:DWORD dst_unused:UNUSED_PAD src0_sel:WORD_1
	v_pk_add_f32 v[32:33], v[38:39], v[32:33]
	s_nop 0
	v_cvt_pk_f16_f32 v41, v32, v33
	v_cvt_f32_f16_e32 v32, v127
	v_cvt_f32_f16_sdwa v33, v127 dst_sel:DWORD dst_unused:UNUSED_PAD src0_sel:WORD_1
	v_pk_add_f32 v[32:33], v[34:35], v[32:33]
	s_nop 0
	v_cvt_pk_f16_f32 v43, v32, v33
	v_cvt_f32_f16_e32 v32, v120
	v_cvt_f32_f16_sdwa v33, v120 dst_sel:DWORD dst_unused:UNUSED_PAD src0_sel:WORD_1
	global_store_dwordx4 v[44:45], v[40:43], off offset:256
	v_pk_add_f32 v[28:29], v[28:29], v[32:33]
	s_nop 0
	v_cvt_pk_f16_f32 v32, v28, v29
	v_cvt_f32_f16_e32 v28, v122
	v_cvt_f32_f16_sdwa v29, v122 dst_sel:DWORD dst_unused:UNUSED_PAD src0_sel:WORD_1
	v_pk_add_f32 v[24:25], v[24:25], v[28:29]
	s_nop 0
	v_cvt_pk_f16_f32 v34, v24, v25
	v_cvt_f32_f16_e32 v24, v121
	v_cvt_f32_f16_sdwa v25, v121 dst_sel:DWORD dst_unused:UNUSED_PAD src0_sel:WORD_1
	v_pk_add_f32 v[24:25], v[30:31], v[24:25]
	s_nop 0
	v_cvt_pk_f16_f32 v33, v24, v25
	v_cvt_f32_f16_e32 v24, v123
	v_cvt_f32_f16_sdwa v25, v123 dst_sel:DWORD dst_unused:UNUSED_PAD src0_sel:WORD_1
	v_pk_add_f32 v[24:25], v[26:27], v[24:25]
	s_nop 0
	v_cvt_pk_f16_f32 v35, v24, v25
	v_lshl_add_u64 v[24:25], s[0:1], 0, v[210:211]
	v_lshl_add_u64 v[28:29], v[24:25], 0, v[206:207]
	v_cvt_f32_f16_e32 v24, v112
	v_cvt_f32_f16_sdwa v25, v112 dst_sel:DWORD dst_unused:UNUSED_PAD src0_sel:WORD_1
	global_store_dwordx4 v[28:29], v[32:35], off
	v_pk_add_f32 v[20:21], v[20:21], v[24:25]
	s_nop 0
	v_cvt_pk_f16_f32 v24, v20, v21
	v_cvt_f32_f16_e32 v20, v114
	v_cvt_f32_f16_sdwa v21, v114 dst_sel:DWORD dst_unused:UNUSED_PAD src0_sel:WORD_1
	v_pk_add_f32 v[16:17], v[16:17], v[20:21]
	s_nop 0
	v_cvt_pk_f16_f32 v26, v16, v17
	v_cvt_f32_f16_e32 v16, v113
	v_cvt_f32_f16_sdwa v17, v113 dst_sel:DWORD dst_unused:UNUSED_PAD src0_sel:WORD_1
	v_pk_add_f32 v[16:17], v[22:23], v[16:17]
	s_nop 0
	v_cvt_pk_f16_f32 v25, v16, v17
	v_cvt_f32_f16_e32 v16, v115
	v_cvt_f32_f16_sdwa v17, v115 dst_sel:DWORD dst_unused:UNUSED_PAD src0_sel:WORD_1
	v_pk_add_f32 v[16:17], v[18:19], v[16:17]
	s_nop 0
	v_cvt_pk_f16_f32 v27, v16, v17
	v_cvt_f32_f16_e32 v16, v100
	v_cvt_f32_f16_sdwa v17, v100 dst_sel:DWORD dst_unused:UNUSED_PAD src0_sel:WORD_1
	global_store_dwordx4 v[28:29], v[24:27], off offset:256
	v_pk_add_f32 v[12:13], v[12:13], v[16:17]
	s_nop 0
	v_cvt_pk_f16_f32 v16, v12, v13
	v_cvt_f32_f16_e32 v12, v102
	v_cvt_f32_f16_sdwa v13, v102 dst_sel:DWORD dst_unused:UNUSED_PAD src0_sel:WORD_1
	v_pk_add_f32 v[8:9], v[8:9], v[12:13]
	s_nop 0
	v_cvt_pk_f16_f32 v18, v8, v9
	v_cvt_f32_f16_e32 v8, v101
	v_cvt_f32_f16_sdwa v9, v101 dst_sel:DWORD dst_unused:UNUSED_PAD src0_sel:WORD_1
	v_pk_add_f32 v[8:9], v[14:15], v[8:9]
	s_nop 0
	v_cvt_pk_f16_f32 v17, v8, v9
	v_cvt_f32_f16_e32 v8, v103
	v_cvt_f32_f16_sdwa v9, v103 dst_sel:DWORD dst_unused:UNUSED_PAD src0_sel:WORD_1
	v_pk_add_f32 v[8:9], v[10:11], v[8:9]
	s_nop 0
	v_cvt_pk_f16_f32 v19, v8, v9
	v_lshl_add_u64 v[8:9], s[0:1], 0, v[208:209]
	v_lshl_add_u64 v[12:13], v[8:9], 0, v[206:207]
	v_cvt_f32_f16_e32 v8, v88
	v_cvt_f32_f16_sdwa v9, v88 dst_sel:DWORD dst_unused:UNUSED_PAD src0_sel:WORD_1
	global_store_dwordx4 v[12:13], v[16:19], off
	v_pk_add_f32 v[4:5], v[4:5], v[8:9]
	s_nop 0
	v_cvt_pk_f16_f32 v8, v4, v5
	v_cvt_f32_f16_e32 v4, v90
	v_cvt_f32_f16_sdwa v5, v90 dst_sel:DWORD dst_unused:UNUSED_PAD src0_sel:WORD_1
	v_pk_add_f32 v[0:1], v[0:1], v[4:5]
	s_nop 0
	v_cvt_pk_f16_f32 v10, v0, v1
	v_cvt_f32_f16_e32 v0, v89
	v_cvt_f32_f16_sdwa v1, v89 dst_sel:DWORD dst_unused:UNUSED_PAD src0_sel:WORD_1
	v_pk_add_f32 v[0:1], v[6:7], v[0:1]
	s_nop 0
	v_cvt_pk_f16_f32 v9, v0, v1
	v_cvt_f32_f16_e32 v0, v91
	v_cvt_f32_f16_sdwa v1, v91 dst_sel:DWORD dst_unused:UNUSED_PAD src0_sel:WORD_1
	v_pk_add_f32 v[0:1], v[2:3], v[0:1]
	s_nop 0
	v_cvt_pk_f16_f32 v11, v0, v1
	global_store_dwordx4 v[12:13], v[8:11], off offset:256
	s_cbranch_vccz .LBB0_744
	s_waitcnt vmcnt(0)
	s_cmpk_gt_u32 s21, 0xff
	s_cbranch_scc1 .LBB0_755
	s_barrier

.LBB0_855:
	s_ashr_i32 s11, s10, 31
	s_lshl_b64 s[12:13], s[10:11], 20
	s_add_u32 s12, s25, s12
	s_addc_u32 s13, s26, s13
	s_and_b64 s[14:15], s[2:3], exec
	s_cselect_b32 s11, s13, s21
	s_cselect_b32 s53, s12, s20
	s_ashr_i32 s9, s8, 31
	s_lshl_b64 s[14:15], s[8:9], 20
	s_add_u32 s14, s27, s14
	s_addc_u32 s15, s28, s15
	s_and_b64 s[22:23], s[2:3], exec
	s_cselect_b32 s9, s15, s19
	s_cselect_b32 s54, s14, s18
	s_add_u32 s55, s18, 0x100
	s_addc_u32 s56, s19, 0
	s_add_u32 s18, s20, 0x80080
	v_mov_b32_e32 v0, 0
	s_addc_u32 s19, s21, 0
	s_mov_b32 s57, -2
	s_cmp_eq_u32 s52, 1
	s_cbranch_scc1 .Lpeel_zero_P7
	v_add_u32_e32 v154, s30, v139
	v_add_u32_e32 v158, s35, v139
	ds_read_b128 v[142:145], v154
	ds_read_b128 v[146:149], v154 offset:1024
	ds_read_b128 v[150:153], v154 offset:2048
	ds_read_b128 v[154:157], v154 offset:3072
	ds_read_b128 v[166:169], v158
	ds_read_b128 v[170:173], v158 offset:1024
	ds_read_b128 v[174:177], v158 offset:2048
	ds_read_b128 v[178:181], v158 offset:3072
	s_add_u32 s20, s18, 0xfff80080
	s_addc_u32 s21, s19, -1
	s_cmp_eq_u32 s57, 28
	s_cselect_b32 s23, s11, s21
	s_cselect_b32 s22, s53, s20
	s_cselect_b32 s21, s9, s56
	s_cselect_b32 s20, s54, s55
	v_lshl_add_u64 v[158:159], s[18:19], 0, v[136:137]
	s_add_i32 m0, s38, 0xc000
	ds_read_b128 v[182:185], v141
	ds_read_b128 v[186:189], v141 offset:1024
	ds_read_b128 v[190:193], v141 offset:2048
	ds_read_b128 v[194:197], v141 offset:3072
	ds_read_b128 v[198:201], v141 offset:4096
	ds_read_b128 v[202:205], v141 offset:5120
	ds_read_b128 v[206:209], v141 offset:6144
	ds_read_b128 v[210:213], v141 offset:7168
	global_load_lds_dwordx4 v[158:159], off
	v_lshl_add_u64 v[158:159], s[18:19], 0, v[134:135]
	s_add_i32 m0, s38, 0xe000
	s_nop 0
	global_load_lds_dwordx4 v[158:159], off
	s_waitcnt vmcnt(16)
	s_waitcnt lgkmcnt(0)
	s_barrier
	s_setprio 1
	s_waitcnt lgkmcnt(0)
	v_mfma_f32_16x16x32_bf16 v[124:127], v[142:145], v[182:185], 0
	v_mfma_f32_16x16x32_bf16 v[116:119], v[150:153], v[182:185], 0
	v_mfma_f32_16x16x32_bf16 v[108:111], v[142:145], v[190:193], 0
	v_mfma_f32_16x16x32_bf16 v[100:103], v[150:153], v[190:193], 0
	v_mfma_f32_16x16x32_bf16 v[92:95], v[142:145], v[198:201], 0
	v_mfma_f32_16x16x32_bf16 v[84:87], v[150:153], v[198:201], 0
	v_mfma_f32_16x16x32_bf16 v[76:79], v[142:145], v[206:209], 0
	v_mfma_f32_16x16x32_bf16 v[68:71], v[150:153], v[206:209], 0
	v_mfma_f32_16x16x32_bf16 v[124:127], v[146:149], v[186:189], v[124:127]
	v_mfma_f32_16x16x32_bf16 v[116:119], v[154:157], v[186:189], v[116:119]
	v_mfma_f32_16x16x32_bf16 v[108:111], v[146:149], v[194:197], v[108:111]
	v_mfma_f32_16x16x32_bf16 v[100:103], v[154:157], v[194:197], v[100:103]
	v_mfma_f32_16x16x32_bf16 v[92:95], v[146:149], v[202:205], v[92:95]
	v_mfma_f32_16x16x32_bf16 v[84:87], v[154:157], v[202:205], v[84:87]
	v_mfma_f32_16x16x32_bf16 v[76:79], v[146:149], v[210:213], v[76:79]
	v_mfma_f32_16x16x32_bf16 v[68:71], v[154:157], v[210:213], v[68:71]
	s_setprio 0
	s_setprio 1
	v_mfma_f32_16x16x32_bf16 v[120:123], v[166:169], v[182:185], 0
	v_mfma_f32_16x16x32_bf16 v[112:115], v[174:177], v[182:185], 0
	v_mfma_f32_16x16x32_bf16 v[104:107], v[166:169], v[190:193], 0
	v_mfma_f32_16x16x32_bf16 v[96:99], v[174:177], v[190:193], 0
	v_mfma_f32_16x16x32_bf16 v[88:91], v[166:169], v[198:201], 0
	v_mfma_f32_16x16x32_bf16 v[80:83], v[174:177], v[198:201], 0
	v_mfma_f32_16x16x32_bf16 v[72:75], v[166:169], v[206:209], 0
	v_mfma_f32_16x16x32_bf16 v[64:67], v[174:177], v[206:209], 0
	v_mfma_f32_16x16x32_bf16 v[120:123], v[170:173], v[186:189], v[120:123]
	v_mfma_f32_16x16x32_bf16 v[112:115], v[178:181], v[186:189], v[112:115]
	v_mfma_f32_16x16x32_bf16 v[104:107], v[170:173], v[194:197], v[104:107]
	v_mfma_f32_16x16x32_bf16 v[96:99], v[178:181], v[194:197], v[96:99]
	v_mfma_f32_16x16x32_bf16 v[88:91], v[170:173], v[202:205], v[88:91]
	v_mfma_f32_16x16x32_bf16 v[80:83], v[178:181], v[202:205], v[80:83]
	v_mfma_f32_16x16x32_bf16 v[72:75], v[170:173], v[210:213], v[72:75]
	v_mfma_f32_16x16x32_bf16 v[64:67], v[178:181], v[210:213], v[64:67]
	s_setprio 0
	s_barrier
	s_mov_b32 m0, s31
	v_lshl_add_u64 v[158:159], s[20:21], 0, v[160:161]
	s_add_u32 s58, s20, 0x80000
	ds_read_b128 v[182:185], v141 offset:16384
	ds_read_b128 v[186:189], v141 offset:17408
	ds_read_b128 v[190:193], v141 offset:18432
	ds_read_b128 v[194:197], v141 offset:19456
	ds_read_b128 v[198:201], v141 offset:20480
	ds_read_b128 v[202:205], v141 offset:21504
	ds_read_b128 v[206:209], v141 offset:22528
	ds_read_b128 v[210:213], v141 offset:23552
	global_load_lds_dwordx4 v[158:159], off
	v_lshl_add_u64 v[162:163], s[20:21], 0, v[128:129]
	s_mov_b32 m0, s34
	s_addc_u32 s59, s21, 0
	global_load_lds_dwordx4 v[162:163], off
	v_lshl_add_u64 v[214:215], s[58:59], 0, v[160:161]
	s_mov_b32 m0, s36
	v_lshl_add_u64 v[216:217], s[22:23], 0, v[130:131]
	global_load_lds_dwordx4 v[214:215], off
	v_lshl_add_u64 v[214:215], s[58:59], 0, v[128:129]
	s_mov_b32 m0, s37
	s_nop 0
	global_load_lds_dwordx4 v[214:215], off
	v_lshl_add_u64 v[214:215], s[22:23], 0, v[132:133]
	s_mov_b32 m0, s38
	s_nop 0
	global_load_lds_dwordx4 v[214:215], off
	s_mov_b32 m0, s39
	s_nop 0
	global_load_lds_dwordx4 v[216:217], off
	s_waitcnt vmcnt(16)
	s_waitcnt lgkmcnt(0)
	s_barrier
	s_setprio 1
	s_waitcnt lgkmcnt(0)
	v_mfma_f32_16x16x32_bf16 v[60:63], v[142:145], v[182:185], 0
	v_mfma_f32_16x16x32_bf16 v[52:55], v[150:153], v[182:185], 0
	v_mfma_f32_16x16x32_bf16 v[44:47], v[142:145], v[190:193], 0
	v_mfma_f32_16x16x32_bf16 v[36:39], v[150:153], v[190:193], 0
	v_mfma_f32_16x16x32_bf16 v[28:31], v[142:145], v[198:201], 0
	v_mfma_f32_16x16x32_bf16 v[20:23], v[150:153], v[198:201], 0
	v_mfma_f32_16x16x32_bf16 v[12:15], v[142:145], v[206:209], 0
	v_mfma_f32_16x16x32_bf16 v[4:7], v[150:153], v[206:209], 0
	v_mfma_f32_16x16x32_bf16 v[60:63], v[146:149], v[186:189], v[60:63]
	v_mfma_f32_16x16x32_bf16 v[52:55], v[154:157], v[186:189], v[52:55]
	v_mfma_f32_16x16x32_bf16 v[44:47], v[146:149], v[194:197], v[44:47]
	v_mfma_f32_16x16x32_bf16 v[36:39], v[154:157], v[194:197], v[36:39]
	v_mfma_f32_16x16x32_bf16 v[28:31], v[146:149], v[202:205], v[28:31]
	v_mfma_f32_16x16x32_bf16 v[20:23], v[154:157], v[202:205], v[20:23]
	v_mfma_f32_16x16x32_bf16 v[12:15], v[146:149], v[210:213], v[12:15]
	v_mfma_f32_16x16x32_bf16 v[4:7], v[154:157], v[210:213], v[4:7]
	s_setprio 0
	s_setprio 1
	v_mfma_f32_16x16x32_bf16 v[56:59], v[166:169], v[182:185], 0
	v_mfma_f32_16x16x32_bf16 v[48:51], v[174:177], v[182:185], 0
	v_mfma_f32_16x16x32_bf16 v[40:43], v[166:169], v[190:193], 0
	v_mfma_f32_16x16x32_bf16 v[32:35], v[174:177], v[190:193], 0
	v_mfma_f32_16x16x32_bf16 v[24:27], v[166:169], v[198:201], 0
	v_mfma_f32_16x16x32_bf16 v[16:19], v[174:177], v[198:201], 0
	v_mfma_f32_16x16x32_bf16 v[8:11], v[166:169], v[206:209], 0
	v_mfma_f32_16x16x32_bf16 v[0:3], v[174:177], v[206:209], 0
	v_mfma_f32_16x16x32_bf16 v[56:59], v[170:173], v[186:189], v[56:59]
	v_mfma_f32_16x16x32_bf16 v[48:51], v[178:181], v[186:189], v[48:51]
	v_mfma_f32_16x16x32_bf16 v[40:43], v[170:173], v[194:197], v[40:43]
	v_mfma_f32_16x16x32_bf16 v[32:35], v[178:181], v[194:197], v[32:35]
	v_mfma_f32_16x16x32_bf16 v[24:27], v[170:173], v[202:205], v[24:27]
	v_mfma_f32_16x16x32_bf16 v[16:19], v[178:181], v[202:205], v[16:19]
	v_mfma_f32_16x16x32_bf16 v[8:11], v[170:173], v[210:213], v[8:11]
	v_mfma_f32_16x16x32_bf16 v[0:3], v[178:181], v[210:213], v[0:3]
	s_setprio 0
	s_barrier
	v_add_u32_e32 v154, s43, v139
	v_add_u32_e32 v165, s48, v139
	ds_read_b128 v[142:145], v154
	ds_read_b128 v[146:149], v154 offset:1024
	ds_read_b128 v[150:153], v154 offset:2048
	ds_read_b128 v[154:157], v154 offset:3072
	ds_read_b128 v[166:169], v165
	ds_read_b128 v[170:173], v165 offset:1024
	ds_read_b128 v[174:177], v165 offset:2048
	ds_read_b128 v[178:181], v165 offset:3072
	s_add_u32 s22, s22, 0x80000
	s_addc_u32 s23, s23, 0
	s_mov_b32 m0, s40
	v_lshl_add_u64 v[218:219], s[22:23], 0, v[132:133]
	ds_read_b128 v[182:185], v141 offset:32768
	ds_read_b128 v[186:189], v141 offset:33792
	ds_read_b128 v[190:193], v141 offset:34816
	ds_read_b128 v[194:197], v141 offset:35840
	ds_read_b128 v[198:201], v141 offset:36864
	ds_read_b128 v[202:205], v141 offset:37888
	ds_read_b128 v[206:209], v141 offset:38912
	ds_read_b128 v[210:213], v141 offset:39936
	global_load_lds_dwordx4 v[218:219], off
	v_lshl_add_u64 v[218:219], s[22:23], 0, v[130:131]
	s_mov_b32 m0, s41
	s_nop 0
	global_load_lds_dwordx4 v[218:219], off
	s_waitcnt vmcnt(8)
	s_waitcnt lgkmcnt(0)
	s_barrier
	s_setprio 1
	s_waitcnt lgkmcnt(0)
	v_mfma_f32_16x16x32_bf16 v[124:127], v[142:145], v[182:185], v[124:127]
	v_mfma_f32_16x16x32_bf16 v[116:119], v[150:153], v[182:185], v[116:119]
	v_mfma_f32_16x16x32_bf16 v[108:111], v[142:145], v[190:193], v[108:111]
	v_mfma_f32_16x16x32_bf16 v[100:103], v[150:153], v[190:193], v[100:103]
	v_mfma_f32_16x16x32_bf16 v[92:95], v[142:145], v[198:201], v[92:95]
	v_mfma_f32_16x16x32_bf16 v[84:87], v[150:153], v[198:201], v[84:87]
	v_mfma_f32_16x16x32_bf16 v[76:79], v[142:145], v[206:209], v[76:79]
	v_mfma_f32_16x16x32_bf16 v[68:71], v[150:153], v[206:209], v[68:71]
	v_mfma_f32_16x16x32_bf16 v[124:127], v[146:149], v[186:189], v[124:127]
	v_mfma_f32_16x16x32_bf16 v[116:119], v[154:157], v[186:189], v[116:119]
	v_mfma_f32_16x16x32_bf16 v[108:111], v[146:149], v[194:197], v[108:111]
	v_mfma_f32_16x16x32_bf16 v[100:103], v[154:157], v[194:197], v[100:103]
	v_mfma_f32_16x16x32_bf16 v[92:95], v[146:149], v[202:205], v[92:95]
	v_mfma_f32_16x16x32_bf16 v[84:87], v[154:157], v[202:205], v[84:87]
	v_mfma_f32_16x16x32_bf16 v[76:79], v[146:149], v[210:213], v[76:79]
	v_mfma_f32_16x16x32_bf16 v[68:71], v[154:157], v[210:213], v[68:71]
	s_setprio 0
	s_setprio 1
	v_mfma_f32_16x16x32_bf16 v[120:123], v[166:169], v[182:185], v[120:123]
	v_mfma_f32_16x16x32_bf16 v[112:115], v[174:177], v[182:185], v[112:115]
	v_mfma_f32_16x16x32_bf16 v[104:107], v[166:169], v[190:193], v[104:107]
	v_mfma_f32_16x16x32_bf16 v[96:99], v[174:177], v[190:193], v[96:99]
	v_mfma_f32_16x16x32_bf16 v[88:91], v[166:169], v[198:201], v[88:91]
	v_mfma_f32_16x16x32_bf16 v[80:83], v[174:177], v[198:201], v[80:83]
	v_mfma_f32_16x16x32_bf16 v[72:75], v[166:169], v[206:209], v[72:75]
	v_mfma_f32_16x16x32_bf16 v[64:67], v[174:177], v[206:209], v[64:67]
	v_mfma_f32_16x16x32_bf16 v[120:123], v[170:173], v[186:189], v[120:123]
	v_mfma_f32_16x16x32_bf16 v[112:115], v[178:181], v[186:189], v[112:115]
	v_mfma_f32_16x16x32_bf16 v[104:107], v[170:173], v[194:197], v[104:107]
	v_mfma_f32_16x16x32_bf16 v[96:99], v[178:181], v[194:197], v[96:99]
	v_mfma_f32_16x16x32_bf16 v[88:91], v[170:173], v[202:205], v[88:91]
	v_mfma_f32_16x16x32_bf16 v[80:83], v[178:181], v[202:205], v[80:83]
	v_mfma_f32_16x16x32_bf16 v[72:75], v[170:173], v[210:213], v[72:75]
	v_mfma_f32_16x16x32_bf16 v[64:67], v[178:181], v[210:213], v[64:67]
	s_setprio 0
	s_barrier
	s_mov_b32 m0, s44
	v_lshl_add_u64 v[158:159], v[158:159], 0, s[86:87]
	s_add_u32 s20, s20, 0x80080
	ds_read_b128 v[182:185], v141 offset:49152
	ds_read_b128 v[186:189], v141 offset:50176
	ds_read_b128 v[190:193], v141 offset:51200
	ds_read_b128 v[194:197], v141 offset:52224
	ds_read_b128 v[198:201], v141 offset:53248
	ds_read_b128 v[202:205], v141 offset:54272
	ds_read_b128 v[206:209], v141 offset:55296
	ds_read_b128 v[210:213], v141 offset:56320
	global_load_lds_dwordx4 v[158:159], off
	v_lshl_add_u64 v[158:159], v[162:163], 0, s[86:87]
	s_mov_b32 m0, s45
	s_addc_u32 s21, s21, 0
	global_load_lds_dwordx4 v[158:159], off
	v_lshl_add_u64 v[158:159], s[20:21], 0, v[160:161]
	s_mov_b32 m0, s49
	s_nop 0
	global_load_lds_dwordx4 v[158:159], off
	v_lshl_add_u64 v[158:159], s[20:21], 0, v[128:129]
	s_mov_b32 m0, s50
	s_nop 0
	global_load_lds_dwordx4 v[158:159], off
	v_lshl_add_u64 v[158:159], v[214:215], 0, s[86:87]
	s_mov_b32 m0, s46
	s_nop 0
	global_load_lds_dwordx4 v[158:159], off
	v_lshl_add_u64 v[158:159], v[216:217], 0, s[86:87]
	s_mov_b32 m0, s47
	s_nop 0
	global_load_lds_dwordx4 v[158:159], off
	s_waitcnt vmcnt(8)
	s_waitcnt lgkmcnt(0)
	s_barrier
	s_setprio 1
	s_waitcnt lgkmcnt(0)
	v_mfma_f32_16x16x32_bf16 v[60:63], v[142:145], v[182:185], v[60:63]
	v_mfma_f32_16x16x32_bf16 v[52:55], v[150:153], v[182:185], v[52:55]
	v_mfma_f32_16x16x32_bf16 v[44:47], v[142:145], v[190:193], v[44:47]
	v_mfma_f32_16x16x32_bf16 v[36:39], v[150:153], v[190:193], v[36:39]
	v_mfma_f32_16x16x32_bf16 v[28:31], v[142:145], v[198:201], v[28:31]
	v_mfma_f32_16x16x32_bf16 v[20:23], v[150:153], v[198:201], v[20:23]
	v_mfma_f32_16x16x32_bf16 v[12:15], v[142:145], v[206:209], v[12:15]
	v_mfma_f32_16x16x32_bf16 v[4:7], v[150:153], v[206:209], v[4:7]
	v_mfma_f32_16x16x32_bf16 v[60:63], v[146:149], v[186:189], v[60:63]
	v_mfma_f32_16x16x32_bf16 v[52:55], v[154:157], v[186:189], v[52:55]
	v_mfma_f32_16x16x32_bf16 v[44:47], v[146:149], v[194:197], v[44:47]
	v_mfma_f32_16x16x32_bf16 v[36:39], v[154:157], v[194:197], v[36:39]
	v_mfma_f32_16x16x32_bf16 v[28:31], v[146:149], v[202:205], v[28:31]
	v_mfma_f32_16x16x32_bf16 v[20:23], v[154:157], v[202:205], v[20:23]
	v_mfma_f32_16x16x32_bf16 v[12:15], v[146:149], v[210:213], v[12:15]
	v_mfma_f32_16x16x32_bf16 v[4:7], v[154:157], v[210:213], v[4:7]
	s_setprio 0
	s_setprio 1
	v_mfma_f32_16x16x32_bf16 v[56:59], v[166:169], v[182:185], v[56:59]
	v_mfma_f32_16x16x32_bf16 v[48:51], v[174:177], v[182:185], v[48:51]
	v_mfma_f32_16x16x32_bf16 v[40:43], v[166:169], v[190:193], v[40:43]
	v_mfma_f32_16x16x32_bf16 v[32:35], v[174:177], v[190:193], v[32:35]
	v_mfma_f32_16x16x32_bf16 v[24:27], v[166:169], v[198:201], v[24:27]
	v_mfma_f32_16x16x32_bf16 v[16:19], v[174:177], v[198:201], v[16:19]
	v_mfma_f32_16x16x32_bf16 v[8:11], v[166:169], v[206:209], v[8:11]
	v_mfma_f32_16x16x32_bf16 v[0:3], v[174:177], v[206:209], v[0:3]
	v_mfma_f32_16x16x32_bf16 v[56:59], v[170:173], v[186:189], v[56:59]
	v_mfma_f32_16x16x32_bf16 v[48:51], v[178:181], v[186:189], v[48:51]
	v_mfma_f32_16x16x32_bf16 v[40:43], v[170:173], v[194:197], v[40:43]
	v_mfma_f32_16x16x32_bf16 v[32:35], v[178:181], v[194:197], v[32:35]
	v_mfma_f32_16x16x32_bf16 v[24:27], v[170:173], v[202:205], v[24:27]
	v_mfma_f32_16x16x32_bf16 v[16:19], v[178:181], v[202:205], v[16:19]
	v_mfma_f32_16x16x32_bf16 v[8:11], v[170:173], v[210:213], v[8:11]
	v_mfma_f32_16x16x32_bf16 v[0:3], v[178:181], v[210:213], v[0:3]
	s_setprio 0
	s_add_i32 s57, s57, 2
	s_add_u32 s55, s55, 0x100
	s_addc_u32 s56, s56, 0
	s_add_u32 s18, s18, 0x100
	s_addc_u32 s19, s19, 0
	s_barrier
	s_branch .LBB0_856

.LBB0_856:
	v_add_u32_e32 v154, s30, v139
	v_add_u32_e32 v158, s35, v139
	ds_read_b128 v[142:145], v154
	ds_read_b128 v[146:149], v154 offset:1024
	ds_read_b128 v[150:153], v154 offset:2048
	ds_read_b128 v[154:157], v154 offset:3072
	ds_read_b128 v[166:169], v158
	ds_read_b128 v[170:173], v158 offset:1024
	ds_read_b128 v[174:177], v158 offset:2048
	ds_read_b128 v[178:181], v158 offset:3072
	s_add_u32 s20, s18, 0xfff80080
	s_addc_u32 s21, s19, -1
	s_cmp_eq_u32 s57, 28
	s_cselect_b32 s23, s11, s21
	s_cselect_b32 s22, s53, s20
	s_cselect_b32 s21, s9, s56
	s_cselect_b32 s20, s54, s55
	v_lshl_add_u64 v[158:159], s[18:19], 0, v[136:137]
	s_add_i32 m0, s38, 0xc000
	ds_read_b128 v[182:185], v141
	ds_read_b128 v[186:189], v141 offset:1024
	ds_read_b128 v[190:193], v141 offset:2048
	ds_read_b128 v[194:197], v141 offset:3072
	ds_read_b128 v[198:201], v141 offset:4096
	ds_read_b128 v[202:205], v141 offset:5120
	ds_read_b128 v[206:209], v141 offset:6144
	ds_read_b128 v[210:213], v141 offset:7168
	global_load_lds_dwordx4 v[158:159], off
	v_lshl_add_u64 v[158:159], s[18:19], 0, v[134:135]
	s_add_i32 m0, s38, 0xe000
	s_nop 0
	global_load_lds_dwordx4 v[158:159], off
	s_waitcnt vmcnt(8)
	s_waitcnt lgkmcnt(0)
	s_barrier
	s_setprio 1
	s_waitcnt lgkmcnt(0)
	v_mfma_f32_16x16x32_bf16 v[124:127], v[142:145], v[182:185], v[124:127]
	v_mfma_f32_16x16x32_bf16 v[116:119], v[150:153], v[182:185], v[116:119]
	v_mfma_f32_16x16x32_bf16 v[108:111], v[142:145], v[190:193], v[108:111]
	v_mfma_f32_16x16x32_bf16 v[100:103], v[150:153], v[190:193], v[100:103]
	v_mfma_f32_16x16x32_bf16 v[92:95], v[142:145], v[198:201], v[92:95]
	v_mfma_f32_16x16x32_bf16 v[84:87], v[150:153], v[198:201], v[84:87]
	v_mfma_f32_16x16x32_bf16 v[76:79], v[142:145], v[206:209], v[76:79]
	v_mfma_f32_16x16x32_bf16 v[68:71], v[150:153], v[206:209], v[68:71]
	v_mfma_f32_16x16x32_bf16 v[124:127], v[146:149], v[186:189], v[124:127]
	v_mfma_f32_16x16x32_bf16 v[116:119], v[154:157], v[186:189], v[116:119]
	v_mfma_f32_16x16x32_bf16 v[108:111], v[146:149], v[194:197], v[108:111]
	v_mfma_f32_16x16x32_bf16 v[100:103], v[154:157], v[194:197], v[100:103]
	v_mfma_f32_16x16x32_bf16 v[92:95], v[146:149], v[202:205], v[92:95]
	v_mfma_f32_16x16x32_bf16 v[84:87], v[154:157], v[202:205], v[84:87]
	v_mfma_f32_16x16x32_bf16 v[76:79], v[146:149], v[210:213], v[76:79]
	v_mfma_f32_16x16x32_bf16 v[68:71], v[154:157], v[210:213], v[68:71]
	s_setprio 0
	s_setprio 1
	v_mfma_f32_16x16x32_bf16 v[120:123], v[166:169], v[182:185], v[120:123]
	v_mfma_f32_16x16x32_bf16 v[112:115], v[174:177], v[182:185], v[112:115]
	v_mfma_f32_16x16x32_bf16 v[104:107], v[166:169], v[190:193], v[104:107]
	v_mfma_f32_16x16x32_bf16 v[96:99], v[174:177], v[190:193], v[96:99]
	v_mfma_f32_16x16x32_bf16 v[88:91], v[166:169], v[198:201], v[88:91]
	v_mfma_f32_16x16x32_bf16 v[80:83], v[174:177], v[198:201], v[80:83]
	v_mfma_f32_16x16x32_bf16 v[72:75], v[166:169], v[206:209], v[72:75]
	v_mfma_f32_16x16x32_bf16 v[64:67], v[174:177], v[206:209], v[64:67]
	v_mfma_f32_16x16x32_bf16 v[120:123], v[170:173], v[186:189], v[120:123]
	v_mfma_f32_16x16x32_bf16 v[112:115], v[178:181], v[186:189], v[112:115]
	v_mfma_f32_16x16x32_bf16 v[104:107], v[170:173], v[194:197], v[104:107]
	v_mfma_f32_16x16x32_bf16 v[96:99], v[178:181], v[194:197], v[96:99]
	v_mfma_f32_16x16x32_bf16 v[88:91], v[170:173], v[202:205], v[88:91]
	v_mfma_f32_16x16x32_bf16 v[80:83], v[178:181], v[202:205], v[80:83]
	v_mfma_f32_16x16x32_bf16 v[72:75], v[170:173], v[210:213], v[72:75]
	v_mfma_f32_16x16x32_bf16 v[64:67], v[178:181], v[210:213], v[64:67]
	s_setprio 0
	s_barrier
	s_mov_b32 m0, s31
	v_lshl_add_u64 v[158:159], s[20:21], 0, v[160:161]
	s_add_u32 s58, s20, 0x80000
	ds_read_b128 v[182:185], v141 offset:16384
	ds_read_b128 v[186:189], v141 offset:17408
	ds_read_b128 v[190:193], v141 offset:18432
	ds_read_b128 v[194:197], v141 offset:19456
	ds_read_b128 v[198:201], v141 offset:20480
	ds_read_b128 v[202:205], v141 offset:21504
	ds_read_b128 v[206:209], v141 offset:22528
	ds_read_b128 v[210:213], v141 offset:23552
	global_load_lds_dwordx4 v[158:159], off
	v_lshl_add_u64 v[162:163], s[20:21], 0, v[128:129]
	s_mov_b32 m0, s34
	s_addc_u32 s59, s21, 0
	global_load_lds_dwordx4 v[162:163], off
	v_lshl_add_u64 v[214:215], s[58:59], 0, v[160:161]
	s_mov_b32 m0, s36
	v_lshl_add_u64 v[216:217], s[22:23], 0, v[130:131]
	global_load_lds_dwordx4 v[214:215], off
	v_lshl_add_u64 v[214:215], s[58:59], 0, v[128:129]
	s_mov_b32 m0, s37
	s_nop 0
	global_load_lds_dwordx4 v[214:215], off
	v_lshl_add_u64 v[214:215], s[22:23], 0, v[132:133]
	s_mov_b32 m0, s38
	s_nop 0
	global_load_lds_dwordx4 v[214:215], off
	s_mov_b32 m0, s39
	s_nop 0
	global_load_lds_dwordx4 v[216:217], off
	s_waitcnt vmcnt(8)
	s_waitcnt lgkmcnt(0)
	s_barrier
	s_setprio 1
	s_waitcnt lgkmcnt(0)
	v_mfma_f32_16x16x32_bf16 v[60:63], v[142:145], v[182:185], v[60:63]
	v_mfma_f32_16x16x32_bf16 v[52:55], v[150:153], v[182:185], v[52:55]
	v_mfma_f32_16x16x32_bf16 v[44:47], v[142:145], v[190:193], v[44:47]
	v_mfma_f32_16x16x32_bf16 v[36:39], v[150:153], v[190:193], v[36:39]
	v_mfma_f32_16x16x32_bf16 v[28:31], v[142:145], v[198:201], v[28:31]
	v_mfma_f32_16x16x32_bf16 v[20:23], v[150:153], v[198:201], v[20:23]
	v_mfma_f32_16x16x32_bf16 v[12:15], v[142:145], v[206:209], v[12:15]
	v_mfma_f32_16x16x32_bf16 v[4:7], v[150:153], v[206:209], v[4:7]
	v_mfma_f32_16x16x32_bf16 v[60:63], v[146:149], v[186:189], v[60:63]
	v_mfma_f32_16x16x32_bf16 v[52:55], v[154:157], v[186:189], v[52:55]
	v_mfma_f32_16x16x32_bf16 v[44:47], v[146:149], v[194:197], v[44:47]
	v_mfma_f32_16x16x32_bf16 v[36:39], v[154:157], v[194:197], v[36:39]
	v_mfma_f32_16x16x32_bf16 v[28:31], v[146:149], v[202:205], v[28:31]
	v_mfma_f32_16x16x32_bf16 v[20:23], v[154:157], v[202:205], v[20:23]
	v_mfma_f32_16x16x32_bf16 v[12:15], v[146:149], v[210:213], v[12:15]
	v_mfma_f32_16x16x32_bf16 v[4:7], v[154:157], v[210:213], v[4:7]
	s_setprio 0
	s_setprio 1
	v_mfma_f32_16x16x32_bf16 v[56:59], v[166:169], v[182:185], v[56:59]
	v_mfma_f32_16x16x32_bf16 v[48:51], v[174:177], v[182:185], v[48:51]
	v_mfma_f32_16x16x32_bf16 v[40:43], v[166:169], v[190:193], v[40:43]
	v_mfma_f32_16x16x32_bf16 v[32:35], v[174:177], v[190:193], v[32:35]
	v_mfma_f32_16x16x32_bf16 v[24:27], v[166:169], v[198:201], v[24:27]
	v_mfma_f32_16x16x32_bf16 v[16:19], v[174:177], v[198:201], v[16:19]
	v_mfma_f32_16x16x32_bf16 v[8:11], v[166:169], v[206:209], v[8:11]
	v_mfma_f32_16x16x32_bf16 v[0:3], v[174:177], v[206:209], v[0:3]
	v_mfma_f32_16x16x32_bf16 v[56:59], v[170:173], v[186:189], v[56:59]
	v_mfma_f32_16x16x32_bf16 v[48:51], v[178:181], v[186:189], v[48:51]
	v_mfma_f32_16x16x32_bf16 v[40:43], v[170:173], v[194:197], v[40:43]
	v_mfma_f32_16x16x32_bf16 v[32:35], v[178:181], v[194:197], v[32:35]
	v_mfma_f32_16x16x32_bf16 v[24:27], v[170:173], v[202:205], v[24:27]
	v_mfma_f32_16x16x32_bf16 v[16:19], v[178:181], v[202:205], v[16:19]
	v_mfma_f32_16x16x32_bf16 v[8:11], v[170:173], v[210:213], v[8:11]
	v_mfma_f32_16x16x32_bf16 v[0:3], v[178:181], v[210:213], v[0:3]
	s_setprio 0
	s_barrier
	v_add_u32_e32 v154, s43, v139
	v_add_u32_e32 v165, s48, v139
	ds_read_b128 v[142:145], v154
	ds_read_b128 v[146:149], v154 offset:1024
	ds_read_b128 v[150:153], v154 offset:2048
	ds_read_b128 v[154:157], v154 offset:3072
	ds_read_b128 v[166:169], v165
	ds_read_b128 v[170:173], v165 offset:1024
	ds_read_b128 v[174:177], v165 offset:2048
	ds_read_b128 v[178:181], v165 offset:3072
	s_add_u32 s22, s22, 0x80000
	s_addc_u32 s23, s23, 0
	s_mov_b32 m0, s40
	v_lshl_add_u64 v[218:219], s[22:23], 0, v[132:133]
	ds_read_b128 v[182:185], v141 offset:32768
	ds_read_b128 v[186:189], v141 offset:33792
	ds_read_b128 v[190:193], v141 offset:34816
	ds_read_b128 v[194:197], v141 offset:35840
	ds_read_b128 v[198:201], v141 offset:36864
	ds_read_b128 v[202:205], v141 offset:37888
	ds_read_b128 v[206:209], v141 offset:38912
	ds_read_b128 v[210:213], v141 offset:39936
	global_load_lds_dwordx4 v[218:219], off
	v_lshl_add_u64 v[218:219], s[22:23], 0, v[130:131]
	s_mov_b32 m0, s41
	s_nop 0
	global_load_lds_dwordx4 v[218:219], off
	s_waitcnt vmcnt(8)
	s_waitcnt lgkmcnt(0)
	s_barrier
	s_setprio 1
	s_waitcnt lgkmcnt(0)
	v_mfma_f32_16x16x32_bf16 v[124:127], v[142:145], v[182:185], v[124:127]
	v_mfma_f32_16x16x32_bf16 v[116:119], v[150:153], v[182:185], v[116:119]
	v_mfma_f32_16x16x32_bf16 v[108:111], v[142:145], v[190:193], v[108:111]
	v_mfma_f32_16x16x32_bf16 v[100:103], v[150:153], v[190:193], v[100:103]
	v_mfma_f32_16x16x32_bf16 v[92:95], v[142:145], v[198:201], v[92:95]
	v_mfma_f32_16x16x32_bf16 v[84:87], v[150:153], v[198:201], v[84:87]
	v_mfma_f32_16x16x32_bf16 v[76:79], v[142:145], v[206:209], v[76:79]
	v_mfma_f32_16x16x32_bf16 v[68:71], v[150:153], v[206:209], v[68:71]
	v_mfma_f32_16x16x32_bf16 v[124:127], v[146:149], v[186:189], v[124:127]
	v_mfma_f32_16x16x32_bf16 v[116:119], v[154:157], v[186:189], v[116:119]
	v_mfma_f32_16x16x32_bf16 v[108:111], v[146:149], v[194:197], v[108:111]
	v_mfma_f32_16x16x32_bf16 v[100:103], v[154:157], v[194:197], v[100:103]
	v_mfma_f32_16x16x32_bf16 v[92:95], v[146:149], v[202:205], v[92:95]
	v_mfma_f32_16x16x32_bf16 v[84:87], v[154:157], v[202:205], v[84:87]
	v_mfma_f32_16x16x32_bf16 v[76:79], v[146:149], v[210:213], v[76:79]
	v_mfma_f32_16x16x32_bf16 v[68:71], v[154:157], v[210:213], v[68:71]
	s_setprio 0
	s_setprio 1
	v_mfma_f32_16x16x32_bf16 v[120:123], v[166:169], v[182:185], v[120:123]
	v_mfma_f32_16x16x32_bf16 v[112:115], v[174:177], v[182:185], v[112:115]
	v_mfma_f32_16x16x32_bf16 v[104:107], v[166:169], v[190:193], v[104:107]
	v_mfma_f32_16x16x32_bf16 v[96:99], v[174:177], v[190:193], v[96:99]
	v_mfma_f32_16x16x32_bf16 v[88:91], v[166:169], v[198:201], v[88:91]
	v_mfma_f32_16x16x32_bf16 v[80:83], v[174:177], v[198:201], v[80:83]
	v_mfma_f32_16x16x32_bf16 v[72:75], v[166:169], v[206:209], v[72:75]
	v_mfma_f32_16x16x32_bf16 v[64:67], v[174:177], v[206:209], v[64:67]
	v_mfma_f32_16x16x32_bf16 v[120:123], v[170:173], v[186:189], v[120:123]
	v_mfma_f32_16x16x32_bf16 v[112:115], v[178:181], v[186:189], v[112:115]
	v_mfma_f32_16x16x32_bf16 v[104:107], v[170:173], v[194:197], v[104:107]
	v_mfma_f32_16x16x32_bf16 v[96:99], v[178:181], v[194:197], v[96:99]
	v_mfma_f32_16x16x32_bf16 v[88:91], v[170:173], v[202:205], v[88:91]
	v_mfma_f32_16x16x32_bf16 v[80:83], v[178:181], v[202:205], v[80:83]
	v_mfma_f32_16x16x32_bf16 v[72:75], v[170:173], v[210:213], v[72:75]
	v_mfma_f32_16x16x32_bf16 v[64:67], v[178:181], v[210:213], v[64:67]
	s_setprio 0
	s_barrier
	s_mov_b32 m0, s44
	v_lshl_add_u64 v[158:159], v[158:159], 0, s[86:87]
	s_add_u32 s20, s20, 0x80080
	ds_read_b128 v[182:185], v141 offset:49152
	ds_read_b128 v[186:189], v141 offset:50176
	ds_read_b128 v[190:193], v141 offset:51200
	ds_read_b128 v[194:197], v141 offset:52224
	ds_read_b128 v[198:201], v141 offset:53248
	ds_read_b128 v[202:205], v141 offset:54272
	ds_read_b128 v[206:209], v141 offset:55296
	ds_read_b128 v[210:213], v141 offset:56320
	global_load_lds_dwordx4 v[158:159], off
	v_lshl_add_u64 v[158:159], v[162:163], 0, s[86:87]
	s_mov_b32 m0, s45
	s_addc_u32 s21, s21, 0
	global_load_lds_dwordx4 v[158:159], off
	v_lshl_add_u64 v[158:159], s[20:21], 0, v[160:161]
	s_mov_b32 m0, s49
	s_nop 0
	global_load_lds_dwordx4 v[158:159], off
	v_lshl_add_u64 v[158:159], s[20:21], 0, v[128:129]
	s_mov_b32 m0, s50
	s_nop 0
	global_load_lds_dwordx4 v[158:159], off
	v_lshl_add_u64 v[158:159], v[214:215], 0, s[86:87]
	s_mov_b32 m0, s46
	s_nop 0
	global_load_lds_dwordx4 v[158:159], off
	v_lshl_add_u64 v[158:159], v[216:217], 0, s[86:87]
	s_mov_b32 m0, s47
	s_nop 0
	global_load_lds_dwordx4 v[158:159], off
	s_waitcnt vmcnt(8)
	s_waitcnt lgkmcnt(0)
	s_barrier
	s_setprio 1
	s_waitcnt lgkmcnt(0)
	v_mfma_f32_16x16x32_bf16 v[60:63], v[142:145], v[182:185], v[60:63]
	v_mfma_f32_16x16x32_bf16 v[52:55], v[150:153], v[182:185], v[52:55]
	v_mfma_f32_16x16x32_bf16 v[44:47], v[142:145], v[190:193], v[44:47]
	v_mfma_f32_16x16x32_bf16 v[36:39], v[150:153], v[190:193], v[36:39]
	v_mfma_f32_16x16x32_bf16 v[28:31], v[142:145], v[198:201], v[28:31]
	v_mfma_f32_16x16x32_bf16 v[20:23], v[150:153], v[198:201], v[20:23]
	v_mfma_f32_16x16x32_bf16 v[12:15], v[142:145], v[206:209], v[12:15]
	v_mfma_f32_16x16x32_bf16 v[4:7], v[150:153], v[206:209], v[4:7]
	v_mfma_f32_16x16x32_bf16 v[60:63], v[146:149], v[186:189], v[60:63]
	v_mfma_f32_16x16x32_bf16 v[52:55], v[154:157], v[186:189], v[52:55]
	v_mfma_f32_16x16x32_bf16 v[44:47], v[146:149], v[194:197], v[44:47]
	v_mfma_f32_16x16x32_bf16 v[36:39], v[154:157], v[194:197], v[36:39]
	v_mfma_f32_16x16x32_bf16 v[28:31], v[146:149], v[202:205], v[28:31]
	v_mfma_f32_16x16x32_bf16 v[20:23], v[154:157], v[202:205], v[20:23]
	v_mfma_f32_16x16x32_bf16 v[12:15], v[146:149], v[210:213], v[12:15]
	v_mfma_f32_16x16x32_bf16 v[4:7], v[154:157], v[210:213], v[4:7]
	s_setprio 0
	s_setprio 1
	v_mfma_f32_16x16x32_bf16 v[56:59], v[166:169], v[182:185], v[56:59]
	v_mfma_f32_16x16x32_bf16 v[48:51], v[174:177], v[182:185], v[48:51]
	v_mfma_f32_16x16x32_bf16 v[40:43], v[166:169], v[190:193], v[40:43]
	v_mfma_f32_16x16x32_bf16 v[32:35], v[174:177], v[190:193], v[32:35]
	v_mfma_f32_16x16x32_bf16 v[24:27], v[166:169], v[198:201], v[24:27]
	v_mfma_f32_16x16x32_bf16 v[16:19], v[174:177], v[198:201], v[16:19]
	v_mfma_f32_16x16x32_bf16 v[8:11], v[166:169], v[206:209], v[8:11]
	v_mfma_f32_16x16x32_bf16 v[0:3], v[174:177], v[206:209], v[0:3]
	v_mfma_f32_16x16x32_bf16 v[56:59], v[170:173], v[186:189], v[56:59]
	v_mfma_f32_16x16x32_bf16 v[48:51], v[178:181], v[186:189], v[48:51]
	v_mfma_f32_16x16x32_bf16 v[40:43], v[170:173], v[194:197], v[40:43]
	v_mfma_f32_16x16x32_bf16 v[32:35], v[178:181], v[194:197], v[32:35]
	v_mfma_f32_16x16x32_bf16 v[24:27], v[170:173], v[202:205], v[24:27]
	v_mfma_f32_16x16x32_bf16 v[16:19], v[178:181], v[202:205], v[16:19]
	v_mfma_f32_16x16x32_bf16 v[8:11], v[170:173], v[210:213], v[8:11]
	v_mfma_f32_16x16x32_bf16 v[0:3], v[178:181], v[210:213], v[0:3]
	s_setprio 0
	s_add_i32 s57, s57, 2
	s_add_u32 s55, s55, 0x100
	s_addc_u32 s56, s56, 0
	s_add_u32 s18, s18, 0x100
	s_addc_u32 s19, s19, 0
	s_cmp_gt_u32 s57, 29
	s_barrier
	s_cbranch_scc0 .LBB0_856
	s_and_b64 vcc, exec, s[6:7]
	s_cbranch_vccz .LBB0_859
	s_barrier

.LBB0_926:
	s_add_u32 s50, s10, 0x100
	v_mov_b32_e32 v0, 0
	s_addc_u32 s51, s11, 0
	s_mov_b32 s52, -2
	s_cmp_eq_u32 s45, 1
	s_cbranch_scc1 .Lpeel_zero_P8
	v_add_u32_e32 v120, s23, v230
	v_add_u32_e32 v148, s26, v230
	ds_read_b128 v[88:91], v120
	ds_read_b128 v[100:103], v120 offset:1024
	ds_read_b128 v[112:115], v120 offset:2048
	ds_read_b128 v[120:123], v120 offset:3072
	ds_read_b128 v[124:127], v148
	ds_read_b128 v[140:143], v148 offset:1024
	ds_read_b128 v[144:147], v148 offset:2048
	ds_read_b128 v[148:151], v148 offset:3072
	s_add_u32 s10, s8, 0x100
	s_addc_u32 s11, s9, 0
	s_cmpk_eq_i32 s52, 0x54
	s_cselect_b32 s15, s5, s11
	s_cselect_b32 s14, s4, s10
	s_cselect_b32 s13, s7, s51
	s_cselect_b32 s12, s6, s50
	v_lshl_add_u64 v[206:207], s[8:9], 0, v[204:205]
	s_add_i32 m0, s29, 0xc000
	ds_read_b128 v[152:155], v232
	ds_read_b128 v[170:173], v232 offset:1024
	ds_read_b128 v[174:177], v232 offset:2048
	ds_read_b128 v[178:181], v232 offset:3072
	ds_read_b128 v[182:185], v232 offset:4096
	ds_read_b128 v[186:189], v232 offset:5120
	ds_read_b128 v[190:193], v232 offset:6144
	ds_read_b128 v[194:197], v232 offset:7168
	global_load_lds_dwordx4 v[206:207], off
	v_lshl_add_u64 v[206:207], s[8:9], 0, v[202:203]
	s_add_i32 m0, s29, 0xe000
	s_nop 0
	global_load_lds_dwordx4 v[206:207], off
	s_waitcnt vmcnt(40)
	s_waitcnt lgkmcnt(0)
	s_barrier
	s_setprio 1
	s_waitcnt lgkmcnt(0)
	v_mfma_f32_16x16x32_bf16 v[166:169], v[88:91], v[152:155], 0
	v_mfma_f32_16x16x32_bf16 v[156:159], v[112:115], v[152:155], 0
	v_mfma_f32_16x16x32_bf16 v[128:131], v[88:91], v[174:177], 0
	v_mfma_f32_16x16x32_bf16 v[116:119], v[112:115], v[174:177], 0
	v_mfma_f32_16x16x32_bf16 v[96:99], v[88:91], v[182:185], 0
	v_mfma_f32_16x16x32_bf16 v[92:95], v[112:115], v[182:185], 0
	v_mfma_f32_16x16x32_bf16 v[76:79], v[88:91], v[190:193], 0
	v_mfma_f32_16x16x32_bf16 v[72:75], v[112:115], v[190:193], 0
	v_mfma_f32_16x16x32_bf16 v[166:169], v[100:103], v[170:173], v[166:169]
	v_mfma_f32_16x16x32_bf16 v[156:159], v[120:123], v[170:173], v[156:159]
	v_mfma_f32_16x16x32_bf16 v[128:131], v[100:103], v[178:181], v[128:131]
	v_mfma_f32_16x16x32_bf16 v[116:119], v[120:123], v[178:181], v[116:119]
	v_mfma_f32_16x16x32_bf16 v[96:99], v[100:103], v[186:189], v[96:99]
	v_mfma_f32_16x16x32_bf16 v[92:95], v[120:123], v[186:189], v[92:95]
	v_mfma_f32_16x16x32_bf16 v[76:79], v[100:103], v[194:197], v[76:79]
	v_mfma_f32_16x16x32_bf16 v[72:75], v[120:123], v[194:197], v[72:75]
	s_setprio 0
	s_setprio 1
	v_mfma_f32_16x16x32_bf16 v[136:139], v[124:127], v[152:155], 0
	v_mfma_f32_16x16x32_bf16 v[132:135], v[144:147], v[152:155], 0
	v_mfma_f32_16x16x32_bf16 v[108:111], v[124:127], v[174:177], 0
	v_mfma_f32_16x16x32_bf16 v[104:107], v[144:147], v[174:177], 0
	v_mfma_f32_16x16x32_bf16 v[84:87], v[124:127], v[182:185], 0
	v_mfma_f32_16x16x32_bf16 v[80:83], v[144:147], v[182:185], 0
	v_mfma_f32_16x16x32_bf16 v[68:71], v[124:127], v[190:193], 0
	v_mfma_f32_16x16x32_bf16 v[64:67], v[144:147], v[190:193], 0
	v_mfma_f32_16x16x32_bf16 v[136:139], v[140:143], v[170:173], v[136:139]
	v_mfma_f32_16x16x32_bf16 v[132:135], v[148:151], v[170:173], v[132:135]
	v_mfma_f32_16x16x32_bf16 v[108:111], v[140:143], v[178:181], v[108:111]
	v_mfma_f32_16x16x32_bf16 v[104:107], v[148:151], v[178:181], v[104:107]
	v_mfma_f32_16x16x32_bf16 v[84:87], v[140:143], v[186:189], v[84:87]
	v_mfma_f32_16x16x32_bf16 v[80:83], v[148:151], v[186:189], v[80:83]
	v_mfma_f32_16x16x32_bf16 v[68:71], v[140:143], v[194:197], v[68:71]
	v_mfma_f32_16x16x32_bf16 v[64:67], v[148:151], v[194:197], v[64:67]
	s_setprio 0
	s_barrier
	s_mov_b32 m0, s24
	v_lshl_add_u64 v[206:207], s[12:13], 0, v[160:161]
	s_add_u32 s8, s12, 0x160000
	ds_read_b128 v[152:155], v232 offset:16384
	ds_read_b128 v[170:173], v232 offset:17408
	ds_read_b128 v[174:177], v232 offset:18432
	ds_read_b128 v[178:181], v232 offset:19456
	ds_read_b128 v[182:185], v232 offset:20480
	ds_read_b128 v[186:189], v232 offset:21504
	ds_read_b128 v[190:193], v232 offset:22528
	ds_read_b128 v[194:197], v232 offset:23552
	global_load_lds_dwordx4 v[206:207], off
	v_lshl_add_u64 v[208:209], s[12:13], 0, v[200:201]
	s_mov_b32 m0, s25
	s_addc_u32 s9, s13, 0
	global_load_lds_dwordx4 v[208:209], off
	v_lshl_add_u64 v[210:211], s[8:9], 0, v[160:161]
	s_mov_b32 m0, s27
	v_lshl_add_u64 v[212:213], s[14:15], 0, v[198:199]
	global_load_lds_dwordx4 v[210:211], off
	v_lshl_add_u64 v[210:211], s[8:9], 0, v[200:201]
	s_mov_b32 m0, s28
	s_nop 0
	global_load_lds_dwordx4 v[210:211], off
	v_lshl_add_u64 v[210:211], s[14:15], 0, v[162:163]
	s_mov_b32 m0, s29
	s_nop 0
	global_load_lds_dwordx4 v[210:211], off
	s_mov_b32 m0, s30
	s_nop 0
	global_load_lds_dwordx4 v[212:213], off
	s_waitcnt vmcnt(40)
	s_waitcnt lgkmcnt(0)
	s_barrier
	s_setprio 1
	s_waitcnt lgkmcnt(0)
	v_mfma_f32_16x16x32_bf16 v[60:63], v[88:91], v[152:155], 0
	v_mfma_f32_16x16x32_bf16 v[56:59], v[112:115], v[152:155], 0
	v_mfma_f32_16x16x32_bf16 v[44:47], v[88:91], v[174:177], 0
	v_mfma_f32_16x16x32_bf16 v[40:43], v[112:115], v[174:177], 0
	v_mfma_f32_16x16x32_bf16 v[28:31], v[88:91], v[182:185], 0
	v_mfma_f32_16x16x32_bf16 v[24:27], v[112:115], v[182:185], 0
	v_mfma_f32_16x16x32_bf16 v[12:15], v[88:91], v[190:193], 0
	v_mfma_f32_16x16x32_bf16 v[8:11], v[112:115], v[190:193], 0
	v_mfma_f32_16x16x32_bf16 v[60:63], v[100:103], v[170:173], v[60:63]
	v_mfma_f32_16x16x32_bf16 v[56:59], v[120:123], v[170:173], v[56:59]
	v_mfma_f32_16x16x32_bf16 v[44:47], v[100:103], v[178:181], v[44:47]
	v_mfma_f32_16x16x32_bf16 v[40:43], v[120:123], v[178:181], v[40:43]
	v_mfma_f32_16x16x32_bf16 v[28:31], v[100:103], v[186:189], v[28:31]
	v_mfma_f32_16x16x32_bf16 v[24:27], v[120:123], v[186:189], v[24:27]
	v_mfma_f32_16x16x32_bf16 v[12:15], v[100:103], v[194:197], v[12:15]
	v_mfma_f32_16x16x32_bf16 v[8:11], v[120:123], v[194:197], v[8:11]
	s_setprio 0
	s_setprio 1
	v_mfma_f32_16x16x32_bf16 v[52:55], v[124:127], v[152:155], 0
	v_mfma_f32_16x16x32_bf16 v[48:51], v[144:147], v[152:155], 0
	v_mfma_f32_16x16x32_bf16 v[36:39], v[124:127], v[174:177], 0
	v_mfma_f32_16x16x32_bf16 v[32:35], v[144:147], v[174:177], 0
	v_mfma_f32_16x16x32_bf16 v[20:23], v[124:127], v[182:185], 0
	v_mfma_f32_16x16x32_bf16 v[16:19], v[144:147], v[182:185], 0
	v_mfma_f32_16x16x32_bf16 v[4:7], v[124:127], v[190:193], 0
	v_mfma_f32_16x16x32_bf16 v[0:3], v[144:147], v[190:193], 0
	v_mfma_f32_16x16x32_bf16 v[52:55], v[140:143], v[170:173], v[52:55]
	v_mfma_f32_16x16x32_bf16 v[48:51], v[148:151], v[170:173], v[48:51]
	v_mfma_f32_16x16x32_bf16 v[36:39], v[140:143], v[178:181], v[36:39]
	v_mfma_f32_16x16x32_bf16 v[32:35], v[148:151], v[178:181], v[32:35]
	v_mfma_f32_16x16x32_bf16 v[20:23], v[140:143], v[186:189], v[20:23]
	v_mfma_f32_16x16x32_bf16 v[16:19], v[148:151], v[186:189], v[16:19]
	v_mfma_f32_16x16x32_bf16 v[4:7], v[140:143], v[194:197], v[4:7]
	v_mfma_f32_16x16x32_bf16 v[0:3], v[148:151], v[194:197], v[0:3]
	s_setprio 0
	s_barrier
	v_add_u32_e32 v120, s36, v230
	v_add_u32_e32 v148, s41, v230
	ds_read_b128 v[88:91], v120
	ds_read_b128 v[100:103], v120 offset:1024
	ds_read_b128 v[112:115], v120 offset:2048
	ds_read_b128 v[120:123], v120 offset:3072
	ds_read_b128 v[124:127], v148
	ds_read_b128 v[140:143], v148 offset:1024
	ds_read_b128 v[144:147], v148 offset:2048
	ds_read_b128 v[148:151], v148 offset:3072
	s_add_u32 s8, s14, 0x160000
	s_addc_u32 s9, s15, 0
	s_mov_b32 m0, s31
	v_lshl_add_u64 v[214:215], s[8:9], 0, v[162:163]
	ds_read_b128 v[152:155], v232 offset:32768
	ds_read_b128 v[170:173], v232 offset:33792
	ds_read_b128 v[174:177], v232 offset:34816
	ds_read_b128 v[178:181], v232 offset:35840
	ds_read_b128 v[182:185], v232 offset:36864
	ds_read_b128 v[186:189], v232 offset:37888
	ds_read_b128 v[190:193], v232 offset:38912
	ds_read_b128 v[194:197], v232 offset:39936
	global_load_lds_dwordx4 v[214:215], off
	v_lshl_add_u64 v[214:215], s[8:9], 0, v[198:199]
	s_mov_b32 m0, s34
	s_nop 0
	global_load_lds_dwordx4 v[214:215], off
	s_waitcnt vmcnt(8)
	s_waitcnt lgkmcnt(0)
	s_barrier
	s_setprio 1
	s_waitcnt lgkmcnt(0)
	v_mfma_f32_16x16x32_bf16 v[166:169], v[88:91], v[152:155], v[166:169]
	v_mfma_f32_16x16x32_bf16 v[156:159], v[112:115], v[152:155], v[156:159]
	v_mfma_f32_16x16x32_bf16 v[128:131], v[88:91], v[174:177], v[128:131]
	v_mfma_f32_16x16x32_bf16 v[116:119], v[112:115], v[174:177], v[116:119]
	v_mfma_f32_16x16x32_bf16 v[96:99], v[88:91], v[182:185], v[96:99]
	v_mfma_f32_16x16x32_bf16 v[92:95], v[112:115], v[182:185], v[92:95]
	v_mfma_f32_16x16x32_bf16 v[76:79], v[88:91], v[190:193], v[76:79]
	v_mfma_f32_16x16x32_bf16 v[72:75], v[112:115], v[190:193], v[72:75]
	v_mfma_f32_16x16x32_bf16 v[166:169], v[100:103], v[170:173], v[166:169]
	v_mfma_f32_16x16x32_bf16 v[156:159], v[120:123], v[170:173], v[156:159]
	v_mfma_f32_16x16x32_bf16 v[128:131], v[100:103], v[178:181], v[128:131]
	v_mfma_f32_16x16x32_bf16 v[116:119], v[120:123], v[178:181], v[116:119]
	v_mfma_f32_16x16x32_bf16 v[96:99], v[100:103], v[186:189], v[96:99]
	v_mfma_f32_16x16x32_bf16 v[92:95], v[120:123], v[186:189], v[92:95]
	v_mfma_f32_16x16x32_bf16 v[76:79], v[100:103], v[194:197], v[76:79]
	v_mfma_f32_16x16x32_bf16 v[72:75], v[120:123], v[194:197], v[72:75]
	s_setprio 0
	s_setprio 1
	v_mfma_f32_16x16x32_bf16 v[136:139], v[124:127], v[152:155], v[136:139]
	v_mfma_f32_16x16x32_bf16 v[132:135], v[144:147], v[152:155], v[132:135]
	v_mfma_f32_16x16x32_bf16 v[108:111], v[124:127], v[174:177], v[108:111]
	v_mfma_f32_16x16x32_bf16 v[104:107], v[144:147], v[174:177], v[104:107]
	v_mfma_f32_16x16x32_bf16 v[84:87], v[124:127], v[182:185], v[84:87]
	v_mfma_f32_16x16x32_bf16 v[80:83], v[144:147], v[182:185], v[80:83]
	v_mfma_f32_16x16x32_bf16 v[68:71], v[124:127], v[190:193], v[68:71]
	v_mfma_f32_16x16x32_bf16 v[64:67], v[144:147], v[190:193], v[64:67]
	v_mfma_f32_16x16x32_bf16 v[136:139], v[140:143], v[170:173], v[136:139]
	v_mfma_f32_16x16x32_bf16 v[132:135], v[148:151], v[170:173], v[132:135]
	v_mfma_f32_16x16x32_bf16 v[108:111], v[140:143], v[178:181], v[108:111]
	v_mfma_f32_16x16x32_bf16 v[104:107], v[148:151], v[178:181], v[104:107]
	v_mfma_f32_16x16x32_bf16 v[84:87], v[140:143], v[186:189], v[84:87]
	v_mfma_f32_16x16x32_bf16 v[80:83], v[148:151], v[186:189], v[80:83]
	v_mfma_f32_16x16x32_bf16 v[68:71], v[140:143], v[194:197], v[68:71]
	v_mfma_f32_16x16x32_bf16 v[64:67], v[148:151], v[194:197], v[64:67]
	s_setprio 0
	s_barrier
	s_mov_b32 m0, s37
	v_lshl_add_u64 v[206:207], v[206:207], 0, s[86:87]
	s_add_u32 s8, s12, 0x160080
	ds_read_b128 v[152:155], v232 offset:49152
	ds_read_b128 v[170:173], v232 offset:50176
	ds_read_b128 v[174:177], v232 offset:51200
	ds_read_b128 v[178:181], v232 offset:52224
	ds_read_b128 v[182:185], v232 offset:53248
	ds_read_b128 v[186:189], v232 offset:54272
	ds_read_b128 v[190:193], v232 offset:55296
	ds_read_b128 v[194:197], v232 offset:56320
	global_load_lds_dwordx4 v[206:207], off
	v_lshl_add_u64 v[206:207], v[208:209], 0, s[86:87]
	s_mov_b32 m0, s38
	s_addc_u32 s9, s13, 0
	global_load_lds_dwordx4 v[206:207], off
	v_lshl_add_u64 v[206:207], s[8:9], 0, v[160:161]
	s_mov_b32 m0, s42
	s_nop 0
	global_load_lds_dwordx4 v[206:207], off
	v_lshl_add_u64 v[206:207], s[8:9], 0, v[200:201]
	s_mov_b32 m0, s43
	s_nop 0
	global_load_lds_dwordx4 v[206:207], off
	v_lshl_add_u64 v[206:207], v[210:211], 0, s[86:87]
	s_mov_b32 m0, s39
	s_nop 0
	global_load_lds_dwordx4 v[206:207], off
	v_lshl_add_u64 v[206:207], v[212:213], 0, s[86:87]
	s_mov_b32 m0, s40
	s_nop 0
	global_load_lds_dwordx4 v[206:207], off
	s_waitcnt vmcnt(8)
	s_waitcnt lgkmcnt(0)
	s_barrier
	s_setprio 1
	s_waitcnt lgkmcnt(0)
	v_mfma_f32_16x16x32_bf16 v[60:63], v[88:91], v[152:155], v[60:63]
	v_mfma_f32_16x16x32_bf16 v[56:59], v[112:115], v[152:155], v[56:59]
	v_mfma_f32_16x16x32_bf16 v[44:47], v[88:91], v[174:177], v[44:47]
	v_mfma_f32_16x16x32_bf16 v[40:43], v[112:115], v[174:177], v[40:43]
	v_mfma_f32_16x16x32_bf16 v[28:31], v[88:91], v[182:185], v[28:31]
	v_mfma_f32_16x16x32_bf16 v[24:27], v[112:115], v[182:185], v[24:27]
	v_mfma_f32_16x16x32_bf16 v[12:15], v[88:91], v[190:193], v[12:15]
	v_mfma_f32_16x16x32_bf16 v[8:11], v[112:115], v[190:193], v[8:11]
	v_mfma_f32_16x16x32_bf16 v[60:63], v[100:103], v[170:173], v[60:63]
	v_mfma_f32_16x16x32_bf16 v[56:59], v[120:123], v[170:173], v[56:59]
	v_mfma_f32_16x16x32_bf16 v[44:47], v[100:103], v[178:181], v[44:47]
	v_mfma_f32_16x16x32_bf16 v[40:43], v[120:123], v[178:181], v[40:43]
	v_mfma_f32_16x16x32_bf16 v[28:31], v[100:103], v[186:189], v[28:31]
	v_mfma_f32_16x16x32_bf16 v[24:27], v[120:123], v[186:189], v[24:27]
	v_mfma_f32_16x16x32_bf16 v[12:15], v[100:103], v[194:197], v[12:15]
	v_mfma_f32_16x16x32_bf16 v[8:11], v[120:123], v[194:197], v[8:11]
	s_setprio 0
	s_setprio 1
	v_mfma_f32_16x16x32_bf16 v[52:55], v[124:127], v[152:155], v[52:55]
	v_mfma_f32_16x16x32_bf16 v[48:51], v[144:147], v[152:155], v[48:51]
	v_mfma_f32_16x16x32_bf16 v[36:39], v[124:127], v[174:177], v[36:39]
	v_mfma_f32_16x16x32_bf16 v[32:35], v[144:147], v[174:177], v[32:35]
	v_mfma_f32_16x16x32_bf16 v[20:23], v[124:127], v[182:185], v[20:23]
	v_mfma_f32_16x16x32_bf16 v[16:19], v[144:147], v[182:185], v[16:19]
	v_mfma_f32_16x16x32_bf16 v[4:7], v[124:127], v[190:193], v[4:7]
	v_mfma_f32_16x16x32_bf16 v[0:3], v[144:147], v[190:193], v[0:3]
	v_mfma_f32_16x16x32_bf16 v[52:55], v[140:143], v[170:173], v[52:55]
	v_mfma_f32_16x16x32_bf16 v[48:51], v[148:151], v[170:173], v[48:51]
	v_mfma_f32_16x16x32_bf16 v[36:39], v[140:143], v[178:181], v[36:39]
	v_mfma_f32_16x16x32_bf16 v[32:35], v[148:151], v[178:181], v[32:35]
	v_mfma_f32_16x16x32_bf16 v[20:23], v[140:143], v[186:189], v[20:23]
	v_mfma_f32_16x16x32_bf16 v[16:19], v[148:151], v[186:189], v[16:19]
	v_mfma_f32_16x16x32_bf16 v[4:7], v[140:143], v[194:197], v[4:7]
	v_mfma_f32_16x16x32_bf16 v[0:3], v[148:151], v[194:197], v[0:3]
	s_setprio 0
	s_add_i32 s52, s52, 2
	s_add_u32 s50, s50, 0x100
	s_addc_u32 s51, s51, 0
	s_mov_b64 s[8:9], s[10:11]
	s_barrier
	s_branch .LBB0_927

.LBB0_927:
	v_add_u32_e32 v120, s23, v230
	v_add_u32_e32 v148, s26, v230
	ds_read_b128 v[88:91], v120
	ds_read_b128 v[100:103], v120 offset:1024
	ds_read_b128 v[112:115], v120 offset:2048
	ds_read_b128 v[120:123], v120 offset:3072
	ds_read_b128 v[124:127], v148
	ds_read_b128 v[140:143], v148 offset:1024
	ds_read_b128 v[144:147], v148 offset:2048
	ds_read_b128 v[148:151], v148 offset:3072
	s_add_u32 s10, s8, 0x100
	s_addc_u32 s11, s9, 0
	s_cmpk_eq_i32 s52, 0x54
	s_cselect_b32 s15, s5, s11
	s_cselect_b32 s14, s4, s10
	s_cselect_b32 s13, s7, s51
	s_cselect_b32 s12, s6, s50
	v_lshl_add_u64 v[206:207], s[8:9], 0, v[204:205]
	s_add_i32 m0, s29, 0xc000
	ds_read_b128 v[152:155], v232
	ds_read_b128 v[170:173], v232 offset:1024
	ds_read_b128 v[174:177], v232 offset:2048
	ds_read_b128 v[178:181], v232 offset:3072
	ds_read_b128 v[182:185], v232 offset:4096
	ds_read_b128 v[186:189], v232 offset:5120
	ds_read_b128 v[190:193], v232 offset:6144
	ds_read_b128 v[194:197], v232 offset:7168
	global_load_lds_dwordx4 v[206:207], off
	v_lshl_add_u64 v[206:207], s[8:9], 0, v[202:203]
	s_add_i32 m0, s29, 0xe000
	s_nop 0
	global_load_lds_dwordx4 v[206:207], off
	s_waitcnt vmcnt(8)
	s_waitcnt lgkmcnt(0)
	s_barrier
	s_setprio 1
	s_waitcnt lgkmcnt(0)
	v_mfma_f32_16x16x32_bf16 v[166:169], v[88:91], v[152:155], v[166:169]
	v_mfma_f32_16x16x32_bf16 v[156:159], v[112:115], v[152:155], v[156:159]
	v_mfma_f32_16x16x32_bf16 v[128:131], v[88:91], v[174:177], v[128:131]
	v_mfma_f32_16x16x32_bf16 v[116:119], v[112:115], v[174:177], v[116:119]
	v_mfma_f32_16x16x32_bf16 v[96:99], v[88:91], v[182:185], v[96:99]
	v_mfma_f32_16x16x32_bf16 v[92:95], v[112:115], v[182:185], v[92:95]
	v_mfma_f32_16x16x32_bf16 v[76:79], v[88:91], v[190:193], v[76:79]
	v_mfma_f32_16x16x32_bf16 v[72:75], v[112:115], v[190:193], v[72:75]
	v_mfma_f32_16x16x32_bf16 v[166:169], v[100:103], v[170:173], v[166:169]
	v_mfma_f32_16x16x32_bf16 v[156:159], v[120:123], v[170:173], v[156:159]
	v_mfma_f32_16x16x32_bf16 v[128:131], v[100:103], v[178:181], v[128:131]
	v_mfma_f32_16x16x32_bf16 v[116:119], v[120:123], v[178:181], v[116:119]
	v_mfma_f32_16x16x32_bf16 v[96:99], v[100:103], v[186:189], v[96:99]
	v_mfma_f32_16x16x32_bf16 v[92:95], v[120:123], v[186:189], v[92:95]
	v_mfma_f32_16x16x32_bf16 v[76:79], v[100:103], v[194:197], v[76:79]
	v_mfma_f32_16x16x32_bf16 v[72:75], v[120:123], v[194:197], v[72:75]
	s_setprio 0
	s_setprio 1
	v_mfma_f32_16x16x32_bf16 v[136:139], v[124:127], v[152:155], v[136:139]
	v_mfma_f32_16x16x32_bf16 v[132:135], v[144:147], v[152:155], v[132:135]
	v_mfma_f32_16x16x32_bf16 v[108:111], v[124:127], v[174:177], v[108:111]
	v_mfma_f32_16x16x32_bf16 v[104:107], v[144:147], v[174:177], v[104:107]
	v_mfma_f32_16x16x32_bf16 v[84:87], v[124:127], v[182:185], v[84:87]
	v_mfma_f32_16x16x32_bf16 v[80:83], v[144:147], v[182:185], v[80:83]
	v_mfma_f32_16x16x32_bf16 v[68:71], v[124:127], v[190:193], v[68:71]
	v_mfma_f32_16x16x32_bf16 v[64:67], v[144:147], v[190:193], v[64:67]
	v_mfma_f32_16x16x32_bf16 v[136:139], v[140:143], v[170:173], v[136:139]
	v_mfma_f32_16x16x32_bf16 v[132:135], v[148:151], v[170:173], v[132:135]
	v_mfma_f32_16x16x32_bf16 v[108:111], v[140:143], v[178:181], v[108:111]
	v_mfma_f32_16x16x32_bf16 v[104:107], v[148:151], v[178:181], v[104:107]
	v_mfma_f32_16x16x32_bf16 v[84:87], v[140:143], v[186:189], v[84:87]
	v_mfma_f32_16x16x32_bf16 v[80:83], v[148:151], v[186:189], v[80:83]
	v_mfma_f32_16x16x32_bf16 v[68:71], v[140:143], v[194:197], v[68:71]
	v_mfma_f32_16x16x32_bf16 v[64:67], v[148:151], v[194:197], v[64:67]
	s_setprio 0
	s_barrier
	s_mov_b32 m0, s24
	v_lshl_add_u64 v[206:207], s[12:13], 0, v[160:161]
	s_add_u32 s8, s12, 0x160000
	ds_read_b128 v[152:155], v232 offset:16384
	ds_read_b128 v[170:173], v232 offset:17408
	ds_read_b128 v[174:177], v232 offset:18432
	ds_read_b128 v[178:181], v232 offset:19456
	ds_read_b128 v[182:185], v232 offset:20480
	ds_read_b128 v[186:189], v232 offset:21504
	ds_read_b128 v[190:193], v232 offset:22528
	ds_read_b128 v[194:197], v232 offset:23552
	global_load_lds_dwordx4 v[206:207], off
	v_lshl_add_u64 v[208:209], s[12:13], 0, v[200:201]
	s_mov_b32 m0, s25
	s_addc_u32 s9, s13, 0
	global_load_lds_dwordx4 v[208:209], off
	v_lshl_add_u64 v[210:211], s[8:9], 0, v[160:161]
	s_mov_b32 m0, s27
	v_lshl_add_u64 v[212:213], s[14:15], 0, v[198:199]
	global_load_lds_dwordx4 v[210:211], off
	v_lshl_add_u64 v[210:211], s[8:9], 0, v[200:201]
	s_mov_b32 m0, s28
	s_nop 0
	global_load_lds_dwordx4 v[210:211], off
	v_lshl_add_u64 v[210:211], s[14:15], 0, v[162:163]
	s_mov_b32 m0, s29
	s_nop 0
	global_load_lds_dwordx4 v[210:211], off
	s_mov_b32 m0, s30
	s_nop 0
	global_load_lds_dwordx4 v[212:213], off
	s_waitcnt vmcnt(8)
	s_waitcnt lgkmcnt(0)
	s_barrier
	s_setprio 1
	s_waitcnt lgkmcnt(0)
	v_mfma_f32_16x16x32_bf16 v[60:63], v[88:91], v[152:155], v[60:63]
	v_mfma_f32_16x16x32_bf16 v[56:59], v[112:115], v[152:155], v[56:59]
	v_mfma_f32_16x16x32_bf16 v[44:47], v[88:91], v[174:177], v[44:47]
	v_mfma_f32_16x16x32_bf16 v[40:43], v[112:115], v[174:177], v[40:43]
	v_mfma_f32_16x16x32_bf16 v[28:31], v[88:91], v[182:185], v[28:31]
	v_mfma_f32_16x16x32_bf16 v[24:27], v[112:115], v[182:185], v[24:27]
	v_mfma_f32_16x16x32_bf16 v[12:15], v[88:91], v[190:193], v[12:15]
	v_mfma_f32_16x16x32_bf16 v[8:11], v[112:115], v[190:193], v[8:11]
	v_mfma_f32_16x16x32_bf16 v[60:63], v[100:103], v[170:173], v[60:63]
	v_mfma_f32_16x16x32_bf16 v[56:59], v[120:123], v[170:173], v[56:59]
	v_mfma_f32_16x16x32_bf16 v[44:47], v[100:103], v[178:181], v[44:47]
	v_mfma_f32_16x16x32_bf16 v[40:43], v[120:123], v[178:181], v[40:43]
	v_mfma_f32_16x16x32_bf16 v[28:31], v[100:103], v[186:189], v[28:31]
	v_mfma_f32_16x16x32_bf16 v[24:27], v[120:123], v[186:189], v[24:27]
	v_mfma_f32_16x16x32_bf16 v[12:15], v[100:103], v[194:197], v[12:15]
	v_mfma_f32_16x16x32_bf16 v[8:11], v[120:123], v[194:197], v[8:11]
	s_setprio 0
	s_setprio 1
	v_mfma_f32_16x16x32_bf16 v[52:55], v[124:127], v[152:155], v[52:55]
	v_mfma_f32_16x16x32_bf16 v[48:51], v[144:147], v[152:155], v[48:51]
	v_mfma_f32_16x16x32_bf16 v[36:39], v[124:127], v[174:177], v[36:39]
	v_mfma_f32_16x16x32_bf16 v[32:35], v[144:147], v[174:177], v[32:35]
	v_mfma_f32_16x16x32_bf16 v[20:23], v[124:127], v[182:185], v[20:23]
	v_mfma_f32_16x16x32_bf16 v[16:19], v[144:147], v[182:185], v[16:19]
	v_mfma_f32_16x16x32_bf16 v[4:7], v[124:127], v[190:193], v[4:7]
	v_mfma_f32_16x16x32_bf16 v[0:3], v[144:147], v[190:193], v[0:3]
	v_mfma_f32_16x16x32_bf16 v[52:55], v[140:143], v[170:173], v[52:55]
	v_mfma_f32_16x16x32_bf16 v[48:51], v[148:151], v[170:173], v[48:51]
	v_mfma_f32_16x16x32_bf16 v[36:39], v[140:143], v[178:181], v[36:39]
	v_mfma_f32_16x16x32_bf16 v[32:35], v[148:151], v[178:181], v[32:35]
	v_mfma_f32_16x16x32_bf16 v[20:23], v[140:143], v[186:189], v[20:23]
	v_mfma_f32_16x16x32_bf16 v[16:19], v[148:151], v[186:189], v[16:19]
	v_mfma_f32_16x16x32_bf16 v[4:7], v[140:143], v[194:197], v[4:7]
	v_mfma_f32_16x16x32_bf16 v[0:3], v[148:151], v[194:197], v[0:3]
	s_setprio 0
	s_barrier
	v_add_u32_e32 v120, s36, v230
	v_add_u32_e32 v148, s41, v230
	ds_read_b128 v[88:91], v120
	ds_read_b128 v[100:103], v120 offset:1024
	ds_read_b128 v[112:115], v120 offset:2048
	ds_read_b128 v[120:123], v120 offset:3072
	ds_read_b128 v[124:127], v148
	ds_read_b128 v[140:143], v148 offset:1024
	ds_read_b128 v[144:147], v148 offset:2048
	ds_read_b128 v[148:151], v148 offset:3072
	s_add_u32 s8, s14, 0x160000
	s_addc_u32 s9, s15, 0
	s_mov_b32 m0, s31
	v_lshl_add_u64 v[214:215], s[8:9], 0, v[162:163]
	ds_read_b128 v[152:155], v232 offset:32768
	ds_read_b128 v[170:173], v232 offset:33792
	ds_read_b128 v[174:177], v232 offset:34816
	ds_read_b128 v[178:181], v232 offset:35840
	ds_read_b128 v[182:185], v232 offset:36864
	ds_read_b128 v[186:189], v232 offset:37888
	ds_read_b128 v[190:193], v232 offset:38912
	ds_read_b128 v[194:197], v232 offset:39936
	global_load_lds_dwordx4 v[214:215], off
	v_lshl_add_u64 v[214:215], s[8:9], 0, v[198:199]
	s_mov_b32 m0, s34
	s_nop 0
	global_load_lds_dwordx4 v[214:215], off
	s_waitcnt vmcnt(8)
	s_waitcnt lgkmcnt(0)
	s_barrier
	s_setprio 1
	s_waitcnt lgkmcnt(0)
	v_mfma_f32_16x16x32_bf16 v[166:169], v[88:91], v[152:155], v[166:169]
	v_mfma_f32_16x16x32_bf16 v[156:159], v[112:115], v[152:155], v[156:159]
	v_mfma_f32_16x16x32_bf16 v[128:131], v[88:91], v[174:177], v[128:131]
	v_mfma_f32_16x16x32_bf16 v[116:119], v[112:115], v[174:177], v[116:119]
	v_mfma_f32_16x16x32_bf16 v[96:99], v[88:91], v[182:185], v[96:99]
	v_mfma_f32_16x16x32_bf16 v[92:95], v[112:115], v[182:185], v[92:95]
	v_mfma_f32_16x16x32_bf16 v[76:79], v[88:91], v[190:193], v[76:79]
	v_mfma_f32_16x16x32_bf16 v[72:75], v[112:115], v[190:193], v[72:75]
	v_mfma_f32_16x16x32_bf16 v[166:169], v[100:103], v[170:173], v[166:169]
	v_mfma_f32_16x16x32_bf16 v[156:159], v[120:123], v[170:173], v[156:159]
	v_mfma_f32_16x16x32_bf16 v[128:131], v[100:103], v[178:181], v[128:131]
	v_mfma_f32_16x16x32_bf16 v[116:119], v[120:123], v[178:181], v[116:119]
	v_mfma_f32_16x16x32_bf16 v[96:99], v[100:103], v[186:189], v[96:99]
	v_mfma_f32_16x16x32_bf16 v[92:95], v[120:123], v[186:189], v[92:95]
	v_mfma_f32_16x16x32_bf16 v[76:79], v[100:103], v[194:197], v[76:79]
	v_mfma_f32_16x16x32_bf16 v[72:75], v[120:123], v[194:197], v[72:75]
	s_setprio 0
	s_setprio 1
	v_mfma_f32_16x16x32_bf16 v[136:139], v[124:127], v[152:155], v[136:139]
	v_mfma_f32_16x16x32_bf16 v[132:135], v[144:147], v[152:155], v[132:135]
	v_mfma_f32_16x16x32_bf16 v[108:111], v[124:127], v[174:177], v[108:111]
	v_mfma_f32_16x16x32_bf16 v[104:107], v[144:147], v[174:177], v[104:107]
	v_mfma_f32_16x16x32_bf16 v[84:87], v[124:127], v[182:185], v[84:87]
	v_mfma_f32_16x16x32_bf16 v[80:83], v[144:147], v[182:185], v[80:83]
	v_mfma_f32_16x16x32_bf16 v[68:71], v[124:127], v[190:193], v[68:71]
	v_mfma_f32_16x16x32_bf16 v[64:67], v[144:147], v[190:193], v[64:67]
	v_mfma_f32_16x16x32_bf16 v[136:139], v[140:143], v[170:173], v[136:139]
	v_mfma_f32_16x16x32_bf16 v[132:135], v[148:151], v[170:173], v[132:135]
	v_mfma_f32_16x16x32_bf16 v[108:111], v[140:143], v[178:181], v[108:111]
	v_mfma_f32_16x16x32_bf16 v[104:107], v[148:151], v[178:181], v[104:107]
	v_mfma_f32_16x16x32_bf16 v[84:87], v[140:143], v[186:189], v[84:87]
	v_mfma_f32_16x16x32_bf16 v[80:83], v[148:151], v[186:189], v[80:83]
	v_mfma_f32_16x16x32_bf16 v[68:71], v[140:143], v[194:197], v[68:71]
	v_mfma_f32_16x16x32_bf16 v[64:67], v[148:151], v[194:197], v[64:67]
	s_setprio 0
	s_barrier
	s_mov_b32 m0, s37
	v_lshl_add_u64 v[206:207], v[206:207], 0, s[86:87]
	s_add_u32 s8, s12, 0x160080
	ds_read_b128 v[152:155], v232 offset:49152
	ds_read_b128 v[170:173], v232 offset:50176
	ds_read_b128 v[174:177], v232 offset:51200
	ds_read_b128 v[178:181], v232 offset:52224
	ds_read_b128 v[182:185], v232 offset:53248
	ds_read_b128 v[186:189], v232 offset:54272
	ds_read_b128 v[190:193], v232 offset:55296
	ds_read_b128 v[194:197], v232 offset:56320
	global_load_lds_dwordx4 v[206:207], off
	v_lshl_add_u64 v[206:207], v[208:209], 0, s[86:87]
	s_mov_b32 m0, s38
	s_addc_u32 s9, s13, 0
	global_load_lds_dwordx4 v[206:207], off
	v_lshl_add_u64 v[206:207], s[8:9], 0, v[160:161]
	s_mov_b32 m0, s42
	s_nop 0
	global_load_lds_dwordx4 v[206:207], off
	v_lshl_add_u64 v[206:207], s[8:9], 0, v[200:201]
	s_mov_b32 m0, s43
	s_nop 0
	global_load_lds_dwordx4 v[206:207], off
	v_lshl_add_u64 v[206:207], v[210:211], 0, s[86:87]
	s_mov_b32 m0, s39
	s_nop 0
	global_load_lds_dwordx4 v[206:207], off
	v_lshl_add_u64 v[206:207], v[212:213], 0, s[86:87]
	s_mov_b32 m0, s40
	s_nop 0
	global_load_lds_dwordx4 v[206:207], off
	s_waitcnt vmcnt(8)
	s_waitcnt lgkmcnt(0)
	s_barrier
	s_setprio 1
	s_waitcnt lgkmcnt(0)
	v_mfma_f32_16x16x32_bf16 v[60:63], v[88:91], v[152:155], v[60:63]
	v_mfma_f32_16x16x32_bf16 v[56:59], v[112:115], v[152:155], v[56:59]
	v_mfma_f32_16x16x32_bf16 v[44:47], v[88:91], v[174:177], v[44:47]
	v_mfma_f32_16x16x32_bf16 v[40:43], v[112:115], v[174:177], v[40:43]
	v_mfma_f32_16x16x32_bf16 v[28:31], v[88:91], v[182:185], v[28:31]
	v_mfma_f32_16x16x32_bf16 v[24:27], v[112:115], v[182:185], v[24:27]
	v_mfma_f32_16x16x32_bf16 v[12:15], v[88:91], v[190:193], v[12:15]
	v_mfma_f32_16x16x32_bf16 v[8:11], v[112:115], v[190:193], v[8:11]
	v_mfma_f32_16x16x32_bf16 v[60:63], v[100:103], v[170:173], v[60:63]
	v_mfma_f32_16x16x32_bf16 v[56:59], v[120:123], v[170:173], v[56:59]
	v_mfma_f32_16x16x32_bf16 v[44:47], v[100:103], v[178:181], v[44:47]
	v_mfma_f32_16x16x32_bf16 v[40:43], v[120:123], v[178:181], v[40:43]
	v_mfma_f32_16x16x32_bf16 v[28:31], v[100:103], v[186:189], v[28:31]
	v_mfma_f32_16x16x32_bf16 v[24:27], v[120:123], v[186:189], v[24:27]
	v_mfma_f32_16x16x32_bf16 v[12:15], v[100:103], v[194:197], v[12:15]
	v_mfma_f32_16x16x32_bf16 v[8:11], v[120:123], v[194:197], v[8:11]
	s_setprio 0
	s_setprio 1
	v_mfma_f32_16x16x32_bf16 v[52:55], v[124:127], v[152:155], v[52:55]
	v_mfma_f32_16x16x32_bf16 v[48:51], v[144:147], v[152:155], v[48:51]
	v_mfma_f32_16x16x32_bf16 v[36:39], v[124:127], v[174:177], v[36:39]
	v_mfma_f32_16x16x32_bf16 v[32:35], v[144:147], v[174:177], v[32:35]
	v_mfma_f32_16x16x32_bf16 v[20:23], v[124:127], v[182:185], v[20:23]
	v_mfma_f32_16x16x32_bf16 v[16:19], v[144:147], v[182:185], v[16:19]
	v_mfma_f32_16x16x32_bf16 v[4:7], v[124:127], v[190:193], v[4:7]
	v_mfma_f32_16x16x32_bf16 v[0:3], v[144:147], v[190:193], v[0:3]
	v_mfma_f32_16x16x32_bf16 v[52:55], v[140:143], v[170:173], v[52:55]
	v_mfma_f32_16x16x32_bf16 v[48:51], v[148:151], v[170:173], v[48:51]
	v_mfma_f32_16x16x32_bf16 v[36:39], v[140:143], v[178:181], v[36:39]
	v_mfma_f32_16x16x32_bf16 v[32:35], v[148:151], v[178:181], v[32:35]
	v_mfma_f32_16x16x32_bf16 v[20:23], v[140:143], v[186:189], v[20:23]
	v_mfma_f32_16x16x32_bf16 v[16:19], v[148:151], v[186:189], v[16:19]
	v_mfma_f32_16x16x32_bf16 v[4:7], v[140:143], v[194:197], v[4:7]
	v_mfma_f32_16x16x32_bf16 v[0:3], v[148:151], v[194:197], v[0:3]
	s_setprio 0
	s_add_i32 s52, s52, 2
	s_add_u32 s50, s50, 0x100
	s_addc_u32 s51, s51, 0
	s_cmpk_gt_u32 s52, 0x55
	s_mov_b64 s[8:9], s[10:11]
	s_barrier
	s_cbranch_scc0 .LBB0_927
	v_lshl_or_b32 v90, s49, 8, v231
	v_lshl_add_u32 v88, s48, 8, v165
	v_ashrrev_i32_e32 v91, 31, v90
	v_lshlrev_b64 v[206:207], 1, v[90:91]
	v_ashrrev_i32_e32 v89, 31, v88
	v_lshl_add_u64 v[90:91], s[0:1], 0, v[206:207]
	v_lshlrev_b64 v[222:223], 12, v[88:89]
	v_lshl_add_u64 v[100:101], v[90:91], 0, v[222:223]
	global_load_dwordx4 v[194:197], v[100:101], off nt
	global_load_dwordx4 v[190:193], v[100:101], off offset:256 nt
	v_or_b32_e32 v100, 16, v88
	v_ashrrev_i32_e32 v101, 31, v100
	v_lshlrev_b64 v[220:221], 12, v[100:101]
	v_lshl_add_u64 v[100:101], v[90:91], 0, v[220:221]
	global_load_dwordx4 v[186:189], v[100:101], off nt
	global_load_dwordx4 v[182:185], v[100:101], off offset:256 nt
	v_or_b32_e32 v100, 32, v88
	v_ashrrev_i32_e32 v101, 31, v100
	v_lshlrev_b64 v[218:219], 12, v[100:101]
	v_lshl_add_u64 v[100:101], v[90:91], 0, v[218:219]
	global_load_dwordx4 v[178:181], v[100:101], off nt
	global_load_dwordx4 v[174:177], v[100:101], off offset:256 nt
	v_or_b32_e32 v88, 48, v88
	v_ashrrev_i32_e32 v89, 31, v88
	v_lshlrev_b64 v[216:217], 12, v[88:89]
	v_lshl_add_u64 v[88:89], v[90:91], 0, v[216:217]
	global_load_dwordx4 v[170:173], v[88:89], off nt
	global_load_dwordx4 v[152:155], v[88:89], off offset:256 nt
	v_lshl_add_u64 v[214:215], v[222:223], 0, s[54:55]
	v_lshl_add_u64 v[88:89], v[90:91], 0, v[214:215]
	global_load_dwordx4 v[148:151], v[88:89], off nt
	global_load_dwordx4 v[144:147], v[88:89], off offset:256 nt
	s_mov_b64 s[8:9], 0x90000
	v_lshl_add_u64 v[212:213], v[222:223], 0, s[8:9]
	v_lshl_add_u64 v[88:89], v[90:91], 0, v[212:213]
	global_load_dwordx4 v[140:143], v[88:89], off nt
	global_load_dwordx4 v[124:127], v[88:89], off offset:256 nt
	s_mov_b64 s[8:9], 0xa0000
	v_lshl_add_u64 v[210:211], v[222:223], 0, s[8:9]
	v_lshl_add_u64 v[88:89], v[90:91], 0, v[210:211]
	global_load_dwordx4 v[120:123], v[88:89], off nt
	global_load_dwordx4 v[112:115], v[88:89], off offset:256 nt
	s_mov_b64 s[8:9], 0xb0000
	v_lshl_add_u64 v[208:209], v[222:223], 0, s[8:9]
	v_lshl_add_u64 v[88:89], v[90:91], 0, v[208:209]
	global_load_dwordx4 v[100:103], v[88:89], off nt
	s_nop 0
	global_load_dwordx4 v[88:91], v[88:89], off offset:256 nt
	s_and_b64 vcc, exec, s[2:3]
	s_mov_b32 s49, s46
	s_mov_b32 s48, s47
	s_mov_b64 s[10:11], s[6:7]
	s_mov_b64 s[8:9], s[4:5]
	s_waitcnt vmcnt(0)
	v_cvt_f32_f16_e32 v224, v194
	v_cvt_f32_f16_sdwa v225, v194 dst_sel:DWORD dst_unused:UNUSED_PAD src0_sel:WORD_1
	v_pk_add_f32 v[166:167], v[166:167], v[224:225]
	s_nop 0
	v_cvt_pk_f16_f32 v194, v166, v167
	v_cvt_f32_f16_e32 v166, v196
	v_cvt_f32_f16_sdwa v167, v196 dst_sel:DWORD dst_unused:UNUSED_PAD src0_sel:WORD_1
	v_pk_add_f32 v[156:157], v[156:157], v[166:167]
	s_nop 0
	v_cvt_pk_f16_f32 v196, v156, v157
	v_cvt_f32_f16_e32 v156, v195
	v_cvt_f32_f16_sdwa v157, v195 dst_sel:DWORD dst_unused:UNUSED_PAD src0_sel:WORD_1
	v_pk_add_f32 v[156:157], v[168:169], v[156:157]
	s_nop 0
	v_cvt_pk_f16_f32 v195, v156, v157
	v_cvt_f32_f16_e32 v156, v197
	v_cvt_f32_f16_sdwa v157, v197 dst_sel:DWORD dst_unused:UNUSED_PAD src0_sel:WORD_1
	v_pk_add_f32 v[156:157], v[158:159], v[156:157]
	s_nop 0
	v_cvt_pk_f16_f32 v197, v156, v157
	v_lshl_add_u64 v[156:157], s[0:1], 0, v[222:223]
	v_lshl_add_u64 v[166:167], v[156:157], 0, v[206:207]
	v_cvt_f32_f16_e32 v156, v190
	v_cvt_f32_f16_sdwa v157, v190 dst_sel:DWORD dst_unused:UNUSED_PAD src0_sel:WORD_1
	global_store_dwordx4 v[166:167], v[194:197], off
	v_pk_add_f32 v[136:137], v[136:137], v[156:157]
	s_nop 0
	v_cvt_pk_f16_f32 v156, v136, v137
	v_cvt_f32_f16_e32 v136, v192
	v_cvt_f32_f16_sdwa v137, v192 dst_sel:DWORD dst_unused:UNUSED_PAD src0_sel:WORD_1
	v_pk_add_f32 v[132:133], v[132:133], v[136:137]
	s_nop 0
	v_cvt_pk_f16_f32 v158, v132, v133
	v_cvt_f32_f16_e32 v132, v191
	v_cvt_f32_f16_sdwa v133, v191 dst_sel:DWORD dst_unused:UNUSED_PAD src0_sel:WORD_1
	v_pk_add_f32 v[132:133], v[138:139], v[132:133]
	s_nop 0
	v_cvt_pk_f16_f32 v157, v132, v133
	v_cvt_f32_f16_e32 v132, v193
	v_cvt_f32_f16_sdwa v133, v193 dst_sel:DWORD dst_unused:UNUSED_PAD src0_sel:WORD_1
	v_pk_add_f32 v[132:133], v[134:135], v[132:133]
	s_nop 0
	v_cvt_pk_f16_f32 v159, v132, v133
	v_cvt_f32_f16_e32 v132, v186
	v_cvt_f32_f16_sdwa v133, v186 dst_sel:DWORD dst_unused:UNUSED_PAD src0_sel:WORD_1
	global_store_dwordx4 v[166:167], v[156:159], off offset:256
	v_pk_add_f32 v[128:129], v[128:129], v[132:133]
	s_nop 0
	v_cvt_pk_f16_f32 v132, v128, v129
	v_cvt_f32_f16_e32 v128, v188
	v_cvt_f32_f16_sdwa v129, v188 dst_sel:DWORD dst_unused:UNUSED_PAD src0_sel:WORD_1
	v_pk_add_f32 v[116:117], v[116:117], v[128:129]
	s_nop 0
	v_cvt_pk_f16_f32 v134, v116, v117
	v_cvt_f32_f16_e32 v116, v187
	v_cvt_f32_f16_sdwa v117, v187 dst_sel:DWORD dst_unused:UNUSED_PAD src0_sel:WORD_1
	v_pk_add_f32 v[116:117], v[130:131], v[116:117]
	s_nop 0
	v_cvt_pk_f16_f32 v133, v116, v117
	v_cvt_f32_f16_e32 v116, v189
	v_cvt_f32_f16_sdwa v117, v189 dst_sel:DWORD dst_unused:UNUSED_PAD src0_sel:WORD_1
	v_pk_add_f32 v[116:117], v[118:119], v[116:117]
	s_nop 0
	v_cvt_pk_f16_f32 v135, v116, v117
	v_lshl_add_u64 v[116:117], s[0:1], 0, v[220:221]
	v_lshl_add_u64 v[128:129], v[116:117], 0, v[206:207]
	v_cvt_f32_f16_e32 v116, v182
	v_cvt_f32_f16_sdwa v117, v182 dst_sel:DWORD dst_unused:UNUSED_PAD src0_sel:WORD_1
	global_store_dwordx4 v[128:129], v[132:135], off
	v_pk_add_f32 v[108:109], v[108:109], v[116:117]
	s_nop 0
	v_cvt_pk_f16_f32 v116, v108, v109
	v_cvt_f32_f16_e32 v108, v184
	v_cvt_f32_f16_sdwa v109, v184 dst_sel:DWORD dst_unused:UNUSED_PAD src0_sel:WORD_1
	v_pk_add_f32 v[104:105], v[104:105], v[108:109]
	s_nop 0
	v_cvt_pk_f16_f32 v118, v104, v105
	v_cvt_f32_f16_e32 v104, v183
	v_cvt_f32_f16_sdwa v105, v183 dst_sel:DWORD dst_unused:UNUSED_PAD src0_sel:WORD_1
	v_pk_add_f32 v[104:105], v[110:111], v[104:105]
	s_nop 0
	v_cvt_pk_f16_f32 v117, v104, v105
	v_cvt_f32_f16_e32 v104, v185
	v_cvt_f32_f16_sdwa v105, v185 dst_sel:DWORD dst_unused:UNUSED_PAD src0_sel:WORD_1
	v_pk_add_f32 v[104:105], v[106:107], v[104:105]
	s_nop 0
	v_cvt_pk_f16_f32 v119, v104, v105
	v_cvt_f32_f16_e32 v104, v178
	v_cvt_f32_f16_sdwa v105, v178 dst_sel:DWORD dst_unused:UNUSED_PAD src0_sel:WORD_1
	global_store_dwordx4 v[128:129], v[116:119], off offset:256
	v_pk_add_f32 v[96:97], v[96:97], v[104:105]
	s_nop 0
	v_cvt_pk_f16_f32 v104, v96, v97
	v_cvt_f32_f16_e32 v96, v180
	v_cvt_f32_f16_sdwa v97, v180 dst_sel:DWORD dst_unused:UNUSED_PAD src0_sel:WORD_1
	v_pk_add_f32 v[92:93], v[92:93], v[96:97]
	s_nop 0
	v_cvt_pk_f16_f32 v106, v92, v93
	v_cvt_f32_f16_e32 v92, v179
	v_cvt_f32_f16_sdwa v93, v179 dst_sel:DWORD dst_unused:UNUSED_PAD src0_sel:WORD_1
	v_pk_add_f32 v[92:93], v[98:99], v[92:93]
	s_nop 0
	v_cvt_pk_f16_f32 v105, v92, v93
	v_cvt_f32_f16_e32 v92, v181
	v_cvt_f32_f16_sdwa v93, v181 dst_sel:DWORD dst_unused:UNUSED_PAD src0_sel:WORD_1
	v_pk_add_f32 v[92:93], v[94:95], v[92:93]
	s_nop 0
	v_cvt_pk_f16_f32 v107, v92, v93
	v_lshl_add_u64 v[92:93], s[0:1], 0, v[218:219]
	v_lshl_add_u64 v[96:97], v[92:93], 0, v[206:207]
	v_cvt_f32_f16_e32 v92, v174
	v_cvt_f32_f16_sdwa v93, v174 dst_sel:DWORD dst_unused:UNUSED_PAD src0_sel:WORD_1
	global_store_dwordx4 v[96:97], v[104:107], off
	v_pk_add_f32 v[84:85], v[84:85], v[92:93]
	s_nop 0
	v_cvt_pk_f16_f32 v92, v84, v85
	v_cvt_f32_f16_e32 v84, v176
	v_cvt_f32_f16_sdwa v85, v176 dst_sel:DWORD dst_unused:UNUSED_PAD src0_sel:WORD_1
	v_pk_add_f32 v[80:81], v[80:81], v[84:85]
	s_nop 0
	v_cvt_pk_f16_f32 v94, v80, v81
	v_cvt_f32_f16_e32 v80, v175
	v_cvt_f32_f16_sdwa v81, v175 dst_sel:DWORD dst_unused:UNUSED_PAD src0_sel:WORD_1
	v_pk_add_f32 v[80:81], v[86:87], v[80:81]
	s_nop 0
	v_cvt_pk_f16_f32 v93, v80, v81
	v_cvt_f32_f16_e32 v80, v177
	v_cvt_f32_f16_sdwa v81, v177 dst_sel:DWORD dst_unused:UNUSED_PAD src0_sel:WORD_1
	v_pk_add_f32 v[80:81], v[82:83], v[80:81]
	s_nop 0
	v_cvt_pk_f16_f32 v95, v80, v81
	v_cvt_f32_f16_e32 v80, v170
	v_cvt_f32_f16_sdwa v81, v170 dst_sel:DWORD dst_unused:UNUSED_PAD src0_sel:WORD_1
	global_store_dwordx4 v[96:97], v[92:95], off offset:256
	v_pk_add_f32 v[76:77], v[76:77], v[80:81]
	s_nop 0
	v_cvt_pk_f16_f32 v80, v76, v77
	v_cvt_f32_f16_e32 v76, v172
	v_cvt_f32_f16_sdwa v77, v172 dst_sel:DWORD dst_unused:UNUSED_PAD src0_sel:WORD_1
	v_pk_add_f32 v[72:73], v[72:73], v[76:77]
	s_nop 0
	v_cvt_pk_f16_f32 v82, v72, v73
	v_cvt_f32_f16_e32 v72, v171
	v_cvt_f32_f16_sdwa v73, v171 dst_sel:DWORD dst_unused:UNUSED_PAD src0_sel:WORD_1
	v_pk_add_f32 v[72:73], v[78:79], v[72:73]
	s_nop 0
	v_cvt_pk_f16_f32 v81, v72, v73
	v_cvt_f32_f16_e32 v72, v173
	v_cvt_f32_f16_sdwa v73, v173 dst_sel:DWORD dst_unused:UNUSED_PAD src0_sel:WORD_1
	v_pk_add_f32 v[72:73], v[74:75], v[72:73]
	s_nop 0
	v_cvt_pk_f16_f32 v83, v72, v73
	v_lshl_add_u64 v[72:73], s[0:1], 0, v[216:217]
	v_lshl_add_u64 v[76:77], v[72:73], 0, v[206:207]
	v_cvt_f32_f16_e32 v72, v152
	v_cvt_f32_f16_sdwa v73, v152 dst_sel:DWORD dst_unused:UNUSED_PAD src0_sel:WORD_1
	global_store_dwordx4 v[76:77], v[80:83], off
	v_pk_add_f32 v[68:69], v[68:69], v[72:73]
	s_nop 0
	v_cvt_pk_f16_f32 v72, v68, v69
	v_cvt_f32_f16_e32 v68, v154
	v_cvt_f32_f16_sdwa v69, v154 dst_sel:DWORD dst_unused:UNUSED_PAD src0_sel:WORD_1
	v_pk_add_f32 v[64:65], v[64:65], v[68:69]
	s_nop 0
	v_cvt_pk_f16_f32 v74, v64, v65
	v_cvt_f32_f16_e32 v64, v153
	v_cvt_f32_f16_sdwa v65, v153 dst_sel:DWORD dst_unused:UNUSED_PAD src0_sel:WORD_1
	v_pk_add_f32 v[64:65], v[70:71], v[64:65]
	s_nop 0
	v_cvt_pk_f16_f32 v73, v64, v65
	v_cvt_f32_f16_e32 v64, v155
	v_cvt_f32_f16_sdwa v65, v155 dst_sel:DWORD dst_unused:UNUSED_PAD src0_sel:WORD_1
	v_pk_add_f32 v[64:65], v[66:67], v[64:65]
	s_nop 0
	v_cvt_pk_f16_f32 v75, v64, v65
	v_cvt_f32_f16_e32 v64, v148
	v_cvt_f32_f16_sdwa v65, v148 dst_sel:DWORD dst_unused:UNUSED_PAD src0_sel:WORD_1
	global_store_dwordx4 v[76:77], v[72:75], off offset:256
	v_pk_add_f32 v[60:61], v[60:61], v[64:65]
	s_nop 0
	v_cvt_pk_f16_f32 v64, v60, v61
	v_cvt_f32_f16_e32 v60, v150
	v_cvt_f32_f16_sdwa v61, v150 dst_sel:DWORD dst_unused:UNUSED_PAD src0_sel:WORD_1
	v_pk_add_f32 v[56:57], v[56:57], v[60:61]
	s_nop 0
	v_cvt_pk_f16_f32 v66, v56, v57
	v_cvt_f32_f16_e32 v56, v149
	v_cvt_f32_f16_sdwa v57, v149 dst_sel:DWORD dst_unused:UNUSED_PAD src0_sel:WORD_1
	v_pk_add_f32 v[56:57], v[62:63], v[56:57]
	s_nop 0
	v_cvt_pk_f16_f32 v65, v56, v57
	v_cvt_f32_f16_e32 v56, v151
	v_cvt_f32_f16_sdwa v57, v151 dst_sel:DWORD dst_unused:UNUSED_PAD src0_sel:WORD_1
	v_pk_add_f32 v[56:57], v[58:59], v[56:57]
	s_nop 0
	v_cvt_pk_f16_f32 v67, v56, v57
	v_lshl_add_u64 v[56:57], s[0:1], 0, v[214:215]
	v_lshl_add_u64 v[60:61], v[56:57], 0, v[206:207]
	v_cvt_f32_f16_e32 v56, v144
	v_cvt_f32_f16_sdwa v57, v144 dst_sel:DWORD dst_unused:UNUSED_PAD src0_sel:WORD_1
	global_store_dwordx4 v[60:61], v[64:67], off
	v_pk_add_f32 v[52:53], v[52:53], v[56:57]
	s_nop 0
	v_cvt_pk_f16_f32 v56, v52, v53
	v_cvt_f32_f16_e32 v52, v146
	v_cvt_f32_f16_sdwa v53, v146 dst_sel:DWORD dst_unused:UNUSED_PAD src0_sel:WORD_1
	v_pk_add_f32 v[48:49], v[48:49], v[52:53]
	s_nop 0
	v_cvt_pk_f16_f32 v58, v48, v49
	v_cvt_f32_f16_e32 v48, v145
	v_cvt_f32_f16_sdwa v49, v145 dst_sel:DWORD dst_unused:UNUSED_PAD src0_sel:WORD_1
	v_pk_add_f32 v[48:49], v[54:55], v[48:49]
	s_nop 0
	v_cvt_pk_f16_f32 v57, v48, v49
	v_cvt_f32_f16_e32 v48, v147
	v_cvt_f32_f16_sdwa v49, v147 dst_sel:DWORD dst_unused:UNUSED_PAD src0_sel:WORD_1
	v_pk_add_f32 v[48:49], v[50:51], v[48:49]
	s_nop 0
	v_cvt_pk_f16_f32 v59, v48, v49
	v_cvt_f32_f16_e32 v48, v140
	v_cvt_f32_f16_sdwa v49, v140 dst_sel:DWORD dst_unused:UNUSED_PAD src0_sel:WORD_1
	global_store_dwordx4 v[60:61], v[56:59], off offset:256
	v_pk_add_f32 v[44:45], v[44:45], v[48:49]
	s_nop 0
	v_cvt_pk_f16_f32 v48, v44, v45
	v_cvt_f32_f16_e32 v44, v142
	v_cvt_f32_f16_sdwa v45, v142 dst_sel:DWORD dst_unused:UNUSED_PAD src0_sel:WORD_1
	v_pk_add_f32 v[40:41], v[40:41], v[44:45]
	s_nop 0
	v_cvt_pk_f16_f32 v50, v40, v41
	v_cvt_f32_f16_e32 v40, v141
	v_cvt_f32_f16_sdwa v41, v141 dst_sel:DWORD dst_unused:UNUSED_PAD src0_sel:WORD_1
	v_pk_add_f32 v[40:41], v[46:47], v[40:41]
	s_nop 0
	v_cvt_pk_f16_f32 v49, v40, v41
	v_cvt_f32_f16_e32 v40, v143
	v_cvt_f32_f16_sdwa v41, v143 dst_sel:DWORD dst_unused:UNUSED_PAD src0_sel:WORD_1
	v_pk_add_f32 v[40:41], v[42:43], v[40:41]
	s_nop 0
	v_cvt_pk_f16_f32 v51, v40, v41
	v_lshl_add_u64 v[40:41], s[0:1], 0, v[212:213]
	v_lshl_add_u64 v[44:45], v[40:41], 0, v[206:207]
	v_cvt_f32_f16_e32 v40, v124
	v_cvt_f32_f16_sdwa v41, v124 dst_sel:DWORD dst_unused:UNUSED_PAD src0_sel:WORD_1
	global_store_dwordx4 v[44:45], v[48:51], off
	v_pk_add_f32 v[36:37], v[36:37], v[40:41]
	s_nop 0
	v_cvt_pk_f16_f32 v40, v36, v37
	v_cvt_f32_f16_e32 v36, v126
	v_cvt_f32_f16_sdwa v37, v126 dst_sel:DWORD dst_unused:UNUSED_PAD src0_sel:WORD_1
	v_pk_add_f32 v[32:33], v[32:33], v[36:37]
	s_nop 0
	v_cvt_pk_f16_f32 v42, v32, v33
	v_cvt_f32_f16_e32 v32, v125
	v_cvt_f32_f16_sdwa v33, v125 dst_sel:DWORD dst_unused:UNUSED_PAD src0_sel:WORD_1
	v_pk_add_f32 v[32:33], v[38:39], v[32:33]
	s_nop 0
	v_cvt_pk_f16_f32 v41, v32, v33
	v_cvt_f32_f16_e32 v32, v127
	v_cvt_f32_f16_sdwa v33, v127 dst_sel:DWORD dst_unused:UNUSED_PAD src0_sel:WORD_1
	v_pk_add_f32 v[32:33], v[34:35], v[32:33]
	s_nop 0
	v_cvt_pk_f16_f32 v43, v32, v33
	v_cvt_f32_f16_e32 v32, v120
	v_cvt_f32_f16_sdwa v33, v120 dst_sel:DWORD dst_unused:UNUSED_PAD src0_sel:WORD_1
	global_store_dwordx4 v[44:45], v[40:43], off offset:256
	v_pk_add_f32 v[28:29], v[28:29], v[32:33]
	s_nop 0
	v_cvt_pk_f16_f32 v32, v28, v29
	v_cvt_f32_f16_e32 v28, v122
	v_cvt_f32_f16_sdwa v29, v122 dst_sel:DWORD dst_unused:UNUSED_PAD src0_sel:WORD_1
	v_pk_add_f32 v[24:25], v[24:25], v[28:29]
	s_nop 0
	v_cvt_pk_f16_f32 v34, v24, v25
	v_cvt_f32_f16_e32 v24, v121
	v_cvt_f32_f16_sdwa v25, v121 dst_sel:DWORD dst_unused:UNUSED_PAD src0_sel:WORD_1
	v_pk_add_f32 v[24:25], v[30:31], v[24:25]
	s_nop 0
	v_cvt_pk_f16_f32 v33, v24, v25
	v_cvt_f32_f16_e32 v24, v123
	v_cvt_f32_f16_sdwa v25, v123 dst_sel:DWORD dst_unused:UNUSED_PAD src0_sel:WORD_1
	v_pk_add_f32 v[24:25], v[26:27], v[24:25]
	s_nop 0
	v_cvt_pk_f16_f32 v35, v24, v25
	v_lshl_add_u64 v[24:25], s[0:1], 0, v[210:211]
	v_lshl_add_u64 v[28:29], v[24:25], 0, v[206:207]
	v_cvt_f32_f16_e32 v24, v112
	v_cvt_f32_f16_sdwa v25, v112 dst_sel:DWORD dst_unused:UNUSED_PAD src0_sel:WORD_1
	global_store_dwordx4 v[28:29], v[32:35], off
	v_pk_add_f32 v[20:21], v[20:21], v[24:25]
	s_nop 0
	v_cvt_pk_f16_f32 v24, v20, v21
	v_cvt_f32_f16_e32 v20, v114
	v_cvt_f32_f16_sdwa v21, v114 dst_sel:DWORD dst_unused:UNUSED_PAD src0_sel:WORD_1
	v_pk_add_f32 v[16:17], v[16:17], v[20:21]
	s_nop 0
	v_cvt_pk_f16_f32 v26, v16, v17
	v_cvt_f32_f16_e32 v16, v113
	v_cvt_f32_f16_sdwa v17, v113 dst_sel:DWORD dst_unused:UNUSED_PAD src0_sel:WORD_1
	v_pk_add_f32 v[16:17], v[22:23], v[16:17]
	s_nop 0
	v_cvt_pk_f16_f32 v25, v16, v17
	v_cvt_f32_f16_e32 v16, v115
	v_cvt_f32_f16_sdwa v17, v115 dst_sel:DWORD dst_unused:UNUSED_PAD src0_sel:WORD_1
	v_pk_add_f32 v[16:17], v[18:19], v[16:17]
	s_nop 0
	v_cvt_pk_f16_f32 v27, v16, v17
	v_cvt_f32_f16_e32 v16, v100
	v_cvt_f32_f16_sdwa v17, v100 dst_sel:DWORD dst_unused:UNUSED_PAD src0_sel:WORD_1
	global_store_dwordx4 v[28:29], v[24:27], off offset:256
	v_pk_add_f32 v[12:13], v[12:13], v[16:17]
	s_nop 0
	v_cvt_pk_f16_f32 v16, v12, v13
	v_cvt_f32_f16_e32 v12, v102
	v_cvt_f32_f16_sdwa v13, v102 dst_sel:DWORD dst_unused:UNUSED_PAD src0_sel:WORD_1
	v_pk_add_f32 v[8:9], v[8:9], v[12:13]
	s_nop 0
	v_cvt_pk_f16_f32 v18, v8, v9
	v_cvt_f32_f16_e32 v8, v101
	v_cvt_f32_f16_sdwa v9, v101 dst_sel:DWORD dst_unused:UNUSED_PAD src0_sel:WORD_1
	v_pk_add_f32 v[8:9], v[14:15], v[8:9]
	s_nop 0
	v_cvt_pk_f16_f32 v17, v8, v9
	v_cvt_f32_f16_e32 v8, v103
	v_cvt_f32_f16_sdwa v9, v103 dst_sel:DWORD dst_unused:UNUSED_PAD src0_sel:WORD_1
	v_pk_add_f32 v[8:9], v[10:11], v[8:9]
	s_nop 0
	v_cvt_pk_f16_f32 v19, v8, v9
	v_lshl_add_u64 v[8:9], s[0:1], 0, v[208:209]
	v_lshl_add_u64 v[12:13], v[8:9], 0, v[206:207]
	v_cvt_f32_f16_e32 v8, v88
	v_cvt_f32_f16_sdwa v9, v88 dst_sel:DWORD dst_unused:UNUSED_PAD src0_sel:WORD_1
	global_store_dwordx4 v[12:13], v[16:19], off
	v_pk_add_f32 v[4:5], v[4:5], v[8:9]
	s_nop 0
	v_cvt_pk_f16_f32 v8, v4, v5
	v_cvt_f32_f16_e32 v4, v90
	v_cvt_f32_f16_sdwa v5, v90 dst_sel:DWORD dst_unused:UNUSED_PAD src0_sel:WORD_1
	v_pk_add_f32 v[0:1], v[0:1], v[4:5]
	s_nop 0
	v_cvt_pk_f16_f32 v10, v0, v1
	v_cvt_f32_f16_e32 v0, v89
	v_cvt_f32_f16_sdwa v1, v89 dst_sel:DWORD dst_unused:UNUSED_PAD src0_sel:WORD_1
	v_pk_add_f32 v[0:1], v[6:7], v[0:1]
	s_nop 0
	v_cvt_pk_f16_f32 v9, v0, v1
	v_cvt_f32_f16_e32 v0, v91
	v_cvt_f32_f16_sdwa v1, v91 dst_sel:DWORD dst_unused:UNUSED_PAD src0_sel:WORD_1
	v_pk_add_f32 v[0:1], v[2:3], v[0:1]
	s_nop 0
	v_cvt_pk_f16_f32 v11, v0, v1
	global_store_dwordx4 v[12:13], v[8:11], off offset:256
	s_cbranch_vccz .LBB0_916
	s_waitcnt vmcnt(0)
	s_cmpk_gt_u32 s17, 0xff
	s_cbranch_scc1 .LBB0_931
	s_barrier
